# qkv epilogue head-norm / k-block-mean lane reductions and the P0 calibration wave_sum: ds_bpermute xor steps replaced by DPP / permlane swaps, redundant lgkm waits dropped
# baseline (speedup 1.0000x reference)
.LBB0_50:
	v_mul_lo_u32 v35, s13, v2
	v_mul_lo_u32 v38, s12, v1
	v_mad_u64_u32 v[36:37], s[14:15], s12, v2, 0
	v_add3_u32 v37, v37, v38, v35
	v_mul_lo_u32 v35, s13, v6
	v_mul_lo_u32 v40, s12, v3
	v_mad_u64_u32 v[38:39], s[14:15], s12, v6, 0
	v_add3_u32 v39, v39, v40, v35
	v_mul_lo_u32 v35, s13, v8
	v_mul_lo_u32 v46, s12, v7
	v_mad_u64_u32 v[44:45], s[14:15], s12, v8, 0
	v_lshl_add_u64 v[36:37], v[36:37], 2, s[6:7]
	v_lshl_add_u64 v[38:39], v[38:39], 2, s[6:7]
	v_add3_u32 v45, v45, v46, v35
	v_mul_lo_u32 v35, s13, v10
	v_mul_lo_u32 v48, s12, v9
	v_mad_u64_u32 v[46:47], s[14:15], s12, v10, 0
	v_lshl_add_u64 v[36:37], v[36:37], 0, v[20:21]
	v_lshl_add_u64 v[40:41], v[38:39], 0, v[22:23]
	v_add3_u32 v47, v47, v48, v35
	v_mul_lo_u32 v35, s13, v12
	v_mul_lo_u32 v54, s12, v11
	v_mad_u64_u32 v[52:53], s[14:15], s12, v12, 0
	global_load_dwordx4 v[36:39], v[36:37], off
	s_nop 0
	global_load_dwordx4 v[40:43], v[40:41], off
	v_lshl_add_u64 v[44:45], v[44:45], 2, s[6:7]
	v_lshl_add_u64 v[46:47], v[46:47], 2, s[6:7]
	v_add3_u32 v53, v53, v54, v35
	v_lshl_add_u64 v[44:45], v[44:45], 0, v[20:21]
	v_lshl_add_u64 v[48:49], v[46:47], 0, v[24:25]
	v_lshl_add_u64 v[52:53], v[52:53], 2, s[6:7]
	global_load_dwordx4 v[44:47], v[44:45], off
	s_nop 0
	global_load_dwordx4 v[48:51], v[48:49], off
	v_lshl_add_u64 v[52:53], v[52:53], 0, v[20:21]
	v_mul_lo_u32 v35, s13, v14
	v_mul_lo_u32 v58, s12, v13
	v_mad_u64_u32 v[56:57], s[14:15], s12, v14, 0
	global_load_dwordx4 v[52:55], v[52:53], off
	v_add3_u32 v57, v57, v58, v35
	v_lshl_add_u64 v[56:57], v[56:57], 2, s[6:7]
	v_mul_lo_u32 v62, s13, v16
	v_mul_lo_u32 v63, s12, v15
	v_mad_u64_u32 v[60:61], s[14:15], s12, v16, 0
	v_lshl_add_u64 v[56:57], v[56:57], 0, v[4:5]
	global_load_dwordx4 v[56:59], v[56:57], off
	v_add3_u32 v61, v61, v63, v62
	v_lshl_add_u64 v[60:61], v[60:61], 2, s[6:7]
	v_mul_lo_u32 v35, s13, v18
	v_mul_lo_u32 v66, s12, v17
	v_lshl_add_u64 v[60:61], v[60:61], 0, v[20:21]
	v_mad_u64_u32 v[64:65], s[12:13], s12, v18, 0
	global_load_dwordx4 v[60:63], v[60:61], off
	v_add3_u32 v65, v65, v66, v35
	v_lshl_add_u64 v[64:65], v[64:65], 2, s[6:7]
	v_lshl_add_u64 v[64:65], v[64:65], 0, v[26:27]
	global_load_dwordx4 v[64:67], v[64:65], off
	s_waitcnt vmcnt(7)
	v_mul_f32_e32 v35, v37, v37
	v_mul_f32_e32 v37, v39, v39
	s_waitcnt vmcnt(6)
	v_mul_f32_e32 v39, v41, v41
	v_mul_f32_e32 v41, v43, v43
	v_fmac_f32_e32 v35, v36, v36
	v_fmac_f32_e32 v37, v38, v38
	v_fmac_f32_e32 v39, v40, v40
	s_waitcnt vmcnt(5)
	v_mul_f32_e32 v43, v45, v45
	v_mul_f32_e32 v45, v47, v47
	v_fmac_f32_e32 v41, v42, v42
	s_waitcnt vmcnt(4)
	v_mul_f32_e32 v47, v49, v49
	v_mul_f32_e32 v49, v51, v51
	v_fmac_f32_e32 v43, v44, v44
	v_fmac_f32_e32 v45, v46, v46
	v_add_f32_e32 v35, v35, v37
	v_add_f32_e32 v36, v39, v41
	s_waitcnt vmcnt(3)
	v_mul_f32_e32 v51, v53, v53
	v_mul_f32_e32 v53, v55, v55
	v_fmac_f32_e32 v47, v48, v48
	v_fmac_f32_e32 v49, v50, v50
	v_add_f32_e32 v37, v43, v45
	v_add_f32_e32 v35, v35, v36
	v_fmac_f32_e32 v51, v52, v52
	v_add_f32_e32 v38, v47, v49
	v_add_f32_e32 v35, v35, v37
	v_fmac_f32_e32 v53, v54, v54
	v_add_f32_e32 v35, v35, v38
	v_add_f32_e32 v36, v51, v53
	v_add_f32_e32 v35, v35, v36
	s_waitcnt vmcnt(2)
	v_mul_f32_e32 v36, v57, v57
	v_mul_f32_e32 v37, v59, v59
	v_fmac_f32_e32 v36, v56, v56
	v_fmac_f32_e32 v37, v58, v58
	v_add_f32_e32 v36, v36, v37
	v_add_f32_e32 v35, v35, v36
	s_waitcnt vmcnt(1)
	v_mul_f32_e32 v36, v61, v61
	v_mul_f32_e32 v37, v63, v63
	v_fmac_f32_e32 v36, v60, v60
	v_fmac_f32_e32 v37, v62, v62
	v_add_f32_e32 v36, v36, v37
	v_add_f32_e32 v35, v35, v36
	s_waitcnt vmcnt(0)
	v_mul_f32_e32 v36, v65, v65
	v_mul_f32_e32 v37, v67, v67
	v_fmac_f32_e32 v36, v64, v64
	v_fmac_f32_e32 v37, v66, v66
	v_add_f32_e32 v36, v36, v37
	v_add_f32_e32 v35, v35, v36
	s_nop 1
	v_mov_b32_dpp v36, v35 quad_perm:[1,0,3,2] row_mask:0xf bank_mask:0xf
	s_waitcnt lgkmcnt(0)
	v_add_f32_e32 v35, v35, v36
	s_nop 1
	v_mov_b32_dpp v36, v35 quad_perm:[2,3,0,1] row_mask:0xf bank_mask:0xf
	v_add_f32_e32 v35, v35, v36
	s_nop 1
	v_mov_b32_dpp v36, v35 row_half_mirror row_mask:0xf bank_mask:0xf
	v_add_f32_e32 v35, v35, v36
	s_nop 1
	v_mov_b32_dpp v36, v35 row_mirror row_mask:0xf bank_mask:0xf
	v_add_f32_e32 v35, v35, v36
	v_mov_b32_e32 v36, v35
	s_nop 1
	v_permlane16_swap_b32_e32 v36, v35
	v_add_f32_e32 v35, v35, v36
	v_mov_b32_e32 v36, v35
	s_nop 1
	v_permlane32_swap_b32_e32 v36, v35
	s_and_saveexec_b64 s[6:7], s[0:1]
	s_cbranch_execz .LBB0_52
	v_add_f32_e32 v35, v35, v36
	v_mov_b32_e32 v36, s18
	ds_write_b32 v36, v35

.LBB0_2091:
	v_cvt_f32_i32_e32 v161, v135
	v_cvt_f32_i32_e32 v160, v134
	v_cvt_f32_i32_e32 v165, v137
	v_cvt_f32_i32_e32 v164, v136
	v_cvt_f32_i32_e32 v159, v131
	v_cvt_f32_i32_e32 v158, v130
	v_cvt_f32_i32_e32 v163, v133
	v_cvt_f32_i32_e32 v162, v132
	s_mov_b64 s[0:1], -1
	s_cmp_lt_i32 s28, 16
	v_mul_f32_e32 v156, v218, v229
	s_cbranch_scc0 .LBB0_2165
	v_and_b32_e32 v123, 64, v238
	v_pk_mul_f32 v[124:125], v[156:157], v[164:165] op_sel_hi:[0,1]
	v_pk_mul_f32 v[126:127], v[156:157], v[160:161] op_sel_hi:[0,1]
	v_add_u32_e32 v155, 64, v123
	v_pk_mul_f32 v[138:139], v[156:157], v[158:159] op_sel_hi:[0,1]
	v_mul_f32_e32 v123, v127, v127
	v_mul_f32_e32 v125, v125, v125
	v_fmac_f32_e32 v123, v126, v126
	v_fmac_f32_e32 v125, v124, v124
	v_mul_f32_e32 v124, v139, v139
	v_xor_b32_e32 v122, 16, v238
	v_pk_mul_f32 v[128:129], v[156:157], v[162:163] op_sel_hi:[0,1]
	v_add_f32_e32 v123, v123, v125
	v_fmac_f32_e32 v124, v138, v138
	v_cmp_lt_i32_e32 vcc, v122, v155
	v_add_f32_e32 v123, v124, v123
	v_mul_f32_e32 v124, v129, v129
	v_cndmask_b32_e32 v122, v238, v122, vcc
	v_fmac_f32_e32 v124, v128, v128
	v_lshlrev_b32_e32 v122, 2, v122
	v_add_f32_e32 v123, v124, v123
	v_mov_b32_e32 v125, v123
	s_nop 1
	v_permlane16_swap_b32_e32 v125, v123
	v_xor_b32_e32 v124, 32, v238
	v_cmp_lt_i32_e32 vcc, v124, v155
	v_lshlrev_b32_e32 v146, 5, v190
	s_waitcnt lgkmcnt(0)
	v_add_f32_e32 v125, v123, v125
	v_cndmask_b32_e32 v124, v238, v124, vcc
	v_lshlrev_b32_e32 v124, 2, v124
	v_mov_b32_e32 v126, v125
	s_nop 1
	v_permlane32_swap_b32_e32 v126, v125
	v_cmp_eq_u32_e32 vcc, 0, v188
	v_add_u32_e32 v123, s59, v146
	s_and_saveexec_b64 s[0:1], vcc
	s_cbranch_execz .LBB0_2094
	v_add_f32_e32 v125, v125, v126
	ds_write_b32 v123, v125
.LBB0_2094:
	s_or_b64 exec, exec, s[0:1]
	v_cvt_f32_i32_e32 v127, v119
	v_cvt_f32_i32_e32 v126, v118
	v_cvt_f32_i32_e32 v129, v121
	v_cvt_f32_i32_e32 v128, v120
	v_mov_b32_e32 v157, v156
	v_cvt_f32_i32_e32 v141, v115
	v_cvt_f32_i32_e32 v140, v114
	v_mov_b32_e32 v138, v156
	v_mov_b32_e32 v139, v156
	v_pk_mul_f32 v[126:127], v[156:157], v[126:127]
	v_cvt_f32_i32_e32 v143, v117
	v_cvt_f32_i32_e32 v142, v116
	v_pk_mul_f32 v[128:129], v[138:139], v[128:129]
	v_mul_f32_e32 v125, v127, v127
	v_fmac_f32_e32 v125, v126, v126
	v_mul_f32_e32 v126, v129, v129
	v_pk_mul_f32 v[140:141], v[156:157], v[140:141]
	v_fmac_f32_e32 v126, v128, v128
	v_add_f32_e32 v125, v125, v126
	v_mul_f32_e32 v126, v141, v141
	v_pk_mul_f32 v[138:139], v[138:139], v[142:143]
	v_fmac_f32_e32 v126, v140, v140
	v_add_f32_e32 v125, v126, v125
	v_mul_f32_e32 v126, v139, v139
	v_fmac_f32_e32 v126, v138, v138
	v_add_f32_e32 v125, v126, v125
	v_mov_b32_e32 v126, v125
	s_nop 1
	v_permlane16_swap_b32_e32 v126, v125
	v_add_f32_e32 v125, v125, v126
	v_mov_b32_e32 v126, v125
	s_nop 1
	v_permlane32_swap_b32_e32 v126, v125
	s_and_saveexec_b64 s[0:1], vcc
	s_cbranch_execz .LBB0_2096
	v_add_f32_e32 v125, v125, v126
	ds_write_b32 v123, v125 offset:16
.LBB0_2096:
	s_or_b64 exec, exec, s[0:1]
	v_cvt_f32_i32_e32 v127, v111
	v_cvt_f32_i32_e32 v126, v110
	v_cvt_f32_i32_e32 v129, v113
	v_cvt_f32_i32_e32 v128, v112
	v_mul_f32_e32 v186, v218, v228
	v_cvt_f32_i32_e32 v139, v107
	v_cvt_f32_i32_e32 v138, v106
	v_pk_mul_f32 v[126:127], v[186:187], v[126:127] op_sel_hi:[0,1]
	v_cvt_f32_i32_e32 v141, v109
	v_cvt_f32_i32_e32 v140, v108
	v_pk_mul_f32 v[128:129], v[186:187], v[128:129] op_sel_hi:[0,1]
	v_mul_f32_e32 v125, v127, v127
	v_fmac_f32_e32 v125, v126, v126
	v_mul_f32_e32 v126, v129, v129
	v_pk_mul_f32 v[138:139], v[186:187], v[138:139] op_sel_hi:[0,1]
	v_fmac_f32_e32 v126, v128, v128
	v_add_f32_e32 v125, v125, v126
	v_mul_f32_e32 v126, v139, v139
	v_pk_mul_f32 v[140:141], v[186:187], v[140:141] op_sel_hi:[0,1]
	v_fmac_f32_e32 v126, v138, v138
	v_add_f32_e32 v125, v126, v125
	v_mul_f32_e32 v126, v141, v141
	v_fmac_f32_e32 v126, v140, v140
	v_add_f32_e32 v125, v126, v125
	v_mov_b32_e32 v126, v125
	s_nop 1
	v_permlane16_swap_b32_e32 v126, v125
	v_add_f32_e32 v125, v125, v126
	v_mov_b32_e32 v126, v125
	s_nop 1
	v_permlane32_swap_b32_e32 v126, v125
	s_and_saveexec_b64 s[0:1], vcc
	s_cbranch_execz .LBB0_2098
	v_add_f32_e32 v125, v125, v126
	ds_write_b32 v123, v125 offset:512
.LBB0_2098:
	s_or_b64 exec, exec, s[0:1]
	v_cvt_f32_i32_e32 v127, v103
	v_cvt_f32_i32_e32 v126, v102
	v_cvt_f32_i32_e32 v129, v105
	v_cvt_f32_i32_e32 v128, v104
	v_mov_b32_e32 v187, v186
	v_cvt_f32_i32_e32 v141, v99
	v_cvt_f32_i32_e32 v140, v98
	v_mov_b32_e32 v138, v186
	v_mov_b32_e32 v139, v186
	v_pk_mul_f32 v[126:127], v[186:187], v[126:127]
	v_cvt_f32_i32_e32 v143, v101
	v_cvt_f32_i32_e32 v142, v100
	v_pk_mul_f32 v[128:129], v[138:139], v[128:129]
	v_mul_f32_e32 v125, v127, v127
	v_fmac_f32_e32 v125, v126, v126
	v_mul_f32_e32 v126, v129, v129
	v_pk_mul_f32 v[140:141], v[186:187], v[140:141]
	v_fmac_f32_e32 v126, v128, v128
	v_add_f32_e32 v125, v125, v126
	v_mul_f32_e32 v126, v141, v141
	v_pk_mul_f32 v[138:139], v[138:139], v[142:143]
	v_fmac_f32_e32 v126, v140, v140
	v_add_f32_e32 v125, v126, v125
	v_mul_f32_e32 v126, v139, v139
	v_fmac_f32_e32 v126, v138, v138
	v_add_f32_e32 v125, v126, v125
	v_mov_b32_e32 v126, v125
	s_nop 1
	v_permlane16_swap_b32_e32 v126, v125
	v_add_f32_e32 v125, v125, v126
	v_mov_b32_e32 v126, v125
	s_nop 1
	v_permlane32_swap_b32_e32 v126, v125
	s_and_saveexec_b64 s[0:1], vcc
	s_cbranch_execz .LBB0_2100
	v_add_f32_e32 v125, v125, v126
	ds_write_b32 v123, v125 offset:528
.LBB0_2100:
	s_or_b64 exec, exec, s[0:1]
	v_cvt_f32_i32_e32 v127, v95
	v_cvt_f32_i32_e32 v126, v94
	v_cvt_f32_i32_e32 v129, v97
	v_cvt_f32_i32_e32 v128, v96
	v_mul_f32_e32 v184, v218, v226
	v_cvt_f32_i32_e32 v139, v91
	v_cvt_f32_i32_e32 v138, v90
	v_pk_mul_f32 v[126:127], v[184:185], v[126:127] op_sel_hi:[0,1]
	v_cvt_f32_i32_e32 v141, v93
	v_cvt_f32_i32_e32 v140, v92
	v_pk_mul_f32 v[128:129], v[184:185], v[128:129] op_sel_hi:[0,1]
	v_mul_f32_e32 v125, v127, v127
	v_fmac_f32_e32 v125, v126, v126
	v_mul_f32_e32 v126, v129, v129
	v_pk_mul_f32 v[138:139], v[184:185], v[138:139] op_sel_hi:[0,1]
	v_fmac_f32_e32 v126, v128, v128
	v_add_f32_e32 v125, v125, v126
	v_mul_f32_e32 v126, v139, v139
	v_pk_mul_f32 v[140:141], v[184:185], v[140:141] op_sel_hi:[0,1]
	v_fmac_f32_e32 v126, v138, v138
	v_add_f32_e32 v125, v126, v125
	v_mul_f32_e32 v126, v141, v141
	v_fmac_f32_e32 v126, v140, v140
	v_add_f32_e32 v125, v126, v125
	v_mov_b32_e32 v126, v125
	s_nop 1
	v_permlane16_swap_b32_e32 v126, v125
	v_add_f32_e32 v125, v125, v126
	v_mov_b32_e32 v126, v125
	s_nop 1
	v_permlane32_swap_b32_e32 v126, v125
	s_and_saveexec_b64 s[0:1], vcc
	s_cbranch_execz .LBB0_2102
	v_add_f32_e32 v125, v125, v126
	ds_write_b32 v123, v125 offset:1024
.LBB0_2102:
	s_or_b64 exec, exec, s[0:1]
	v_cvt_f32_i32_e32 v127, v87
	v_cvt_f32_i32_e32 v126, v86
	v_cvt_f32_i32_e32 v129, v89
	v_cvt_f32_i32_e32 v128, v88
	v_mov_b32_e32 v185, v184
	v_cvt_f32_i32_e32 v141, v83
	v_cvt_f32_i32_e32 v140, v82
	v_mov_b32_e32 v138, v184
	v_mov_b32_e32 v139, v184
	v_pk_mul_f32 v[126:127], v[184:185], v[126:127]
	v_cvt_f32_i32_e32 v143, v85
	v_cvt_f32_i32_e32 v142, v84
	v_pk_mul_f32 v[128:129], v[138:139], v[128:129]
	v_mul_f32_e32 v125, v127, v127
	v_fmac_f32_e32 v125, v126, v126
	v_mul_f32_e32 v126, v129, v129
	v_pk_mul_f32 v[140:141], v[184:185], v[140:141]
	v_fmac_f32_e32 v126, v128, v128
	v_add_f32_e32 v125, v125, v126
	v_mul_f32_e32 v126, v141, v141
	v_pk_mul_f32 v[138:139], v[138:139], v[142:143]
	v_fmac_f32_e32 v126, v140, v140
	v_add_f32_e32 v125, v126, v125
	v_mul_f32_e32 v126, v139, v139
	v_fmac_f32_e32 v126, v138, v138
	v_add_f32_e32 v125, v126, v125
	v_mov_b32_e32 v126, v125
	s_nop 1
	v_permlane16_swap_b32_e32 v126, v125
	v_add_f32_e32 v125, v125, v126
	v_mov_b32_e32 v126, v125
	s_nop 1
	v_permlane32_swap_b32_e32 v126, v125
	s_and_saveexec_b64 s[0:1], vcc
	s_cbranch_execz .LBB0_2104
	v_add_f32_e32 v125, v125, v126
	ds_write_b32 v123, v125 offset:1040
.LBB0_2104:
	s_or_b64 exec, exec, s[0:1]
	v_cvt_f32_i32_e32 v127, v79
	v_cvt_f32_i32_e32 v126, v78
	v_cvt_f32_i32_e32 v129, v81
	v_cvt_f32_i32_e32 v128, v80
	v_mul_f32_e32 v182, v218, v224
	v_cvt_f32_i32_e32 v139, v75
	v_cvt_f32_i32_e32 v138, v74
	v_pk_mul_f32 v[126:127], v[182:183], v[126:127] op_sel_hi:[0,1]
	v_cvt_f32_i32_e32 v141, v77
	v_cvt_f32_i32_e32 v140, v76
	v_pk_mul_f32 v[128:129], v[182:183], v[128:129] op_sel_hi:[0,1]
	v_mul_f32_e32 v125, v127, v127
	v_fmac_f32_e32 v125, v126, v126
	v_mul_f32_e32 v126, v129, v129
	v_pk_mul_f32 v[138:139], v[182:183], v[138:139] op_sel_hi:[0,1]
	v_fmac_f32_e32 v126, v128, v128
	v_add_f32_e32 v125, v125, v126
	v_mul_f32_e32 v126, v139, v139
	v_pk_mul_f32 v[140:141], v[182:183], v[140:141] op_sel_hi:[0,1]
	v_fmac_f32_e32 v126, v138, v138
	v_add_f32_e32 v125, v126, v125
	v_mul_f32_e32 v126, v141, v141
	v_fmac_f32_e32 v126, v140, v140
	v_add_f32_e32 v125, v126, v125
	v_mov_b32_e32 v126, v125
	s_nop 1
	v_permlane16_swap_b32_e32 v126, v125
	v_add_f32_e32 v125, v125, v126
	v_mov_b32_e32 v126, v125
	s_nop 1
	v_permlane32_swap_b32_e32 v126, v125
	s_and_saveexec_b64 s[0:1], vcc
	s_cbranch_execz .LBB0_2106
	v_add_f32_e32 v125, v125, v126
	ds_write_b32 v123, v125 offset:1536
.LBB0_2106:
	s_or_b64 exec, exec, s[0:1]
	v_cvt_f32_i32_e32 v127, v71
	v_cvt_f32_i32_e32 v126, v70
	v_cvt_f32_i32_e32 v129, v73
	v_cvt_f32_i32_e32 v128, v72
	v_mov_b32_e32 v183, v182
	v_cvt_f32_i32_e32 v141, v67
	v_cvt_f32_i32_e32 v140, v66
	v_mov_b32_e32 v138, v182
	v_mov_b32_e32 v139, v182
	v_pk_mul_f32 v[126:127], v[182:183], v[126:127]
	v_cvt_f32_i32_e32 v143, v69
	v_cvt_f32_i32_e32 v142, v68
	v_pk_mul_f32 v[128:129], v[138:139], v[128:129]
	v_mul_f32_e32 v125, v127, v127
	v_fmac_f32_e32 v125, v126, v126
	v_mul_f32_e32 v126, v129, v129
	v_pk_mul_f32 v[140:141], v[182:183], v[140:141]
	v_fmac_f32_e32 v126, v128, v128
	v_add_f32_e32 v125, v125, v126
	v_mul_f32_e32 v126, v141, v141
	v_pk_mul_f32 v[138:139], v[138:139], v[142:143]
	v_fmac_f32_e32 v126, v140, v140
	v_add_f32_e32 v125, v126, v125
	v_mul_f32_e32 v126, v139, v139
	v_fmac_f32_e32 v126, v138, v138
	v_add_f32_e32 v125, v126, v125
	v_mov_b32_e32 v126, v125
	s_nop 1
	v_permlane16_swap_b32_e32 v126, v125
	v_add_f32_e32 v125, v125, v126
	v_mov_b32_e32 v126, v125
	s_nop 1
	v_permlane32_swap_b32_e32 v126, v125
	s_and_saveexec_b64 s[0:1], vcc
	s_cbranch_execz .LBB0_2108
	v_add_f32_e32 v125, v125, v126
	ds_write_b32 v123, v125 offset:1552
.LBB0_2108:
	s_or_b64 exec, exec, s[0:1]
	v_cvt_f32_i32_e32 v127, v63
	v_cvt_f32_i32_e32 v126, v62
	v_cvt_f32_i32_e32 v129, v65
	v_cvt_f32_i32_e32 v128, v64
	v_mul_f32_e32 v180, v218, v222
	v_cvt_f32_i32_e32 v139, v59
	v_cvt_f32_i32_e32 v138, v58
	v_pk_mul_f32 v[126:127], v[180:181], v[126:127] op_sel_hi:[0,1]
	v_cvt_f32_i32_e32 v141, v61
	v_cvt_f32_i32_e32 v140, v60
	v_pk_mul_f32 v[128:129], v[180:181], v[128:129] op_sel_hi:[0,1]
	v_mul_f32_e32 v125, v127, v127
	v_fmac_f32_e32 v125, v126, v126
	v_mul_f32_e32 v126, v129, v129
	v_pk_mul_f32 v[138:139], v[180:181], v[138:139] op_sel_hi:[0,1]
	v_fmac_f32_e32 v126, v128, v128
	v_add_f32_e32 v125, v125, v126
	v_mul_f32_e32 v126, v139, v139
	v_pk_mul_f32 v[140:141], v[180:181], v[140:141] op_sel_hi:[0,1]
	v_fmac_f32_e32 v126, v138, v138
	v_add_f32_e32 v125, v126, v125
	v_mul_f32_e32 v126, v141, v141
	v_fmac_f32_e32 v126, v140, v140
	v_add_f32_e32 v125, v126, v125
	v_mov_b32_e32 v126, v125
	s_nop 1
	v_permlane16_swap_b32_e32 v126, v125
	v_add_f32_e32 v125, v125, v126
	v_mov_b32_e32 v126, v125
	s_nop 1
	v_permlane32_swap_b32_e32 v126, v125
	s_and_saveexec_b64 s[0:1], vcc
	s_cbranch_execz .LBB0_2110
	v_add_f32_e32 v125, v125, v126
	ds_write_b32 v123, v125 offset:4096
.LBB0_2110:
	s_or_b64 exec, exec, s[0:1]
	v_cvt_f32_i32_e32 v127, v55
	v_cvt_f32_i32_e32 v126, v54
	v_cvt_f32_i32_e32 v129, v57
	v_cvt_f32_i32_e32 v128, v56
	v_mov_b32_e32 v181, v180
	v_cvt_f32_i32_e32 v141, v51
	v_cvt_f32_i32_e32 v140, v50
	v_mov_b32_e32 v138, v180
	v_mov_b32_e32 v139, v180
	v_pk_mul_f32 v[126:127], v[180:181], v[126:127]
	v_cvt_f32_i32_e32 v143, v53
	v_cvt_f32_i32_e32 v142, v52
	v_pk_mul_f32 v[128:129], v[138:139], v[128:129]
	v_mul_f32_e32 v125, v127, v127
	v_fmac_f32_e32 v125, v126, v126
	v_mul_f32_e32 v126, v129, v129
	v_pk_mul_f32 v[140:141], v[180:181], v[140:141]
	v_fmac_f32_e32 v126, v128, v128
	v_add_f32_e32 v125, v125, v126
	v_mul_f32_e32 v126, v141, v141
	v_pk_mul_f32 v[138:139], v[138:139], v[142:143]
	v_fmac_f32_e32 v126, v140, v140
	v_add_f32_e32 v125, v126, v125
	v_mul_f32_e32 v126, v139, v139
	v_fmac_f32_e32 v126, v138, v138
	v_add_f32_e32 v125, v126, v125
	v_mov_b32_e32 v126, v125
	s_nop 1
	v_permlane16_swap_b32_e32 v126, v125
	v_add_f32_e32 v125, v125, v126
	v_mov_b32_e32 v126, v125
	s_nop 1
	v_permlane32_swap_b32_e32 v126, v125
	s_and_saveexec_b64 s[0:1], vcc
	s_cbranch_execz .LBB0_2112
	v_add_f32_e32 v125, v125, v126
	ds_write_b32 v123, v125 offset:4112
.LBB0_2112:
	s_or_b64 exec, exec, s[0:1]
	v_cvt_f32_i32_e32 v127, v47
	v_cvt_f32_i32_e32 v126, v46
	v_cvt_f32_i32_e32 v129, v49
	v_cvt_f32_i32_e32 v128, v48
	v_mul_f32_e32 v174, v218, v221
	v_cvt_f32_i32_e32 v139, v43
	v_cvt_f32_i32_e32 v138, v42
	v_pk_mul_f32 v[126:127], v[174:175], v[126:127] op_sel_hi:[0,1]
	v_cvt_f32_i32_e32 v141, v45
	v_cvt_f32_i32_e32 v140, v44
	v_pk_mul_f32 v[128:129], v[174:175], v[128:129] op_sel_hi:[0,1]
	v_mul_f32_e32 v125, v127, v127
	v_fmac_f32_e32 v125, v126, v126
	v_mul_f32_e32 v126, v129, v129
	v_pk_mul_f32 v[138:139], v[174:175], v[138:139] op_sel_hi:[0,1]
	v_fmac_f32_e32 v126, v128, v128
	v_add_f32_e32 v125, v125, v126
	v_mul_f32_e32 v126, v139, v139
	v_pk_mul_f32 v[140:141], v[174:175], v[140:141] op_sel_hi:[0,1]
	v_fmac_f32_e32 v126, v138, v138
	v_add_f32_e32 v125, v126, v125
	v_mul_f32_e32 v126, v141, v141
	v_fmac_f32_e32 v126, v140, v140
	v_add_f32_e32 v125, v126, v125
	v_mov_b32_e32 v126, v125
	s_nop 1
	v_permlane16_swap_b32_e32 v126, v125
	v_add_f32_e32 v125, v125, v126
	v_mov_b32_e32 v126, v125
	s_nop 1
	v_permlane32_swap_b32_e32 v126, v125
	s_and_saveexec_b64 s[0:1], vcc
	s_cbranch_execz .LBB0_2114
	v_add_f32_e32 v125, v125, v126
	ds_write_b32 v123, v125 offset:4608
.LBB0_2114:
	s_or_b64 exec, exec, s[0:1]
	v_cvt_f32_i32_e32 v127, v39
	v_cvt_f32_i32_e32 v126, v38
	v_cvt_f32_i32_e32 v129, v41
	v_cvt_f32_i32_e32 v128, v40
	v_mov_b32_e32 v175, v174
	v_cvt_f32_i32_e32 v141, v35
	v_cvt_f32_i32_e32 v140, v34
	v_mov_b32_e32 v138, v174
	v_mov_b32_e32 v139, v174
	v_pk_mul_f32 v[126:127], v[174:175], v[126:127]
	v_cvt_f32_i32_e32 v143, v37
	v_cvt_f32_i32_e32 v142, v36
	v_pk_mul_f32 v[128:129], v[138:139], v[128:129]
	v_mul_f32_e32 v125, v127, v127
	v_fmac_f32_e32 v125, v126, v126
	v_mul_f32_e32 v126, v129, v129
	v_pk_mul_f32 v[140:141], v[174:175], v[140:141]
	v_fmac_f32_e32 v126, v128, v128
	v_add_f32_e32 v125, v125, v126
	v_mul_f32_e32 v126, v141, v141
	v_pk_mul_f32 v[138:139], v[138:139], v[142:143]
	v_fmac_f32_e32 v126, v140, v140
	v_add_f32_e32 v125, v126, v125
	v_mul_f32_e32 v126, v139, v139
	v_fmac_f32_e32 v126, v138, v138
	v_add_f32_e32 v125, v126, v125
	v_mov_b32_e32 v126, v125
	s_nop 1
	v_permlane16_swap_b32_e32 v126, v125
	v_add_f32_e32 v125, v125, v126
	v_mov_b32_e32 v126, v125
	s_nop 1
	v_permlane32_swap_b32_e32 v126, v125
	s_and_saveexec_b64 s[0:1], vcc
	s_cbranch_execz .LBB0_2116
	v_add_f32_e32 v125, v125, v126
	ds_write_b32 v123, v125 offset:4624
.LBB0_2116:
	s_or_b64 exec, exec, s[0:1]
	v_cvt_f32_i32_e32 v127, v31
	v_cvt_f32_i32_e32 v126, v30
	v_cvt_f32_i32_e32 v129, v33
	v_cvt_f32_i32_e32 v128, v32
	v_mul_f32_e32 v170, v218, v220
	v_cvt_f32_i32_e32 v139, v27
	v_cvt_f32_i32_e32 v138, v26
	v_pk_mul_f32 v[126:127], v[170:171], v[126:127] op_sel_hi:[0,1]
	v_cvt_f32_i32_e32 v141, v29
	v_cvt_f32_i32_e32 v140, v28
	v_pk_mul_f32 v[128:129], v[170:171], v[128:129] op_sel_hi:[0,1]
	v_mul_f32_e32 v125, v127, v127
	v_fmac_f32_e32 v125, v126, v126
	v_mul_f32_e32 v126, v129, v129
	v_pk_mul_f32 v[138:139], v[170:171], v[138:139] op_sel_hi:[0,1]
	v_fmac_f32_e32 v126, v128, v128
	v_add_f32_e32 v125, v125, v126
	v_mul_f32_e32 v126, v139, v139
	v_pk_mul_f32 v[140:141], v[170:171], v[140:141] op_sel_hi:[0,1]
	v_fmac_f32_e32 v126, v138, v138
	v_add_f32_e32 v125, v126, v125
	v_mul_f32_e32 v126, v141, v141
	v_fmac_f32_e32 v126, v140, v140
	v_add_f32_e32 v125, v126, v125
	v_mov_b32_e32 v126, v125
	s_nop 1
	v_permlane16_swap_b32_e32 v126, v125
	v_add_f32_e32 v125, v125, v126
	v_mov_b32_e32 v126, v125
	s_nop 1
	v_permlane32_swap_b32_e32 v126, v125
	s_and_saveexec_b64 s[0:1], vcc
	s_cbranch_execz .LBB0_2118
	v_add_f32_e32 v125, v125, v126
	ds_write_b32 v123, v125 offset:5120
.LBB0_2118:
	s_or_b64 exec, exec, s[0:1]
	v_cvt_f32_i32_e32 v127, v23
	v_cvt_f32_i32_e32 v126, v22
	v_cvt_f32_i32_e32 v129, v25
	v_cvt_f32_i32_e32 v128, v24
	v_mov_b32_e32 v171, v170
	v_cvt_f32_i32_e32 v141, v19
	v_cvt_f32_i32_e32 v140, v18
	v_mov_b32_e32 v138, v170
	v_mov_b32_e32 v139, v170
	v_pk_mul_f32 v[126:127], v[170:171], v[126:127]
	v_cvt_f32_i32_e32 v143, v21
	v_cvt_f32_i32_e32 v142, v20
	v_pk_mul_f32 v[128:129], v[138:139], v[128:129]
	v_mul_f32_e32 v125, v127, v127
	v_fmac_f32_e32 v125, v126, v126
	v_mul_f32_e32 v126, v129, v129
	v_pk_mul_f32 v[140:141], v[170:171], v[140:141]
	v_fmac_f32_e32 v126, v128, v128
	v_add_f32_e32 v125, v125, v126
	v_mul_f32_e32 v126, v141, v141
	v_pk_mul_f32 v[138:139], v[138:139], v[142:143]
	v_fmac_f32_e32 v126, v140, v140
	v_add_f32_e32 v125, v126, v125
	v_mul_f32_e32 v126, v139, v139
	v_fmac_f32_e32 v126, v138, v138
	v_add_f32_e32 v125, v126, v125
	v_mov_b32_e32 v126, v125
	s_nop 1
	v_permlane16_swap_b32_e32 v126, v125
	v_add_f32_e32 v125, v125, v126
	v_mov_b32_e32 v126, v125
	s_nop 1
	v_permlane32_swap_b32_e32 v126, v125
	s_and_saveexec_b64 s[0:1], vcc
	s_cbranch_execz .LBB0_2120
	v_add_f32_e32 v125, v125, v126
	ds_write_b32 v123, v125 offset:5136
.LBB0_2120:
	s_or_b64 exec, exec, s[0:1]
	v_cvt_f32_i32_e32 v127, v15
	v_cvt_f32_i32_e32 v126, v14
	v_cvt_f32_i32_e32 v129, v17
	v_cvt_f32_i32_e32 v128, v16
	v_mul_f32_e32 v166, v218, v219
	v_cvt_f32_i32_e32 v139, v11
	v_cvt_f32_i32_e32 v138, v10
	v_pk_mul_f32 v[126:127], v[166:167], v[126:127] op_sel_hi:[0,1]
	v_cvt_f32_i32_e32 v141, v13
	v_cvt_f32_i32_e32 v140, v12
	v_pk_mul_f32 v[128:129], v[166:167], v[128:129] op_sel_hi:[0,1]
	v_mul_f32_e32 v125, v127, v127
	v_fmac_f32_e32 v125, v126, v126
	v_mul_f32_e32 v126, v129, v129
	v_pk_mul_f32 v[138:139], v[166:167], v[138:139] op_sel_hi:[0,1]
	v_fmac_f32_e32 v126, v128, v128
	v_add_f32_e32 v125, v125, v126
	v_mul_f32_e32 v126, v139, v139
	v_pk_mul_f32 v[140:141], v[166:167], v[140:141] op_sel_hi:[0,1]
	v_fmac_f32_e32 v126, v138, v138
	v_add_f32_e32 v125, v126, v125
	v_mul_f32_e32 v126, v141, v141
	v_fmac_f32_e32 v126, v140, v140
	v_add_f32_e32 v125, v126, v125
	v_mov_b32_e32 v126, v125
	s_nop 1
	v_permlane16_swap_b32_e32 v126, v125
	v_add_f32_e32 v125, v125, v126
	v_mov_b32_e32 v126, v125
	s_nop 1
	v_permlane32_swap_b32_e32 v126, v125
	s_and_saveexec_b64 s[0:1], vcc
	s_cbranch_execz .LBB0_2122
	v_add_f32_e32 v125, v125, v126
	ds_write_b32 v123, v125 offset:5632
.LBB0_2122:
	s_or_b64 exec, exec, s[0:1]
	v_cvt_f32_i32_e32 v127, v7
	v_cvt_f32_i32_e32 v126, v6
	v_cvt_f32_i32_e32 v129, v9
	v_cvt_f32_i32_e32 v128, v8
	v_mov_b32_e32 v167, v166
	v_cvt_f32_i32_e32 v141, v3
	v_cvt_f32_i32_e32 v140, v2
	v_mov_b32_e32 v138, v166
	v_mov_b32_e32 v139, v166
	v_pk_mul_f32 v[126:127], v[166:167], v[126:127]
	v_cvt_f32_i32_e32 v143, v5
	v_cvt_f32_i32_e32 v142, v4
	v_pk_mul_f32 v[128:129], v[138:139], v[128:129]
	v_mul_f32_e32 v125, v127, v127
	v_fmac_f32_e32 v125, v126, v126
	v_mul_f32_e32 v126, v129, v129
	v_pk_mul_f32 v[140:141], v[166:167], v[140:141]
	v_fmac_f32_e32 v126, v128, v128
	v_add_f32_e32 v125, v125, v126
	v_mul_f32_e32 v126, v141, v141
	v_pk_mul_f32 v[138:139], v[138:139], v[142:143]
	v_fmac_f32_e32 v126, v140, v140
	v_add_f32_e32 v125, v126, v125
	v_mul_f32_e32 v126, v139, v139
	v_fmac_f32_e32 v126, v138, v138
	v_add_f32_e32 v125, v126, v125
	v_mov_b32_e32 v122, v125
	s_nop 1
	v_permlane16_swap_b32_e32 v122, v125
	v_add_f32_e32 v122, v125, v122
	v_mov_b32_e32 v124, v122
	s_nop 1
	v_permlane32_swap_b32_e32 v124, v122
	s_and_saveexec_b64 s[0:1], vcc
	s_cbranch_execz .LBB0_2124
	v_add_f32_e32 v122, v122, v124
	ds_write_b32 v123, v122 offset:5648
.LBB0_2124:
	s_or_b64 exec, exec, s[0:1]
	v_readlane_b32 s68, v254, 24
	v_lshl_add_u32 v168, v188, 2, s56
	s_cmp_gt_i32 s28, 7
	v_readlane_b32 s78, v254, 34
	v_readlane_b32 s79, v254, 35
	v_readlane_b32 s80, v254, 36
	v_readlane_b32 s81, v254, 37
	v_ashrrev_i32_e32 v169, 31, v168
	v_lshlrev_b32_e32 v138, 8, v154
	s_cselect_b32 s0, s80, s78
	s_cselect_b32 s1, s81, s79
	v_lshlrev_b64 v[172:173], 2, v[168:169]
	v_and_b32_e32 v202, 0x7ff00, v138
	s_waitcnt lgkmcnt(0)
	s_barrier
	s_mov_b64 s[98:99], 0x1000
	s_mov_b64 s[100:101], 0x5000
	v_lshl_add_u64 v[122:123], s[0:1], 0, v[172:173]
	v_lshl_add_u64 v[138:139], s[8:9], 0, v[202:203]
	v_lshl_add_u64 v[142:143], s[16:17], 0, v[202:203]
	global_load_dwordx4 v[126:129], v[122:123], off
	s_waitcnt lgkmcnt(0)
	global_load_dwordx4 v[122:125], v[122:123], off offset:256
	v_lshl_add_u64 v[138:139], v[138:139], 0, v[172:173]
	v_lshl_add_u64 v[142:143], v[142:143], 0, v[172:173]
	v_lshl_add_u64 v[244:245], v[138:139], 0, s[98:99]
	v_lshl_add_u64 v[250:251], v[142:143], 0, s[98:99]
	global_load_dwordx4 v[138:141], v[138:139], off
	s_cselect_b32 s2, 0x800, 0
	global_load_dwordx4 v[142:145], v[142:143], off
	global_load_dwordx4 v[244:247], v[244:245], off
	global_load_dwordx4 v[250:253], v[250:251], off
	s_lshl_b32 s21, s28, 8
	s_and_b32 s21, s21, 0x700
	s_or_b32 s2, s2, s21
	s_add_i32 s21, 0, 0x20000
	v_add_u32_e32 v157, s21, v146
	ds_read_b128 v[146:149], v157
	v_mov_b64_e32 v[176:177], s[6:7]
	v_cvt_f32_i32_e32 v131, v131
	v_cvt_f32_i32_e32 v130, v130
	s_waitcnt lgkmcnt(0)
	v_mov_b32_e32 v150, v147
	v_mov_b32_e32 v151, v148
	v_mov_b32_e32 v147, v149
	v_pk_add_f32 v[146:147], v[150:151], v[146:147]
	v_cvt_f32_i32_e32 v133, v133
	v_add_f32_e32 v146, v146, v147
	v_fmamk_f32 v146, v146, 0x3c000000, v235
	v_cmp_gt_f32_e32 vcc, s63, v146
	v_mul_f32_e32 v147, 0x4f800000, v146
	v_cvt_f32_i32_e32 v132, v132
	v_cndmask_b32_e32 v146, v146, v147, vcc
	v_sqrt_f32_e32 v147, v146
	v_cvt_f32_i32_e32 v137, v137
	v_cvt_f32_i32_e32 v136, v136
	v_cvt_f32_i32_e32 v135, v135
	v_add_u32_e32 v148, -1, v147
	v_fma_f32 v149, -v148, v147, v146
	v_cmp_ge_f32_e64 s[0:1], 0, v149
	v_add_u32_e32 v149, 1, v147
	v_cvt_f32_i32_e32 v134, v134
	v_cndmask_b32_e64 v148, v147, v148, s[0:1]
	v_fma_f32 v147, -v149, v147, v146
	v_cmp_lt_f32_e64 s[0:1], 0, v147
	s_lshl_b32 s2, s2, 1
	v_mov_b64_e32 v[216:217], v[108:109]
	v_cndmask_b32_e64 v147, v148, v149, s[0:1]
	v_mul_f32_e32 v148, 0x37800000, v147
	v_cndmask_b32_e32 v147, v147, v148, vcc
	v_cmp_class_f32_e32 vcc, v146, v236
	v_mad_i64_i32 v[178:179], s[0:1], v154, s64, v[176:177]
	s_nop 0
	v_cndmask_b32_e32 v146, v147, v146, vcc
	v_div_scale_f32 v147, s[0:1], v146, v146, 1.0
	v_rcp_f32_e32 v148, v147
	v_lshl_add_u64 v[192:193], v[178:179], 0, s[2:3]
	v_lshlrev_b64 v[178:179], 1, v[168:169]
	v_lshl_add_u64 v[192:193], v[192:193], 0, v[178:179]
	v_fma_f32 v149, -v147, v148, 1.0
	v_fmac_f32_e32 v148, v149, v148
	v_div_scale_f32 v149, vcc, 1.0, v146, 1.0
	v_mul_f32_e32 v150, v149, v148
	v_fma_f32 v151, -v147, v150, v149
	v_fmac_f32_e32 v150, v151, v148
	v_fma_f32 v147, -v147, v150, v149
	v_div_fmas_f32 v147, v147, v148, v150
	v_div_fixup_f32 v146, v147, v146, 1.0
	v_mul_f32_e32 v146, v156, v146
	v_pk_mul_f32 v[132:133], v[146:147], v[132:133] op_sel_hi:[0,1]
	v_pk_mul_f32 v[130:131], v[146:147], v[130:131] op_sel_hi:[0,1]
	v_pk_mul_f32 v[134:135], v[146:147], v[134:135] op_sel_hi:[0,1]
	v_pk_mul_f32 v[136:137], v[146:147], v[136:137] op_sel_hi:[0,1]
	v_mov_b64_e32 v[214:215], v[106:107]
	s_cmp_lt_i32 s28, 8
	v_readlane_b32 s69, v254, 25
	v_readlane_b32 s70, v254, 26
	v_readlane_b32 s71, v254, 27
	v_readlane_b32 s72, v254, 28
	v_readlane_b32 s73, v254, 29
	v_readlane_b32 s74, v254, 30
	v_readlane_b32 s75, v254, 31
	v_readlane_b32 s76, v254, 32
	s_waitcnt vmcnt(2)
	v_pk_mul_f32 v[136:137], v[128:129], v[136:137]
	v_pk_mul_f32 v[130:131], v[122:123], v[130:131]
	v_pk_mul_f32 v[132:133], v[124:125], v[132:133]
	v_pk_mul_f32 v[134:135], v[126:127], v[134:135]
	v_readlane_b32 s77, v254, 33
	v_readlane_b32 s82, v254, 38
	v_pk_mul_f32 v[146:147], v[144:145], v[132:133]
	v_pk_mul_f32 v[148:149], v[142:143], v[130:131]
	v_pk_fma_f32 v[146:147], v[140:141], v[136:137], v[146:147] neg_lo:[0,0,1] neg_hi:[0,0,1]
	v_pk_fma_f32 v[148:149], v[138:139], v[134:135], v[148:149] neg_lo:[0,0,1] neg_hi:[0,0,1]
	v_pk_mul_f32 v[136:137], v[144:145], v[136:137]
	v_pk_mul_f32 v[134:135], v[142:143], v[134:135]
	v_pk_fma_f32 v[152:153], v[140:141], v[132:133], v[136:137]
	v_pk_fma_f32 v[150:151], v[138:139], v[130:131], v[134:135]
	v_pk_add_f32 v[136:137], v[146:147], 0 op_sel_hi:[1,0]
	v_pk_add_f32 v[134:135], v[148:149], 0 op_sel_hi:[1,0]
	v_pk_add_f32 v[132:133], v[152:153], 0 op_sel_hi:[1,0]
	v_pk_add_f32 v[130:131], v[150:151], 0 op_sel_hi:[1,0]
	v_readlane_b32 s83, v254, 39
	v_cvt_pk_bf16_f32 v148, v148, v149
	v_cvt_pk_bf16_f32 v149, v146, v147
	v_cvt_pk_bf16_f32 v146, v150, v151
	v_cvt_pk_bf16_f32 v147, v152, v153
	global_store_dwordx2 v[192:193], v[148:149], off
	global_store_dwordx2 v[192:193], v[146:147], off offset:128
	ds_read_b128 v[146:149], v157 offset:16
	s_waitcnt lgkmcnt(0)
	v_mov_b32_e32 v150, v147
	v_mov_b32_e32 v151, v148
	v_mov_b32_e32 v147, v149
	v_pk_add_f32 v[146:147], v[150:151], v[146:147]
	s_nop 0
	v_add_f32_e32 v146, v146, v147
	v_fmamk_f32 v146, v146, 0x3c000000, v235
	v_cmp_gt_f32_e32 vcc, s63, v146
	v_mul_f32_e32 v147, 0x4f800000, v146
	s_nop 0
	v_cndmask_b32_e32 v146, v146, v147, vcc
	v_sqrt_f32_e32 v147, v146
	s_nop 0
	v_add_u32_e32 v148, -1, v147
	v_fma_f32 v149, -v148, v147, v146
	v_cmp_ge_f32_e64 s[0:1], 0, v149
	v_add_u32_e32 v149, 1, v147
	s_nop 0
	v_cndmask_b32_e64 v148, v147, v148, s[0:1]
	v_fma_f32 v147, -v149, v147, v146
	v_cmp_lt_f32_e64 s[0:1], 0, v147
	s_nop 1
	v_cndmask_b32_e64 v147, v148, v149, s[0:1]
	v_mul_f32_e32 v148, 0x37800000, v147
	v_cndmask_b32_e32 v147, v147, v148, vcc
	v_cmp_class_f32_e32 vcc, v146, v236
	s_nop 1
	v_cndmask_b32_e32 v146, v147, v146, vcc
	v_div_scale_f32 v147, s[0:1], v146, v146, 1.0
	v_rcp_f32_e32 v148, v147
	s_nop 0
	v_fma_f32 v149, -v147, v148, 1.0
	v_fmac_f32_e32 v148, v149, v148
	v_div_scale_f32 v149, vcc, 1.0, v146, 1.0
	v_mul_f32_e32 v150, v149, v148
	v_fma_f32 v151, -v147, v150, v149
	v_fmac_f32_e32 v150, v151, v148
	v_fma_f32 v147, -v147, v150, v149
	v_div_fmas_f32 v147, v147, v148, v150
	v_div_fixup_f32 v157, v147, v146, 1.0
	v_mov_b64_e32 v[148:149], v[116:117]
	v_mov_b64_e32 v[152:153], v[120:121]
	v_mov_b64_e32 v[146:147], v[114:115]
	v_mov_b64_e32 v[150:151], v[118:119]
	v_mul_f32_e32 v202, v156, v157
	v_cvt_f32_i32_e32 v153, v153
	v_cvt_f32_i32_e32 v152, v152
	v_cvt_f32_i32_e32 v151, v151
	v_cvt_f32_i32_e32 v150, v150
	v_cvt_f32_i32_e32 v147, v147
	v_cvt_f32_i32_e32 v146, v146
	v_cvt_f32_i32_e32 v149, v149
	v_cvt_f32_i32_e32 v148, v148
	v_pk_mul_f32 v[150:151], v[202:203], v[150:151] op_sel_hi:[0,1]
	v_pk_mul_f32 v[152:153], v[202:203], v[152:153] op_sel_hi:[0,1]
	v_pk_mul_f32 v[146:147], v[202:203], v[146:147] op_sel_hi:[0,1]
	v_pk_mul_f32 v[148:149], v[202:203], v[148:149] op_sel_hi:[0,1]
	v_pk_mul_f32 v[152:153], v[128:129], v[152:153]
	v_pk_mul_f32 v[150:151], v[126:127], v[150:151]
	v_pk_mul_f32 v[146:147], v[122:123], v[146:147]
	v_pk_mul_f32 v[148:149], v[124:125], v[148:149]
	v_pk_mul_f32 v[212:213], v[142:143], v[146:147]
	v_pk_mul_f32 v[210:211], v[144:145], v[148:149]
	v_pk_mul_f32 v[144:145], v[144:145], v[152:153]
	v_pk_mul_f32 v[142:143], v[142:143], v[150:151]
	v_pk_fma_f32 v[212:213], v[138:139], v[150:151], v[212:213] neg_lo:[0,0,1] neg_hi:[0,0,1]
	v_pk_fma_f32 v[210:211], v[140:141], v[152:153], v[210:211] neg_lo:[0,0,1] neg_hi:[0,0,1]
	v_pk_fma_f32 v[146:147], v[138:139], v[146:147], v[142:143]
	v_pk_fma_f32 v[148:149], v[140:141], v[148:149], v[144:145]
	v_pk_add_f32 v[144:145], v[210:211], 0 op_sel_hi:[1,0]
	v_pk_add_f32 v[142:143], v[212:213], 0 op_sel_hi:[1,0]
	v_pk_add_f32 v[140:141], v[148:149], 0 op_sel_hi:[1,0]
	v_pk_add_f32 v[138:139], v[146:147], 0 op_sel_hi:[1,0]
	v_add_u32_e32 v157, 16, v190
	v_cvt_pk_bf16_f32 v150, v212, v213
	v_cvt_pk_bf16_f32 v151, v210, v211
	v_cvt_pk_bf16_f32 v146, v146, v147
	v_add_u32_e32 v167, s19, v157
	v_cvt_pk_bf16_f32 v147, v148, v149
	global_store_dwordx2 v[192:193], v[150:151], off offset:256
	global_store_dwordx2 v[192:193], v[146:147], off offset:384
	v_lshlrev_b32_e32 v146, 8, v167
	v_and_b32_e32 v202, 0x7ff00, v146
	v_lshl_add_u64 v[146:147], s[8:9], 0, v[202:203]
	v_lshl_add_u64 v[150:151], s[16:17], 0, v[202:203]
	v_lshl_add_u64 v[146:147], v[146:147], 0, v[172:173]
	v_lshl_add_u64 v[150:151], v[150:151], 0, v[172:173]
	s_waitcnt vmcnt(4)
	v_mov_b32_e32 v148, v246
	v_mov_b32_e32 v149, v247
	v_lshl_add_u64 v[246:247], v[146:147], 0, s[98:99]
	v_mov_b32_e32 v146, v244
	v_mov_b32_e32 v147, v245
	global_load_dwordx4 v[244:247], v[246:247], off
	v_lshl_add_u32 v157, v157, 5, s21
	v_mov_b32_e32 v152, v252
	v_mov_b32_e32 v153, v253
	v_lshl_add_u64 v[252:253], v[150:151], 0, s[98:99]
	v_mov_b32_e32 v150, v250
	v_mov_b32_e32 v151, v251
	global_load_dwordx4 v[250:253], v[252:253], off
	ds_read_b128 v[210:213], v157
	s_waitcnt lgkmcnt(0)
	v_mov_b32_e32 v192, v211
	v_mov_b32_e32 v193, v212
	v_mov_b32_e32 v211, v213
	v_pk_add_f32 v[192:193], v[192:193], v[210:211]
	v_mov_b64_e32 v[212:213], v[112:113]
	v_add_f32_e32 v169, v192, v193
	v_fmamk_f32 v169, v169, 0x3c000000, v235
	v_cmp_gt_f32_e32 vcc, s63, v169
	v_mul_f32_e32 v171, 0x4f800000, v169
	v_mov_b64_e32 v[210:211], v[110:111]
	v_cndmask_b32_e32 v169, v169, v171, vcc
	v_sqrt_f32_e32 v171, v169
	s_nop 0
	v_cvt_f32_i32_e32 v193, v213
	v_add_u32_e32 v175, -1, v171
	v_fma_f32 v181, -v175, v171, v169
	v_cmp_ge_f32_e64 s[0:1], 0, v181
	v_add_u32_e32 v181, 1, v171
	v_cvt_f32_i32_e32 v192, v212
	v_cndmask_b32_e64 v175, v171, v175, s[0:1]
	v_fma_f32 v171, -v181, v171, v169
	v_cmp_lt_f32_e64 s[0:1], 0, v171
	v_cvt_f32_i32_e32 v213, v215
	v_cvt_f32_i32_e32 v212, v214
	v_cndmask_b32_e64 v171, v175, v181, s[0:1]
	v_mul_f32_e32 v175, 0x37800000, v171
	v_cndmask_b32_e32 v171, v171, v175, vcc
	v_cmp_class_f32_e32 vcc, v169, v236
	v_cvt_f32_i32_e32 v215, v217
	v_cvt_f32_i32_e32 v214, v216
	v_cndmask_b32_e32 v169, v171, v169, vcc
	v_div_scale_f32 v171, s[0:1], v169, v169, 1.0
	v_rcp_f32_e32 v175, v171
	v_cvt_f32_i32_e32 v211, v211
	v_cvt_f32_i32_e32 v210, v210
	v_fma_f32 v181, -v171, v175, 1.0
	v_fmac_f32_e32 v175, v181, v175
	v_div_scale_f32 v181, vcc, 1.0, v169, 1.0
	v_mul_f32_e32 v183, v181, v175
	v_fma_f32 v185, -v171, v183, v181
	v_fmac_f32_e32 v183, v185, v175
	v_fma_f32 v171, -v171, v183, v181
	v_div_fmas_f32 v171, v171, v175, v183
	v_div_fixup_f32 v169, v171, v169, 1.0
	v_mul_f32_e32 v202, v186, v169
	v_pk_mul_f32 v[214:215], v[202:203], v[214:215] op_sel_hi:[0,1]
	v_pk_mul_f32 v[212:213], v[202:203], v[212:213] op_sel_hi:[0,1]
	v_pk_mul_f32 v[210:211], v[202:203], v[210:211] op_sel_hi:[0,1]
	v_pk_mul_f32 v[192:193], v[202:203], v[192:193] op_sel_hi:[0,1]
	v_pk_mul_f32 v[212:213], v[122:123], v[212:213]
	v_pk_mul_f32 v[214:215], v[124:125], v[214:215]
	v_pk_mul_f32 v[192:193], v[128:129], v[192:193]
	v_pk_mul_f32 v[210:211], v[126:127], v[210:211]
	v_pk_mul_f32 v[216:217], v[152:153], v[214:215]
	v_pk_mul_f32 v[240:241], v[150:151], v[212:213]
	v_pk_fma_f32 v[216:217], v[148:149], v[192:193], v[216:217] neg_lo:[0,0,1] neg_hi:[0,0,1]
	v_pk_fma_f32 v[240:241], v[146:147], v[210:211], v[240:241] neg_lo:[0,0,1] neg_hi:[0,0,1]
	v_pk_mul_f32 v[192:193], v[152:153], v[192:193]
	v_pk_mul_f32 v[210:211], v[150:151], v[210:211]
	v_pk_fma_f32 v[192:193], v[148:149], v[214:215], v[192:193]
	v_pk_fma_f32 v[210:211], v[146:147], v[212:213], v[210:211]
	v_mad_i64_i32 v[212:213], s[0:1], v167, s64, v[176:177]
	v_pk_add_f32 v[136:137], v[136:137], v[216:217]
	v_pk_add_f32 v[134:135], v[134:135], v[240:241]
	v_pk_add_f32 v[132:133], v[132:133], v[192:193]
	v_pk_add_f32 v[130:131], v[130:131], v[210:211]
	v_lshl_add_u64 v[212:213], v[212:213], 0, s[2:3]
	v_lshl_add_u64 v[242:243], v[212:213], 0, v[178:179]
	v_cvt_pk_bf16_f32 v212, v240, v241
	v_cvt_pk_bf16_f32 v213, v216, v217
	v_cvt_pk_bf16_f32 v210, v210, v211
	v_cvt_pk_bf16_f32 v211, v192, v193
	global_store_dwordx2 v[242:243], v[212:213], off
	global_store_dwordx2 v[242:243], v[210:211], off offset:128
	ds_read_b128 v[210:213], v157 offset:16
	v_mov_b64_e32 v[216:217], v[104:105]
	v_mov_b64_e32 v[214:215], v[102:103]
	s_waitcnt lgkmcnt(0)
	v_mov_b32_e32 v192, v211
	v_mov_b32_e32 v193, v212
	v_mov_b32_e32 v211, v213
	v_pk_add_f32 v[192:193], v[192:193], v[210:211]
	v_mov_b64_e32 v[212:213], v[100:101]
	v_add_f32_e32 v157, v192, v193
	v_fmamk_f32 v157, v157, 0x3c000000, v235
	v_cmp_gt_f32_e32 vcc, s63, v157
	v_mul_f32_e32 v167, 0x4f800000, v157
	v_mov_b64_e32 v[210:211], v[98:99]
	v_cndmask_b32_e32 v157, v157, v167, vcc
	v_sqrt_f32_e32 v167, v157
	s_nop 0
	v_cvt_f32_i32_e32 v193, v217
	v_add_u32_e32 v169, -1, v167
	v_fma_f32 v171, -v169, v167, v157
	v_cmp_ge_f32_e64 s[0:1], 0, v171
	v_add_u32_e32 v171, 1, v167
	v_cvt_f32_i32_e32 v192, v216
	v_cndmask_b32_e64 v169, v167, v169, s[0:1]
	v_fma_f32 v167, -v171, v167, v157
	v_cmp_lt_f32_e64 s[0:1], 0, v167
	v_cvt_f32_i32_e32 v215, v215
	v_cvt_f32_i32_e32 v214, v214
	v_cndmask_b32_e64 v167, v169, v171, s[0:1]
	v_mul_f32_e32 v169, 0x37800000, v167
	v_cndmask_b32_e32 v167, v167, v169, vcc
	v_cmp_class_f32_e32 vcc, v157, v236
	v_cvt_f32_i32_e32 v211, v211
	v_cvt_f32_i32_e32 v210, v210
	v_cndmask_b32_e32 v157, v167, v157, vcc
	v_div_scale_f32 v167, s[0:1], v157, v157, 1.0
	v_rcp_f32_e32 v169, v167
	v_cvt_f32_i32_e32 v213, v213
	v_cvt_f32_i32_e32 v212, v212
	v_fma_f32 v171, -v167, v169, 1.0
	v_fmac_f32_e32 v169, v171, v169
	v_div_scale_f32 v171, vcc, 1.0, v157, 1.0
	v_mul_f32_e32 v175, v171, v169
	v_fma_f32 v181, -v167, v175, v171
	v_fmac_f32_e32 v175, v181, v169
	v_fma_f32 v167, -v167, v175, v171
	v_div_fmas_f32 v167, v167, v169, v175
	v_div_fixup_f32 v157, v167, v157, 1.0
	v_mul_f32_e32 v186, v186, v157
	v_pk_mul_f32 v[214:215], v[186:187], v[214:215] op_sel_hi:[0,1]
	v_pk_mul_f32 v[192:193], v[186:187], v[192:193] op_sel_hi:[0,1]
	v_pk_mul_f32 v[212:213], v[186:187], v[212:213] op_sel_hi:[0,1]
	v_pk_mul_f32 v[186:187], v[186:187], v[210:211] op_sel_hi:[0,1]
	v_pk_mul_f32 v[192:193], v[128:129], v[192:193]
	v_pk_mul_f32 v[214:215], v[126:127], v[214:215]
	v_pk_mul_f32 v[186:187], v[122:123], v[186:187]
	v_pk_mul_f32 v[210:211], v[124:125], v[212:213]
	v_pk_mul_f32 v[216:217], v[150:151], v[186:187]
	v_pk_mul_f32 v[212:213], v[152:153], v[210:211]
	v_pk_mul_f32 v[152:153], v[152:153], v[192:193]
	v_pk_mul_f32 v[150:151], v[150:151], v[214:215]
	v_pk_fma_f32 v[216:217], v[146:147], v[214:215], v[216:217] neg_lo:[0,0,1] neg_hi:[0,0,1]
	v_pk_fma_f32 v[212:213], v[148:149], v[192:193], v[212:213] neg_lo:[0,0,1] neg_hi:[0,0,1]
	v_pk_fma_f32 v[146:147], v[146:147], v[186:187], v[150:151]
	v_pk_fma_f32 v[148:149], v[148:149], v[210:211], v[152:153]
	v_pk_add_f32 v[144:145], v[144:145], v[212:213]
	v_pk_add_f32 v[142:143], v[142:143], v[216:217]
	v_pk_add_f32 v[140:141], v[140:141], v[148:149]
	v_pk_add_f32 v[138:139], v[138:139], v[146:147]
	v_add_u32_e32 v157, 32, v190
	v_cvt_pk_bf16_f32 v150, v216, v217
	v_cvt_pk_bf16_f32 v151, v212, v213
	v_cvt_pk_bf16_f32 v146, v146, v147
	v_add_u32_e32 v167, s19, v157
	v_cvt_pk_bf16_f32 v147, v148, v149
	global_store_dwordx2 v[242:243], v[150:151], off offset:256
	global_store_dwordx2 v[242:243], v[146:147], off offset:384
	v_lshlrev_b32_e32 v146, 8, v167
	v_and_b32_e32 v202, 0x7ff00, v146
	v_lshl_add_u64 v[146:147], s[8:9], 0, v[202:203]
	v_lshl_add_u64 v[150:151], s[16:17], 0, v[202:203]
	v_lshl_add_u64 v[146:147], v[146:147], 0, v[172:173]
	v_lshl_add_u64 v[150:151], v[150:151], 0, v[172:173]
	s_waitcnt vmcnt(4)
	v_mov_b32_e32 v148, v246
	v_mov_b32_e32 v149, v247
	v_lshl_add_u64 v[246:247], v[146:147], 0, s[98:99]
	v_mov_b32_e32 v146, v244
	v_mov_b32_e32 v147, v245
	global_load_dwordx4 v[244:247], v[246:247], off
	v_lshl_add_u32 v157, v157, 5, s21
	v_mov_b32_e32 v152, v252
	v_mov_b32_e32 v153, v253
	v_lshl_add_u64 v[252:253], v[150:151], 0, s[98:99]
	v_mov_b32_e32 v150, v250
	v_mov_b32_e32 v151, v251
	global_load_dwordx4 v[250:253], v[252:253], off
	ds_read_b128 v[210:213], v157
	v_mov_b64_e32 v[216:217], v[96:97]
	v_mov_b64_e32 v[214:215], v[94:95]
	s_waitcnt lgkmcnt(0)
	v_mov_b32_e32 v186, v211
	v_mov_b32_e32 v187, v212
	v_mov_b32_e32 v211, v213
	v_pk_add_f32 v[186:187], v[186:187], v[210:211]
	v_mov_b64_e32 v[212:213], v[92:93]
	v_add_f32_e32 v169, v186, v187
	v_fmamk_f32 v169, v169, 0x3c000000, v235
	v_cmp_gt_f32_e32 vcc, s63, v169
	v_mul_f32_e32 v171, 0x4f800000, v169
	v_mov_b64_e32 v[210:211], v[90:91]
	v_cndmask_b32_e32 v169, v169, v171, vcc
	v_sqrt_f32_e32 v171, v169
	s_nop 0
	v_cvt_f32_i32_e32 v211, v211
	v_add_u32_e32 v175, -1, v171
	v_fma_f32 v181, -v175, v171, v169
	v_cmp_ge_f32_e64 s[0:1], 0, v181
	v_add_u32_e32 v181, 1, v171
	v_cvt_f32_i32_e32 v210, v210
	v_cndmask_b32_e64 v175, v171, v175, s[0:1]
	v_fma_f32 v171, -v181, v171, v169
	v_cmp_lt_f32_e64 s[0:1], 0, v171
	v_cvt_f32_i32_e32 v213, v213
	v_cvt_f32_i32_e32 v212, v212
	v_cndmask_b32_e64 v171, v175, v181, s[0:1]
	v_mul_f32_e32 v175, 0x37800000, v171
	v_cndmask_b32_e32 v171, v171, v175, vcc
	v_cmp_class_f32_e32 vcc, v169, v236
	v_cvt_f32_i32_e32 v187, v217
	v_cvt_f32_i32_e32 v186, v216
	v_cndmask_b32_e32 v169, v171, v169, vcc
	v_div_scale_f32 v171, s[0:1], v169, v169, 1.0
	v_rcp_f32_e32 v175, v171
	v_cvt_f32_i32_e32 v193, v215
	v_cvt_f32_i32_e32 v192, v214
	v_fma_f32 v181, -v171, v175, 1.0
	v_fmac_f32_e32 v175, v181, v175
	v_div_scale_f32 v181, vcc, 1.0, v169, 1.0
	v_mul_f32_e32 v183, v181, v175
	v_fma_f32 v185, -v171, v183, v181
	v_fmac_f32_e32 v183, v185, v175
	v_fma_f32 v171, -v171, v183, v181
	v_div_fmas_f32 v171, v171, v175, v183
	v_div_fixup_f32 v169, v171, v169, 1.0
	v_mul_f32_e32 v202, v184, v169
	v_pk_mul_f32 v[212:213], v[202:203], v[212:213] op_sel_hi:[0,1]
	v_pk_mul_f32 v[210:211], v[202:203], v[210:211] op_sel_hi:[0,1]
	v_pk_mul_f32 v[192:193], v[202:203], v[192:193] op_sel_hi:[0,1]
	v_pk_mul_f32 v[186:187], v[202:203], v[186:187] op_sel_hi:[0,1]
	v_pk_mul_f32 v[210:211], v[122:123], v[210:211]
	v_pk_mul_f32 v[212:213], v[124:125], v[212:213]
	v_pk_mul_f32 v[186:187], v[128:129], v[186:187]
	v_pk_mul_f32 v[192:193], v[126:127], v[192:193]
	v_pk_mul_f32 v[214:215], v[152:153], v[212:213]
	v_pk_mul_f32 v[216:217], v[150:151], v[210:211]
	v_pk_fma_f32 v[214:215], v[148:149], v[186:187], v[214:215] neg_lo:[0,0,1] neg_hi:[0,0,1]
	v_pk_fma_f32 v[216:217], v[146:147], v[192:193], v[216:217] neg_lo:[0,0,1] neg_hi:[0,0,1]
	v_pk_mul_f32 v[186:187], v[152:153], v[186:187]
	v_pk_mul_f32 v[192:193], v[150:151], v[192:193]
	v_pk_fma_f32 v[186:187], v[148:149], v[212:213], v[186:187]
	v_pk_fma_f32 v[192:193], v[146:147], v[210:211], v[192:193]
	v_mad_i64_i32 v[210:211], s[0:1], v167, s64, v[176:177]
	v_pk_add_f32 v[136:137], v[136:137], v[214:215]
	v_pk_add_f32 v[134:135], v[134:135], v[216:217]
	v_pk_add_f32 v[132:133], v[132:133], v[186:187]
	v_pk_add_f32 v[130:131], v[130:131], v[192:193]
	v_lshl_add_u64 v[210:211], v[210:211], 0, s[2:3]
	v_lshl_add_u64 v[240:241], v[210:211], 0, v[178:179]
	v_cvt_pk_bf16_f32 v210, v216, v217
	v_cvt_pk_bf16_f32 v211, v214, v215
	v_cvt_pk_bf16_f32 v192, v192, v193
	v_cvt_pk_bf16_f32 v193, v186, v187
	global_store_dwordx2 v[240:241], v[210:211], off
	global_store_dwordx2 v[240:241], v[192:193], off offset:128
	ds_read_b128 v[210:213], v157 offset:16
	v_mov_b64_e32 v[216:217], v[84:85]
	v_mov_b64_e32 v[214:215], v[82:83]
	s_waitcnt lgkmcnt(0)
	v_mov_b32_e32 v186, v211
	v_mov_b32_e32 v187, v212
	v_mov_b32_e32 v211, v213
	v_pk_add_f32 v[186:187], v[186:187], v[210:211]
	v_mov_b64_e32 v[212:213], v[88:89]
	v_add_f32_e32 v157, v186, v187
	v_fmamk_f32 v157, v157, 0x3c000000, v235
	v_cmp_gt_f32_e32 vcc, s63, v157
	v_mul_f32_e32 v167, 0x4f800000, v157
	v_mov_b64_e32 v[210:211], v[86:87]
	v_cndmask_b32_e32 v157, v157, v167, vcc
	v_sqrt_f32_e32 v167, v157
	s_nop 0
	v_cvt_f32_i32_e32 v187, v213
	v_add_u32_e32 v169, -1, v167
	v_fma_f32 v171, -v169, v167, v157
	v_cmp_ge_f32_e64 s[0:1], 0, v171
	v_add_u32_e32 v171, 1, v167
	v_cvt_f32_i32_e32 v186, v212
	v_cndmask_b32_e64 v169, v167, v169, s[0:1]
	v_fma_f32 v167, -v171, v167, v157
	v_cmp_lt_f32_e64 s[0:1], 0, v167
	v_cvt_f32_i32_e32 v193, v211
	v_cvt_f32_i32_e32 v192, v210
	v_cndmask_b32_e64 v167, v169, v171, s[0:1]
	v_mul_f32_e32 v169, 0x37800000, v167
	v_cndmask_b32_e32 v167, v167, v169, vcc
	v_cmp_class_f32_e32 vcc, v157, v236
	v_cvt_f32_i32_e32 v211, v215
	v_cvt_f32_i32_e32 v210, v214
	v_cndmask_b32_e32 v157, v167, v157, vcc
	v_div_scale_f32 v167, s[0:1], v157, v157, 1.0
	v_rcp_f32_e32 v169, v167
	v_cvt_f32_i32_e32 v213, v217
	v_cvt_f32_i32_e32 v212, v216
	v_fma_f32 v171, -v167, v169, 1.0
	v_fmac_f32_e32 v169, v171, v169
	v_div_scale_f32 v171, vcc, 1.0, v157, 1.0
	v_mul_f32_e32 v175, v171, v169
	v_fma_f32 v181, -v167, v175, v171
	v_fmac_f32_e32 v175, v181, v169
	v_fma_f32 v167, -v167, v175, v171
	v_div_fmas_f32 v167, v167, v169, v175
	v_div_fixup_f32 v157, v167, v157, 1.0
	v_mul_f32_e32 v184, v184, v157
	v_pk_mul_f32 v[192:193], v[184:185], v[192:193] op_sel_hi:[0,1]
	v_pk_mul_f32 v[186:187], v[184:185], v[186:187] op_sel_hi:[0,1]
	v_pk_mul_f32 v[212:213], v[184:185], v[212:213] op_sel_hi:[0,1]
	v_pk_mul_f32 v[184:185], v[184:185], v[210:211] op_sel_hi:[0,1]
	v_pk_mul_f32 v[186:187], v[128:129], v[186:187]
	v_pk_mul_f32 v[192:193], v[126:127], v[192:193]
	v_pk_mul_f32 v[184:185], v[122:123], v[184:185]
	v_pk_mul_f32 v[210:211], v[124:125], v[212:213]
	v_pk_mul_f32 v[214:215], v[150:151], v[184:185]
	v_pk_mul_f32 v[212:213], v[152:153], v[210:211]
	v_pk_mul_f32 v[152:153], v[152:153], v[186:187]
	v_pk_mul_f32 v[150:151], v[150:151], v[192:193]
	v_pk_fma_f32 v[214:215], v[146:147], v[192:193], v[214:215] neg_lo:[0,0,1] neg_hi:[0,0,1]
	v_pk_fma_f32 v[212:213], v[148:149], v[186:187], v[212:213] neg_lo:[0,0,1] neg_hi:[0,0,1]
	v_pk_fma_f32 v[146:147], v[146:147], v[184:185], v[150:151]
	v_pk_fma_f32 v[148:149], v[148:149], v[210:211], v[152:153]
	v_pk_add_f32 v[144:145], v[144:145], v[212:213]
	v_pk_add_f32 v[142:143], v[142:143], v[214:215]
	v_pk_add_f32 v[140:141], v[140:141], v[148:149]
	v_pk_add_f32 v[138:139], v[138:139], v[146:147]
	v_add_u32_e32 v157, 48, v190
	v_cvt_pk_bf16_f32 v150, v214, v215
	v_cvt_pk_bf16_f32 v151, v212, v213
	v_cvt_pk_bf16_f32 v146, v146, v147
	v_add_u32_e32 v167, s19, v157
	v_cvt_pk_bf16_f32 v147, v148, v149
	global_store_dwordx2 v[240:241], v[150:151], off offset:256
	global_store_dwordx2 v[240:241], v[146:147], off offset:384
	v_lshlrev_b32_e32 v146, 8, v167
	v_and_b32_e32 v202, 0x7ff00, v146
	v_lshl_add_u64 v[146:147], s[8:9], 0, v[202:203]
	v_lshl_add_u64 v[150:151], s[16:17], 0, v[202:203]
	v_lshl_add_u64 v[146:147], v[146:147], 0, v[172:173]
	v_lshl_add_u64 v[150:151], v[150:151], 0, v[172:173]
	s_waitcnt vmcnt(4)
	v_mov_b32_e32 v148, v246
	v_mov_b32_e32 v149, v247
	v_lshl_add_u64 v[246:247], v[146:147], 0, s[100:101]
	v_mov_b32_e32 v146, v244
	v_mov_b32_e32 v147, v245
	global_load_dwordx4 v[244:247], v[246:247], off
	v_lshl_add_u32 v157, v157, 5, s21
	v_mov_b32_e32 v152, v252
	v_mov_b32_e32 v153, v253
	v_lshl_add_u64 v[252:253], v[150:151], 0, s[100:101]
	v_mov_b32_e32 v150, v250
	v_mov_b32_e32 v151, v251
	global_load_dwordx4 v[250:253], v[252:253], off
	ds_read_b128 v[184:187], v157
	v_mov_b64_e32 v[212:213], v[80:81]
	v_mov_b64_e32 v[210:211], v[78:79]
	s_waitcnt lgkmcnt(0)
	v_mov_b32_e32 v192, v185
	v_mov_b32_e32 v193, v186
	v_mov_b32_e32 v185, v187
	v_pk_add_f32 v[184:185], v[192:193], v[184:185]
	s_nop 0
	v_add_f32_e32 v169, v184, v185
	v_fmamk_f32 v169, v169, 0x3c000000, v235
	v_cmp_gt_f32_e32 vcc, s63, v169
	v_mul_f32_e32 v171, 0x4f800000, v169
	s_nop 0
	v_cndmask_b32_e32 v169, v169, v171, vcc
	v_sqrt_f32_e32 v171, v169
	s_nop 0
	v_add_u32_e32 v175, -1, v171
	v_fma_f32 v181, -v175, v171, v169
	v_cmp_ge_f32_e64 s[0:1], 0, v181
	v_add_u32_e32 v181, 1, v171
	s_nop 0
	v_cndmask_b32_e64 v175, v171, v175, s[0:1]
	v_fma_f32 v171, -v181, v171, v169
	v_cmp_lt_f32_e64 s[0:1], 0, v171
	s_nop 1
	v_cndmask_b32_e64 v171, v175, v181, s[0:1]
	v_mul_f32_e32 v175, 0x37800000, v171
	v_cndmask_b32_e32 v171, v171, v175, vcc
	v_cmp_class_f32_e32 vcc, v169, v236
	s_nop 1
	v_cndmask_b32_e32 v169, v171, v169, vcc
	v_div_scale_f32 v171, s[0:1], v169, v169, 1.0
	v_rcp_f32_e32 v175, v171
	s_nop 0
	v_fma_f32 v181, -v171, v175, 1.0
	v_fmac_f32_e32 v175, v181, v175
	v_div_scale_f32 v181, vcc, 1.0, v169, 1.0
	v_mul_f32_e32 v183, v181, v175
	v_fma_f32 v184, -v171, v183, v181
	v_fmac_f32_e32 v183, v184, v175
	v_mov_b64_e32 v[186:187], v[76:77]
	v_mov_b64_e32 v[184:185], v[74:75]
	v_fma_f32 v171, -v171, v183, v181
	v_cvt_f32_i32_e32 v185, v185
	v_cvt_f32_i32_e32 v184, v184
	v_cvt_f32_i32_e32 v187, v187
	v_cvt_f32_i32_e32 v186, v186
	v_div_fmas_f32 v171, v171, v175, v183
	v_cvt_f32_i32_e32 v193, v213
	v_cvt_f32_i32_e32 v192, v212
	v_cvt_f32_i32_e32 v211, v211
	v_cvt_f32_i32_e32 v210, v210
	v_div_fixup_f32 v169, v171, v169, 1.0
	v_mul_f32_e32 v202, v182, v169
	v_pk_mul_f32 v[186:187], v[202:203], v[186:187] op_sel_hi:[0,1]
	v_pk_mul_f32 v[184:185], v[202:203], v[184:185] op_sel_hi:[0,1]
	v_pk_mul_f32 v[210:211], v[202:203], v[210:211] op_sel_hi:[0,1]
	v_pk_mul_f32 v[192:193], v[202:203], v[192:193] op_sel_hi:[0,1]
	v_pk_mul_f32 v[184:185], v[122:123], v[184:185]
	v_pk_mul_f32 v[186:187], v[124:125], v[186:187]
	v_pk_mul_f32 v[192:193], v[128:129], v[192:193]
	v_pk_mul_f32 v[210:211], v[126:127], v[210:211]
	v_pk_mul_f32 v[212:213], v[152:153], v[186:187]
	v_pk_mul_f32 v[214:215], v[150:151], v[184:185]
	v_pk_fma_f32 v[212:213], v[148:149], v[192:193], v[212:213] neg_lo:[0,0,1] neg_hi:[0,0,1]
	v_pk_fma_f32 v[214:215], v[146:147], v[210:211], v[214:215] neg_lo:[0,0,1] neg_hi:[0,0,1]
	v_pk_mul_f32 v[192:193], v[152:153], v[192:193]
	v_pk_mul_f32 v[210:211], v[150:151], v[210:211]
	v_pk_fma_f32 v[186:187], v[148:149], v[186:187], v[192:193]
	v_pk_fma_f32 v[184:185], v[146:147], v[184:185], v[210:211]
	v_mad_i64_i32 v[192:193], s[0:1], v167, s64, v[176:177]
	v_pk_add_f32 v[136:137], v[136:137], v[212:213]
	v_pk_add_f32 v[134:135], v[134:135], v[214:215]
	v_pk_add_f32 v[132:133], v[132:133], v[186:187]
	v_pk_add_f32 v[130:131], v[130:131], v[184:185]
	v_lshl_add_u64 v[192:193], v[192:193], 0, s[2:3]
	v_lshl_add_u64 v[192:193], v[192:193], 0, v[178:179]
	v_cvt_pk_bf16_f32 v210, v214, v215
	v_cvt_pk_bf16_f32 v211, v212, v213
	v_cvt_pk_bf16_f32 v184, v184, v185
	v_cvt_pk_bf16_f32 v185, v186, v187
	global_store_dwordx2 v[192:193], v[210:211], off
	global_store_dwordx2 v[192:193], v[184:185], off offset:128
	ds_read_b128 v[184:187], v157 offset:16
	s_waitcnt lgkmcnt(0)
	v_mov_b32_e32 v210, v185
	v_mov_b32_e32 v211, v186
	v_mov_b32_e32 v185, v187
	v_pk_add_f32 v[184:185], v[210:211], v[184:185]
	v_mov_b64_e32 v[212:213], v[68:69]
	v_add_f32_e32 v157, v184, v185
	v_fmamk_f32 v157, v157, 0x3c000000, v235
	v_cmp_gt_f32_e32 vcc, s63, v157
	v_mul_f32_e32 v167, 0x4f800000, v157
	v_mov_b64_e32 v[186:187], v[72:73]
	v_cndmask_b32_e32 v157, v157, v167, vcc
	v_sqrt_f32_e32 v167, v157
	v_mov_b64_e32 v[184:185], v[70:71]
	v_mov_b64_e32 v[210:211], v[66:67]
	v_add_u32_e32 v169, -1, v167
	v_fma_f32 v171, -v169, v167, v157
	v_cmp_ge_f32_e64 s[0:1], 0, v171
	v_add_u32_e32 v171, 1, v167
	v_cvt_f32_i32_e32 v187, v187
	v_cndmask_b32_e64 v169, v167, v169, s[0:1]
	v_fma_f32 v167, -v171, v167, v157
	v_cmp_lt_f32_e64 s[0:1], 0, v167
	v_cvt_f32_i32_e32 v186, v186
	v_cvt_f32_i32_e32 v185, v185
	v_cndmask_b32_e64 v167, v169, v171, s[0:1]
	v_mul_f32_e32 v169, 0x37800000, v167
	v_cndmask_b32_e32 v167, v167, v169, vcc
	v_cmp_class_f32_e32 vcc, v157, v236
	v_cvt_f32_i32_e32 v184, v184
	v_cvt_f32_i32_e32 v211, v211
	v_cndmask_b32_e32 v157, v167, v157, vcc
	v_div_scale_f32 v167, s[0:1], v157, v157, 1.0
	v_rcp_f32_e32 v169, v167
	v_cvt_f32_i32_e32 v210, v210
	v_cvt_f32_i32_e32 v213, v213
	v_cvt_f32_i32_e32 v212, v212
	v_fma_f32 v171, -v167, v169, 1.0
	v_fmac_f32_e32 v169, v171, v169
	v_div_scale_f32 v171, vcc, 1.0, v157, 1.0
	v_mul_f32_e32 v175, v171, v169
	v_fma_f32 v181, -v167, v175, v171
	v_fmac_f32_e32 v175, v181, v169
	v_fma_f32 v167, -v167, v175, v171
	v_div_fmas_f32 v167, v167, v169, v175
	v_div_fixup_f32 v157, v167, v157, 1.0
	v_mul_f32_e32 v182, v182, v157
	v_pk_mul_f32 v[184:185], v[182:183], v[184:185] op_sel_hi:[0,1]
	v_pk_mul_f32 v[186:187], v[182:183], v[186:187] op_sel_hi:[0,1]
	v_pk_mul_f32 v[212:213], v[182:183], v[212:213] op_sel_hi:[0,1]
	v_pk_mul_f32 v[182:183], v[182:183], v[210:211] op_sel_hi:[0,1]
	v_pk_mul_f32 v[186:187], v[128:129], v[186:187]
	v_pk_mul_f32 v[184:185], v[126:127], v[184:185]
	v_pk_mul_f32 v[182:183], v[122:123], v[182:183]
	v_pk_mul_f32 v[210:211], v[124:125], v[212:213]
	v_pk_mul_f32 v[214:215], v[150:151], v[182:183]
	v_pk_mul_f32 v[212:213], v[152:153], v[210:211]
	v_pk_mul_f32 v[152:153], v[152:153], v[186:187]
	v_pk_mul_f32 v[150:151], v[150:151], v[184:185]
	v_pk_fma_f32 v[214:215], v[146:147], v[184:185], v[214:215] neg_lo:[0,0,1] neg_hi:[0,0,1]
	v_pk_fma_f32 v[212:213], v[148:149], v[186:187], v[212:213] neg_lo:[0,0,1] neg_hi:[0,0,1]
	v_pk_fma_f32 v[146:147], v[146:147], v[182:183], v[150:151]
	v_pk_fma_f32 v[148:149], v[148:149], v[210:211], v[152:153]
	v_pk_add_f32 v[144:145], v[144:145], v[212:213]
	v_pk_add_f32 v[142:143], v[142:143], v[214:215]
	v_pk_add_f32 v[140:141], v[140:141], v[148:149]
	v_pk_add_f32 v[138:139], v[138:139], v[146:147]
	v_add_u32_e32 v157, 0x80, v190
	v_cvt_pk_bf16_f32 v150, v214, v215
	v_cvt_pk_bf16_f32 v151, v212, v213
	v_cvt_pk_bf16_f32 v146, v146, v147
	v_add_u32_e32 v167, s19, v157
	v_cvt_pk_bf16_f32 v147, v148, v149
	global_store_dwordx2 v[192:193], v[150:151], off offset:256
	global_store_dwordx2 v[192:193], v[146:147], off offset:384
	v_lshlrev_b32_e32 v146, 8, v167
	v_and_b32_e32 v202, 0x7ff00, v146
	v_lshl_add_u64 v[146:147], s[8:9], 0, v[202:203]
	v_lshl_add_u64 v[150:151], s[16:17], 0, v[202:203]
	v_lshl_add_u64 v[146:147], v[146:147], 0, v[172:173]
	v_lshl_add_u64 v[150:151], v[150:151], 0, v[172:173]
	s_waitcnt vmcnt(4)
	v_mov_b32_e32 v148, v246
	v_mov_b32_e32 v149, v247
	v_lshl_add_u64 v[246:247], v[146:147], 0, s[98:99]
	v_mov_b32_e32 v146, v244
	v_mov_b32_e32 v147, v245
	global_load_dwordx4 v[244:247], v[246:247], off
	v_lshl_add_u32 v157, v157, 5, s21
	v_mov_b32_e32 v152, v252
	v_mov_b32_e32 v153, v253
	v_lshl_add_u64 v[252:253], v[150:151], 0, s[98:99]
	v_mov_b32_e32 v150, v250
	v_mov_b32_e32 v151, v251
	global_load_dwordx4 v[250:253], v[252:253], off
	ds_read_b128 v[182:185], v157
	v_mov_b64_e32 v[212:213], v[64:65]
	v_mov_b64_e32 v[210:211], v[62:63]
	s_waitcnt lgkmcnt(0)
	v_mov_b32_e32 v186, v183
	v_mov_b32_e32 v187, v184
	v_mov_b32_e32 v183, v185
	v_pk_add_f32 v[182:183], v[186:187], v[182:183]
	s_nop 0
	v_add_f32_e32 v169, v182, v183
	v_fmamk_f32 v169, v169, 0x3c000000, v235
	v_cmp_gt_f32_e32 vcc, s63, v169
	v_mul_f32_e32 v171, 0x4f800000, v169
	s_nop 0
	v_cndmask_b32_e32 v169, v169, v171, vcc
	v_sqrt_f32_e32 v171, v169
	s_nop 0
	v_add_u32_e32 v175, -1, v171
	v_fma_f32 v181, -v175, v171, v169
	v_cmp_ge_f32_e64 s[0:1], 0, v181
	v_add_u32_e32 v181, 1, v171
	s_nop 0
	v_cndmask_b32_e64 v175, v171, v175, s[0:1]
	v_fma_f32 v171, -v181, v171, v169
	v_cmp_lt_f32_e64 s[0:1], 0, v171
	s_nop 1
	v_cndmask_b32_e64 v171, v175, v181, s[0:1]
	v_mul_f32_e32 v175, 0x37800000, v171
	v_cndmask_b32_e32 v171, v171, v175, vcc
	v_cmp_class_f32_e32 vcc, v169, v236
	s_nop 1
	v_cndmask_b32_e32 v169, v171, v169, vcc
	v_div_scale_f32 v171, s[0:1], v169, v169, 1.0
	v_rcp_f32_e32 v175, v171
	s_nop 0
	v_fma_f32 v181, -v171, v175, 1.0
	v_fmac_f32_e32 v175, v181, v175
	v_div_scale_f32 v181, vcc, 1.0, v169, 1.0
	v_mul_f32_e32 v182, v181, v175
	v_fma_f32 v183, -v171, v182, v181
	v_fmac_f32_e32 v182, v183, v175
	v_fma_f32 v171, -v171, v182, v181
	v_div_fmas_f32 v171, v171, v175, v182
	v_mov_b64_e32 v[184:185], v[60:61]
	v_mov_b64_e32 v[182:183], v[58:59]
	v_div_fixup_f32 v169, v171, v169, 1.0
	v_cvt_f32_i32_e32 v183, v183
	v_cvt_f32_i32_e32 v182, v182
	v_cvt_f32_i32_e32 v185, v185
	v_cvt_f32_i32_e32 v184, v184
	v_cvt_f32_i32_e32 v187, v213
	v_cvt_f32_i32_e32 v186, v212
	v_cvt_f32_i32_e32 v193, v211
	v_cvt_f32_i32_e32 v192, v210
	v_mul_f32_e32 v202, v180, v169
	v_pk_mul_f32 v[184:185], v[202:203], v[184:185] op_sel_hi:[0,1]
	v_pk_mul_f32 v[182:183], v[202:203], v[182:183] op_sel_hi:[0,1]
	v_pk_mul_f32 v[192:193], v[202:203], v[192:193] op_sel_hi:[0,1]
	v_pk_mul_f32 v[186:187], v[202:203], v[186:187] op_sel_hi:[0,1]
	v_pk_mul_f32 v[182:183], v[122:123], v[182:183]
	v_pk_mul_f32 v[184:185], v[124:125], v[184:185]
	v_pk_mul_f32 v[186:187], v[128:129], v[186:187]
	v_pk_mul_f32 v[192:193], v[126:127], v[192:193]
	v_pk_mul_f32 v[210:211], v[152:153], v[184:185]
	v_pk_mul_f32 v[212:213], v[150:151], v[182:183]
	v_pk_fma_f32 v[210:211], v[148:149], v[186:187], v[210:211] neg_lo:[0,0,1] neg_hi:[0,0,1]
	v_pk_fma_f32 v[212:213], v[146:147], v[192:193], v[212:213] neg_lo:[0,0,1] neg_hi:[0,0,1]
	v_pk_mul_f32 v[186:187], v[152:153], v[186:187]
	v_pk_mul_f32 v[192:193], v[150:151], v[192:193]
	v_pk_fma_f32 v[184:185], v[148:149], v[184:185], v[186:187]
	v_pk_fma_f32 v[182:183], v[146:147], v[182:183], v[192:193]
	v_mad_i64_i32 v[186:187], s[0:1], v167, s64, v[176:177]
	v_pk_add_f32 v[136:137], v[136:137], v[210:211]
	v_pk_add_f32 v[134:135], v[134:135], v[212:213]
	v_pk_add_f32 v[132:133], v[132:133], v[184:185]
	v_pk_add_f32 v[130:131], v[130:131], v[182:183]
	v_lshl_add_u64 v[186:187], v[186:187], 0, s[2:3]
	v_lshl_add_u64 v[186:187], v[186:187], 0, v[178:179]
	v_cvt_pk_bf16_f32 v192, v212, v213
	v_cvt_pk_bf16_f32 v193, v210, v211
	v_cvt_pk_bf16_f32 v182, v182, v183
	v_cvt_pk_bf16_f32 v183, v184, v185
	global_store_dwordx2 v[186:187], v[192:193], off
	global_store_dwordx2 v[186:187], v[182:183], off offset:128
	ds_read_b128 v[182:185], v157 offset:16
	v_mov_b64_e32 v[212:213], v[52:53]
	v_mov_b64_e32 v[210:211], v[50:51]
	s_waitcnt lgkmcnt(0)
	v_mov_b32_e32 v192, v183
	v_mov_b32_e32 v193, v184
	v_mov_b32_e32 v183, v185
	v_pk_add_f32 v[182:183], v[192:193], v[182:183]
	s_nop 0
	v_add_f32_e32 v157, v182, v183
	v_fmamk_f32 v157, v157, 0x3c000000, v235
	v_cmp_gt_f32_e32 vcc, s63, v157
	v_mul_f32_e32 v167, 0x4f800000, v157
	v_mov_b64_e32 v[184:185], v[56:57]
	v_cndmask_b32_e32 v157, v157, v167, vcc
	v_sqrt_f32_e32 v167, v157
	v_mov_b64_e32 v[182:183], v[54:55]
	v_add_u32_e32 v169, -1, v167
	v_fma_f32 v171, -v169, v167, v157
	v_cmp_ge_f32_e64 s[0:1], 0, v171
	v_add_u32_e32 v171, 1, v167
	v_cvt_f32_i32_e32 v185, v185
	v_cndmask_b32_e64 v169, v167, v169, s[0:1]
	v_fma_f32 v167, -v171, v167, v157
	v_cmp_lt_f32_e64 s[0:1], 0, v167
	v_cvt_f32_i32_e32 v184, v184
	v_cvt_f32_i32_e32 v183, v183
	v_cndmask_b32_e64 v167, v169, v171, s[0:1]
	v_mul_f32_e32 v169, 0x37800000, v167
	v_cndmask_b32_e32 v167, v167, v169, vcc
	v_cmp_class_f32_e32 vcc, v157, v236
	v_cvt_f32_i32_e32 v182, v182
	v_cvt_f32_i32_e32 v193, v211
	v_cndmask_b32_e32 v157, v167, v157, vcc
	v_div_scale_f32 v167, s[0:1], v157, v157, 1.0
	v_rcp_f32_e32 v169, v167
	v_cvt_f32_i32_e32 v192, v210
	v_cvt_f32_i32_e32 v211, v213
	v_cvt_f32_i32_e32 v210, v212
	v_fma_f32 v171, -v167, v169, 1.0
	v_fmac_f32_e32 v169, v171, v169
	v_div_scale_f32 v171, vcc, 1.0, v157, 1.0
	v_mul_f32_e32 v175, v171, v169
	v_fma_f32 v181, -v167, v175, v171
	v_fmac_f32_e32 v175, v181, v169
	v_fma_f32 v167, -v167, v175, v171
	v_div_fmas_f32 v167, v167, v169, v175
	v_div_fixup_f32 v157, v167, v157, 1.0
	v_mul_f32_e32 v180, v180, v157
	v_pk_mul_f32 v[182:183], v[180:181], v[182:183] op_sel_hi:[0,1]
	v_pk_mul_f32 v[184:185], v[180:181], v[184:185] op_sel_hi:[0,1]
	v_pk_mul_f32 v[210:211], v[180:181], v[210:211] op_sel_hi:[0,1]
	v_pk_mul_f32 v[180:181], v[180:181], v[192:193] op_sel_hi:[0,1]
	v_pk_mul_f32 v[184:185], v[128:129], v[184:185]
	v_pk_mul_f32 v[182:183], v[126:127], v[182:183]
	v_pk_mul_f32 v[180:181], v[122:123], v[180:181]
	v_pk_mul_f32 v[192:193], v[124:125], v[210:211]
	v_pk_mul_f32 v[212:213], v[150:151], v[180:181]
	v_pk_mul_f32 v[210:211], v[152:153], v[192:193]
	v_pk_mul_f32 v[152:153], v[152:153], v[184:185]
	v_pk_mul_f32 v[150:151], v[150:151], v[182:183]
	v_pk_fma_f32 v[212:213], v[146:147], v[182:183], v[212:213] neg_lo:[0,0,1] neg_hi:[0,0,1]
	v_pk_fma_f32 v[210:211], v[148:149], v[184:185], v[210:211] neg_lo:[0,0,1] neg_hi:[0,0,1]
	v_pk_fma_f32 v[146:147], v[146:147], v[180:181], v[150:151]
	v_pk_fma_f32 v[148:149], v[148:149], v[192:193], v[152:153]
	v_pk_add_f32 v[144:145], v[144:145], v[210:211]
	v_pk_add_f32 v[142:143], v[142:143], v[212:213]
	v_pk_add_f32 v[140:141], v[140:141], v[148:149]
	v_pk_add_f32 v[138:139], v[138:139], v[146:147]
	v_add_u32_e32 v157, 0x90, v190
	v_cvt_pk_bf16_f32 v150, v212, v213
	v_cvt_pk_bf16_f32 v151, v210, v211
	v_cvt_pk_bf16_f32 v146, v146, v147
	v_add_u32_e32 v167, s19, v157
	v_cvt_pk_bf16_f32 v147, v148, v149
	global_store_dwordx2 v[186:187], v[150:151], off offset:256
	global_store_dwordx2 v[186:187], v[146:147], off offset:384
	v_lshlrev_b32_e32 v146, 8, v167
	v_and_b32_e32 v202, 0x7ff00, v146
	v_lshl_add_u64 v[146:147], s[8:9], 0, v[202:203]
	v_lshl_add_u64 v[150:151], s[16:17], 0, v[202:203]
	v_lshl_add_u64 v[146:147], v[146:147], 0, v[172:173]
	v_lshl_add_u64 v[150:151], v[150:151], 0, v[172:173]
	s_waitcnt vmcnt(4)
	v_mov_b32_e32 v148, v246
	v_mov_b32_e32 v149, v247
	v_lshl_add_u64 v[246:247], v[146:147], 0, s[98:99]
	v_mov_b32_e32 v146, v244
	v_mov_b32_e32 v147, v245
	global_load_dwordx4 v[244:247], v[246:247], off
	v_lshl_add_u32 v157, v157, 5, s21
	v_mov_b32_e32 v152, v252
	v_mov_b32_e32 v153, v253
	v_lshl_add_u64 v[252:253], v[150:151], 0, s[98:99]
	v_mov_b32_e32 v150, v250
	v_mov_b32_e32 v151, v251
	global_load_dwordx4 v[250:253], v[252:253], off
	ds_read_b128 v[180:183], v157
	s_waitcnt lgkmcnt(0)
	v_mov_b32_e32 v184, v181
	v_mov_b32_e32 v185, v182
	v_mov_b32_e32 v181, v183
	v_pk_add_f32 v[180:181], v[184:185], v[180:181]
	v_mov_b64_e32 v[186:187], v[48:49]
	v_add_f32_e32 v169, v180, v181
	v_fmamk_f32 v169, v169, 0x3c000000, v235
	v_cmp_gt_f32_e32 vcc, s63, v169
	v_mul_f32_e32 v171, 0x4f800000, v169
	v_mov_b64_e32 v[184:185], v[46:47]
	v_cndmask_b32_e32 v169, v169, v171, vcc
	v_sqrt_f32_e32 v171, v169
	s_nop 0
	v_add_u32_e32 v175, -1, v171
	v_fma_f32 v180, -v175, v171, v169
	v_cmp_ge_f32_e64 s[0:1], 0, v180
	v_add_u32_e32 v180, 1, v171
	s_nop 0
	v_cndmask_b32_e64 v175, v171, v175, s[0:1]
	v_fma_f32 v171, -v180, v171, v169
	v_cmp_lt_f32_e64 s[0:1], 0, v171
	s_nop 1
	v_cndmask_b32_e64 v171, v175, v180, s[0:1]
	v_mul_f32_e32 v175, 0x37800000, v171
	v_cndmask_b32_e32 v171, v171, v175, vcc
	v_cmp_class_f32_e32 vcc, v169, v236
	s_nop 1
	v_cndmask_b32_e32 v169, v171, v169, vcc
	v_div_scale_f32 v171, s[0:1], v169, v169, 1.0
	v_rcp_f32_e32 v175, v171
	s_nop 0
	v_fma_f32 v180, -v171, v175, 1.0
	v_fmac_f32_e32 v175, v180, v175
	v_div_scale_f32 v180, vcc, 1.0, v169, 1.0
	v_mul_f32_e32 v181, v180, v175
	v_fma_f32 v182, -v171, v181, v180
	v_fmac_f32_e32 v181, v182, v175
	v_fma_f32 v171, -v171, v181, v180
	v_div_fmas_f32 v171, v171, v175, v181
	v_mov_b64_e32 v[182:183], v[44:45]
	v_mov_b64_e32 v[180:181], v[42:43]
	v_div_fixup_f32 v169, v171, v169, 1.0
	v_cvt_f32_i32_e32 v181, v181
	v_cvt_f32_i32_e32 v180, v180
	v_cvt_f32_i32_e32 v183, v183
	v_cvt_f32_i32_e32 v182, v182
	v_cvt_f32_i32_e32 v187, v187
	v_cvt_f32_i32_e32 v186, v186
	v_cvt_f32_i32_e32 v185, v185
	v_cvt_f32_i32_e32 v184, v184
	v_mul_f32_e32 v192, v174, v169
	v_pk_mul_f32 v[182:183], v[192:193], v[182:183] op_sel_hi:[0,1]
	v_pk_mul_f32 v[180:181], v[192:193], v[180:181] op_sel_hi:[0,1]
	v_pk_mul_f32 v[184:185], v[192:193], v[184:185] op_sel_hi:[0,1]
	v_pk_mul_f32 v[186:187], v[192:193], v[186:187] op_sel_hi:[0,1]
	v_pk_mul_f32 v[180:181], v[122:123], v[180:181]
	v_pk_mul_f32 v[182:183], v[124:125], v[182:183]
	v_pk_mul_f32 v[186:187], v[128:129], v[186:187]
	v_pk_mul_f32 v[184:185], v[126:127], v[184:185]
	v_pk_mul_f32 v[192:193], v[152:153], v[182:183]
	v_pk_mul_f32 v[210:211], v[150:151], v[180:181]
	v_pk_fma_f32 v[192:193], v[148:149], v[186:187], v[192:193] neg_lo:[0,0,1] neg_hi:[0,0,1]
	v_pk_fma_f32 v[210:211], v[146:147], v[184:185], v[210:211] neg_lo:[0,0,1] neg_hi:[0,0,1]
	v_pk_mul_f32 v[186:187], v[152:153], v[186:187]
	v_pk_mul_f32 v[184:185], v[150:151], v[184:185]
	v_pk_fma_f32 v[182:183], v[148:149], v[182:183], v[186:187]
	v_pk_fma_f32 v[180:181], v[146:147], v[180:181], v[184:185]
	v_mad_i64_i32 v[184:185], s[0:1], v167, s64, v[176:177]
	v_pk_add_f32 v[136:137], v[136:137], v[192:193]
	v_pk_add_f32 v[134:135], v[134:135], v[210:211]
	v_pk_add_f32 v[132:133], v[132:133], v[182:183]
	v_pk_add_f32 v[130:131], v[130:131], v[180:181]
	v_lshl_add_u64 v[184:185], v[184:185], 0, s[2:3]
	v_lshl_add_u64 v[212:213], v[184:185], 0, v[178:179]
	v_cvt_pk_bf16_f32 v184, v210, v211
	v_cvt_pk_bf16_f32 v185, v192, v193
	v_cvt_pk_bf16_f32 v180, v180, v181
	v_cvt_pk_bf16_f32 v181, v182, v183
	global_store_dwordx2 v[212:213], v[184:185], off
	global_store_dwordx2 v[212:213], v[180:181], off offset:128
	ds_read_b128 v[180:183], v157 offset:16
	s_waitcnt lgkmcnt(0)
	v_mov_b32_e32 v184, v181
	v_mov_b32_e32 v185, v182
	v_mov_b32_e32 v181, v183
	v_pk_add_f32 v[180:181], v[184:185], v[180:181]
	v_mov_b64_e32 v[186:187], v[40:41]
	v_add_f32_e32 v157, v180, v181
	v_fmamk_f32 v157, v157, 0x3c000000, v235
	v_cmp_gt_f32_e32 vcc, s63, v157
	v_mul_f32_e32 v167, 0x4f800000, v157
	v_mov_b64_e32 v[184:185], v[38:39]
	v_cndmask_b32_e32 v157, v157, v167, vcc
	v_sqrt_f32_e32 v167, v157
	s_nop 0
	v_add_u32_e32 v169, -1, v167
	v_fma_f32 v171, -v169, v167, v157
	v_cmp_ge_f32_e64 s[0:1], 0, v171
	v_add_u32_e32 v171, 1, v167
	s_nop 0
	v_cndmask_b32_e64 v169, v167, v169, s[0:1]
	v_fma_f32 v167, -v171, v167, v157
	v_cmp_lt_f32_e64 s[0:1], 0, v167
	s_nop 1
	v_cndmask_b32_e64 v167, v169, v171, s[0:1]
	v_mul_f32_e32 v169, 0x37800000, v167
	v_cndmask_b32_e32 v167, v167, v169, vcc
	v_cmp_class_f32_e32 vcc, v157, v236
	s_nop 1
	v_cndmask_b32_e32 v157, v167, v157, vcc
	v_div_scale_f32 v167, s[0:1], v157, v157, 1.0
	v_rcp_f32_e32 v169, v167
	s_nop 0
	v_fma_f32 v171, -v167, v169, 1.0
	v_fmac_f32_e32 v169, v171, v169
	v_div_scale_f32 v171, vcc, 1.0, v157, 1.0
	v_mul_f32_e32 v175, v171, v169
	v_fma_f32 v180, -v167, v175, v171
	v_fmac_f32_e32 v175, v180, v169
	v_mov_b64_e32 v[182:183], v[36:37]
	v_mov_b64_e32 v[180:181], v[34:35]
	v_fma_f32 v167, -v167, v175, v171
	v_cvt_f32_i32_e32 v187, v187
	v_cvt_f32_i32_e32 v186, v186
	v_cvt_f32_i32_e32 v185, v185
	v_cvt_f32_i32_e32 v184, v184
	v_cvt_f32_i32_e32 v181, v181
	v_cvt_f32_i32_e32 v180, v180
	v_cvt_f32_i32_e32 v183, v183
	v_cvt_f32_i32_e32 v182, v182
	v_div_fmas_f32 v167, v167, v169, v175
	v_div_fixup_f32 v157, v167, v157, 1.0
	v_mul_f32_e32 v174, v174, v157
	v_pk_mul_f32 v[184:185], v[174:175], v[184:185] op_sel_hi:[0,1]
	v_pk_mul_f32 v[186:187], v[174:175], v[186:187] op_sel_hi:[0,1]
	v_pk_mul_f32 v[182:183], v[174:175], v[182:183] op_sel_hi:[0,1]
	v_pk_mul_f32 v[174:175], v[174:175], v[180:181] op_sel_hi:[0,1]
	v_pk_mul_f32 v[186:187], v[128:129], v[186:187]
	v_pk_mul_f32 v[184:185], v[126:127], v[184:185]
	v_pk_mul_f32 v[174:175], v[122:123], v[174:175]
	v_pk_mul_f32 v[180:181], v[124:125], v[182:183]
	v_pk_mul_f32 v[192:193], v[150:151], v[174:175]
	v_pk_mul_f32 v[182:183], v[152:153], v[180:181]
	v_pk_mul_f32 v[152:153], v[152:153], v[186:187]
	v_pk_mul_f32 v[150:151], v[150:151], v[184:185]
	v_pk_fma_f32 v[192:193], v[146:147], v[184:185], v[192:193] neg_lo:[0,0,1] neg_hi:[0,0,1]
	v_pk_fma_f32 v[182:183], v[148:149], v[186:187], v[182:183] neg_lo:[0,0,1] neg_hi:[0,0,1]
	v_pk_fma_f32 v[150:151], v[146:147], v[174:175], v[150:151]
	v_pk_fma_f32 v[152:153], v[148:149], v[180:181], v[152:153]
	v_pk_add_f32 v[144:145], v[144:145], v[182:183]
	v_pk_add_f32 v[142:143], v[142:143], v[192:193]
	v_pk_add_f32 v[148:149], v[140:141], v[152:153]
	v_pk_add_f32 v[146:147], v[138:139], v[150:151]
	v_add_u32_e32 v157, 0xa0, v190
	v_cvt_pk_bf16_f32 v138, v192, v193
	v_cvt_pk_bf16_f32 v139, v182, v183
	v_add_u32_e32 v167, s19, v157
	v_cvt_pk_bf16_f32 v140, v150, v151
	v_cvt_pk_bf16_f32 v141, v152, v153
	global_store_dwordx2 v[212:213], v[138:139], off offset:256
	global_store_dwordx2 v[212:213], v[140:141], off offset:384
	v_lshlrev_b32_e32 v138, 8, v167
	v_and_b32_e32 v202, 0x7ff00, v138
	v_lshl_add_u64 v[138:139], s[8:9], 0, v[202:203]
	v_lshl_add_u64 v[150:151], s[16:17], 0, v[202:203]
	v_lshl_add_u64 v[138:139], v[138:139], 0, v[172:173]
	v_lshl_add_u64 v[150:151], v[150:151], 0, v[172:173]
	s_waitcnt vmcnt(4)
	v_mov_b32_e32 v140, v246
	v_mov_b32_e32 v141, v247
	v_lshl_add_u64 v[246:247], v[138:139], 0, s[98:99]
	v_mov_b32_e32 v138, v244
	v_mov_b32_e32 v139, v245
	global_load_dwordx4 v[244:247], v[246:247], off
	v_lshl_add_u32 v157, v157, 5, s21
	v_mov_b32_e32 v152, v252
	v_mov_b32_e32 v153, v253
	v_lshl_add_u64 v[252:253], v[150:151], 0, s[98:99]
	v_mov_b32_e32 v150, v250
	v_mov_b32_e32 v151, v251
	global_load_dwordx4 v[250:253], v[252:253], off
	ds_read_b128 v[180:183], v157
	v_mov_b64_e32 v[186:187], v[28:29]
	v_mov_b64_e32 v[184:185], v[26:27]
	s_waitcnt lgkmcnt(0)
	v_mov_b32_e32 v174, v181
	v_mov_b32_e32 v175, v182
	v_mov_b32_e32 v181, v183
	v_pk_add_f32 v[174:175], v[174:175], v[180:181]
	s_nop 0
	v_add_f32_e32 v169, v174, v175
	v_fmamk_f32 v169, v169, 0x3c000000, v235
	v_cmp_gt_f32_e32 vcc, s63, v169
	v_mul_f32_e32 v171, 0x4f800000, v169
	s_nop 0
	v_cndmask_b32_e32 v169, v169, v171, vcc
	v_sqrt_f32_e32 v171, v169
	s_nop 0
	v_add_u32_e32 v174, -1, v171
	v_fma_f32 v175, -v174, v171, v169
	v_cmp_ge_f32_e64 s[0:1], 0, v175
	v_add_u32_e32 v175, 1, v171
	s_nop 0
	v_cndmask_b32_e64 v174, v171, v174, s[0:1]
	v_fma_f32 v171, -v175, v171, v169
	v_cmp_lt_f32_e64 s[0:1], 0, v171
	s_nop 1
	v_cndmask_b32_e64 v171, v174, v175, s[0:1]
	v_mul_f32_e32 v174, 0x37800000, v171
	v_cndmask_b32_e32 v171, v171, v174, vcc
	v_cmp_class_f32_e32 vcc, v169, v236
	s_nop 1
	v_cndmask_b32_e32 v169, v171, v169, vcc
	v_div_scale_f32 v171, s[0:1], v169, v169, 1.0
	v_rcp_f32_e32 v174, v171
	s_nop 0
	v_fma_f32 v175, -v171, v174, 1.0
	v_fmac_f32_e32 v174, v175, v174
	v_div_scale_f32 v175, vcc, 1.0, v169, 1.0
	v_mul_f32_e32 v180, v175, v174
	v_fma_f32 v181, -v171, v180, v175
	v_fmac_f32_e32 v180, v181, v174
	v_fma_f32 v171, -v171, v180, v175
	v_div_fmas_f32 v171, v171, v174, v180
	v_mov_b64_e32 v[182:183], v[32:33]
	v_mov_b64_e32 v[180:181], v[30:31]
	v_div_fixup_f32 v169, v171, v169, 1.0
	v_cvt_f32_i32_e32 v175, v183
	v_cvt_f32_i32_e32 v174, v182
	v_cvt_f32_i32_e32 v181, v181
	v_cvt_f32_i32_e32 v180, v180
	v_cvt_f32_i32_e32 v185, v185
	v_cvt_f32_i32_e32 v184, v184
	v_cvt_f32_i32_e32 v187, v187
	v_cvt_f32_i32_e32 v186, v186
	v_mul_f32_e32 v182, v170, v169
	v_pk_mul_f32 v[180:181], v[182:183], v[180:181] op_sel_hi:[0,1]
	v_pk_mul_f32 v[174:175], v[182:183], v[174:175] op_sel_hi:[0,1]
	v_pk_mul_f32 v[186:187], v[182:183], v[186:187] op_sel_hi:[0,1]
	v_pk_mul_f32 v[182:183], v[182:183], v[184:185] op_sel_hi:[0,1]
	v_pk_mul_f32 v[182:183], v[122:123], v[182:183]
	v_pk_mul_f32 v[184:185], v[124:125], v[186:187]
	v_pk_mul_f32 v[174:175], v[128:129], v[174:175]
	v_pk_mul_f32 v[180:181], v[126:127], v[180:181]
	v_pk_mul_f32 v[186:187], v[152:153], v[184:185]
	v_pk_mul_f32 v[192:193], v[150:151], v[182:183]
	v_pk_fma_f32 v[186:187], v[140:141], v[174:175], v[186:187] neg_lo:[0,0,1] neg_hi:[0,0,1]
	v_pk_fma_f32 v[192:193], v[138:139], v[180:181], v[192:193] neg_lo:[0,0,1] neg_hi:[0,0,1]
	v_pk_mul_f32 v[174:175], v[152:153], v[174:175]
	v_pk_mul_f32 v[180:181], v[150:151], v[180:181]
	v_pk_fma_f32 v[174:175], v[140:141], v[184:185], v[174:175]
	v_pk_fma_f32 v[180:181], v[138:139], v[182:183], v[180:181]
	v_mad_i64_i32 v[182:183], s[0:1], v167, s64, v[176:177]
	v_pk_add_f32 v[136:137], v[136:137], v[186:187]
	v_pk_add_f32 v[134:135], v[134:135], v[192:193]
	v_pk_add_f32 v[132:133], v[132:133], v[174:175]
	v_pk_add_f32 v[130:131], v[130:131], v[180:181]
	v_lshl_add_u64 v[182:183], v[182:183], 0, s[2:3]
	v_lshl_add_u64 v[210:211], v[182:183], 0, v[178:179]
	v_cvt_pk_bf16_f32 v182, v192, v193
	v_cvt_pk_bf16_f32 v183, v186, v187
	v_cvt_pk_bf16_f32 v180, v180, v181
	v_cvt_pk_bf16_f32 v181, v174, v175
	global_store_dwordx2 v[210:211], v[182:183], off
	global_store_dwordx2 v[210:211], v[180:181], off offset:128
	ds_read_b128 v[180:183], v157 offset:16
	v_mov_b64_e32 v[186:187], v[24:25]
	v_mov_b64_e32 v[184:185], v[22:23]
	s_waitcnt lgkmcnt(0)
	v_mov_b32_e32 v174, v181
	v_mov_b32_e32 v175, v182
	v_mov_b32_e32 v181, v183
	v_pk_add_f32 v[174:175], v[174:175], v[180:181]
	v_mov_b64_e32 v[182:183], v[20:21]
	v_add_f32_e32 v157, v174, v175
	v_fmamk_f32 v157, v157, 0x3c000000, v235
	v_cmp_gt_f32_e32 vcc, s63, v157
	v_mul_f32_e32 v167, 0x4f800000, v157
	v_mov_b64_e32 v[180:181], v[18:19]
	v_cndmask_b32_e32 v157, v157, v167, vcc
	v_sqrt_f32_e32 v167, v157
	s_nop 0
	v_cvt_f32_i32_e32 v185, v185
	v_add_u32_e32 v169, -1, v167
	v_fma_f32 v171, -v169, v167, v157
	v_cmp_ge_f32_e64 s[0:1], 0, v171
	v_add_u32_e32 v171, 1, v167
	v_cvt_f32_i32_e32 v184, v184
	v_cndmask_b32_e64 v169, v167, v169, s[0:1]
	v_fma_f32 v167, -v171, v167, v157
	v_cmp_lt_f32_e64 s[0:1], 0, v167
	v_cvt_f32_i32_e32 v181, v181
	v_cvt_f32_i32_e32 v180, v180
	v_cndmask_b32_e64 v167, v169, v171, s[0:1]
	v_mul_f32_e32 v169, 0x37800000, v167
	v_cndmask_b32_e32 v167, v167, v169, vcc
	v_cmp_class_f32_e32 vcc, v157, v236
	v_cvt_f32_i32_e32 v183, v183
	v_cvt_f32_i32_e32 v182, v182
	v_cndmask_b32_e32 v157, v167, v157, vcc
	v_div_scale_f32 v167, s[0:1], v157, v157, 1.0
	v_rcp_f32_e32 v169, v167
	s_nop 0
	v_fma_f32 v171, -v167, v169, 1.0
	v_fmac_f32_e32 v169, v171, v169
	v_div_scale_f32 v171, vcc, 1.0, v157, 1.0
	v_mul_f32_e32 v174, v171, v169
	v_fma_f32 v175, -v167, v174, v171
	v_fmac_f32_e32 v174, v175, v169
	v_fma_f32 v167, -v167, v174, v171
	v_div_fmas_f32 v167, v167, v169, v174
	v_cvt_f32_i32_e32 v175, v187
	v_cvt_f32_i32_e32 v174, v186
	v_div_fixup_f32 v157, v167, v157, 1.0
	v_mul_f32_e32 v170, v170, v157
	v_pk_mul_f32 v[184:185], v[170:171], v[184:185] op_sel_hi:[0,1]
	v_pk_mul_f32 v[174:175], v[170:171], v[174:175] op_sel_hi:[0,1]
	v_pk_mul_f32 v[182:183], v[170:171], v[182:183] op_sel_hi:[0,1]
	v_pk_mul_f32 v[170:171], v[170:171], v[180:181] op_sel_hi:[0,1]
	v_pk_mul_f32 v[174:175], v[128:129], v[174:175]
	v_pk_mul_f32 v[184:185], v[126:127], v[184:185]
	v_pk_mul_f32 v[170:171], v[122:123], v[170:171]
	v_pk_mul_f32 v[180:181], v[124:125], v[182:183]
	v_pk_mul_f32 v[186:187], v[150:151], v[170:171]
	v_pk_mul_f32 v[182:183], v[152:153], v[180:181]
	v_pk_mul_f32 v[152:153], v[152:153], v[174:175]
	v_pk_mul_f32 v[150:151], v[150:151], v[184:185]
	v_pk_fma_f32 v[186:187], v[138:139], v[184:185], v[186:187] neg_lo:[0,0,1] neg_hi:[0,0,1]
	v_pk_fma_f32 v[182:183], v[140:141], v[174:175], v[182:183] neg_lo:[0,0,1] neg_hi:[0,0,1]
	v_pk_fma_f32 v[150:151], v[138:139], v[170:171], v[150:151]
	v_pk_fma_f32 v[152:153], v[140:141], v[180:181], v[152:153]
	v_pk_add_f32 v[140:141], v[144:145], v[182:183]
	v_pk_add_f32 v[138:139], v[142:143], v[186:187]
	v_pk_add_f32 v[144:145], v[148:149], v[152:153]
	v_pk_add_f32 v[142:143], v[146:147], v[150:151]
	v_add_u32_e32 v157, 0xb0, v190
	v_cvt_pk_bf16_f32 v146, v186, v187
	v_cvt_pk_bf16_f32 v147, v182, v183
	v_add_u32_e32 v167, s19, v157
	v_cvt_pk_bf16_f32 v148, v150, v151
	v_cvt_pk_bf16_f32 v149, v152, v153
	global_store_dwordx2 v[210:211], v[146:147], off offset:256
	global_store_dwordx2 v[210:211], v[148:149], off offset:384
	v_lshlrev_b32_e32 v146, 8, v167
	v_and_b32_e32 v202, 0x7ff00, v146
	v_lshl_add_u64 v[146:147], s[8:9], 0, v[202:203]
	v_lshl_add_u64 v[150:151], s[16:17], 0, v[202:203]
	v_lshl_add_u64 v[146:147], v[146:147], 0, v[172:173]
	v_lshl_add_u64 v[150:151], v[150:151], 0, v[172:173]
	s_waitcnt vmcnt(4)
	v_mov_b32_e32 v146, v244
	v_mov_b32_e32 v147, v245
	v_mov_b32_e32 v148, v246
	v_mov_b32_e32 v149, v247
	v_lshl_add_u32 v157, v157, 5, s21
	v_mov_b32_e32 v150, v250
	v_mov_b32_e32 v151, v251
	v_mov_b32_e32 v152, v252
	v_mov_b32_e32 v153, v253
	ds_read_b128 v[170:173], v157
	v_mov_b64_e32 v[182:183], v[12:13]
	v_mov_b64_e32 v[180:181], v[10:11]
	s_waitcnt lgkmcnt(0)
	v_mov_b32_e32 v174, v171
	v_mov_b32_e32 v175, v172
	v_mov_b32_e32 v171, v173
	v_pk_add_f32 v[170:171], v[174:175], v[170:171]
	s_nop 0
	v_add_f32_e32 v169, v170, v171
	v_fmamk_f32 v169, v169, 0x3c000000, v235
	v_cmp_gt_f32_e32 vcc, s63, v169
	v_mul_f32_e32 v170, 0x4f800000, v169
	s_nop 0
	v_cndmask_b32_e32 v169, v169, v170, vcc
	v_sqrt_f32_e32 v170, v169
	s_nop 0
	v_add_u32_e32 v171, -1, v170
	v_fma_f32 v172, -v171, v170, v169
	v_cmp_ge_f32_e64 s[0:1], 0, v172
	v_add_u32_e32 v172, 1, v170
	s_nop 0
	v_cndmask_b32_e64 v171, v170, v171, s[0:1]
	v_fma_f32 v170, -v172, v170, v169
	v_cmp_lt_f32_e64 s[0:1], 0, v170
	s_nop 1
	v_cndmask_b32_e64 v170, v171, v172, s[0:1]
	v_mul_f32_e32 v171, 0x37800000, v170
	v_cndmask_b32_e32 v170, v170, v171, vcc
	v_cmp_class_f32_e32 vcc, v169, v236
	s_nop 1
	v_cndmask_b32_e32 v169, v170, v169, vcc
	v_div_scale_f32 v170, s[0:1], v169, v169, 1.0
	v_rcp_f32_e32 v171, v170
	s_nop 0
	v_fma_f32 v172, -v170, v171, 1.0
	v_fmac_f32_e32 v171, v172, v171
	v_div_scale_f32 v172, vcc, 1.0, v169, 1.0
	v_mul_f32_e32 v173, v172, v171
	v_fma_f32 v174, -v170, v173, v172
	v_fmac_f32_e32 v173, v174, v171
	v_fma_f32 v170, -v170, v173, v172
	v_div_fmas_f32 v170, v170, v171, v173
	v_div_fixup_f32 v169, v170, v169, 1.0
	v_mov_b64_e32 v[172:173], v[16:17]
	v_mov_b64_e32 v[170:171], v[14:15]
	v_mul_f32_e32 v174, v166, v169
	v_cvt_f32_i32_e32 v173, v173
	v_cvt_f32_i32_e32 v172, v172
	v_cvt_f32_i32_e32 v171, v171
	v_cvt_f32_i32_e32 v170, v170
	v_cvt_f32_i32_e32 v181, v181
	v_cvt_f32_i32_e32 v180, v180
	v_cvt_f32_i32_e32 v183, v183
	v_cvt_f32_i32_e32 v182, v182
	v_pk_mul_f32 v[170:171], v[174:175], v[170:171] op_sel_hi:[0,1]
	v_pk_mul_f32 v[172:173], v[174:175], v[172:173] op_sel_hi:[0,1]
	v_pk_mul_f32 v[172:173], v[128:129], v[172:173]
	v_pk_mul_f32 v[182:183], v[174:175], v[182:183] op_sel_hi:[0,1]
	v_pk_mul_f32 v[174:175], v[174:175], v[180:181] op_sel_hi:[0,1]
	v_pk_mul_f32 v[174:175], v[122:123], v[174:175]
	v_pk_mul_f32 v[180:181], v[124:125], v[182:183]
	v_pk_mul_f32 v[170:171], v[126:127], v[170:171]
	v_pk_mul_f32 v[182:183], v[152:153], v[180:181]
	v_pk_mul_f32 v[184:185], v[150:151], v[174:175]
	v_pk_fma_f32 v[182:183], v[148:149], v[172:173], v[182:183] neg_lo:[0,0,1] neg_hi:[0,0,1]
	v_pk_fma_f32 v[184:185], v[146:147], v[170:171], v[184:185] neg_lo:[0,0,1] neg_hi:[0,0,1]
	v_pk_mul_f32 v[172:173], v[152:153], v[172:173]
	v_pk_mul_f32 v[170:171], v[150:151], v[170:171]
	v_pk_fma_f32 v[172:173], v[148:149], v[180:181], v[172:173]
	v_pk_fma_f32 v[170:171], v[146:147], v[174:175], v[170:171]
	v_mad_i64_i32 v[174:175], s[0:1], v167, s64, v[176:177]
	v_pk_add_f32 v[136:137], v[136:137], v[182:183]
	v_pk_add_f32 v[134:135], v[134:135], v[184:185]
	v_pk_add_f32 v[132:133], v[132:133], v[172:173]
	v_pk_add_f32 v[130:131], v[130:131], v[170:171]
	v_lshl_add_u64 v[174:175], v[174:175], 0, s[2:3]
	v_lshl_add_u64 v[178:179], v[174:175], 0, v[178:179]
	v_cvt_pk_bf16_f32 v174, v184, v185
	v_cvt_pk_bf16_f32 v175, v182, v183
	v_cvt_pk_bf16_f32 v170, v170, v171
	v_cvt_pk_bf16_f32 v171, v172, v173
	global_store_dwordx2 v[178:179], v[174:175], off
	global_store_dwordx2 v[178:179], v[170:171], off offset:128
	ds_read_b128 v[170:173], v157 offset:16
	s_waitcnt lgkmcnt(0)
	v_mov_b32_e32 v174, v171
	v_mov_b32_e32 v175, v172
	v_mov_b32_e32 v171, v173
	v_pk_add_f32 v[170:171], v[174:175], v[170:171]
	v_mov_b64_e32 v[176:177], v[8:9]
	v_add_f32_e32 v157, v170, v171
	v_fmamk_f32 v157, v157, 0x3c000000, v235
	v_cmp_gt_f32_e32 vcc, s63, v157
	v_mul_f32_e32 v167, 0x4f800000, v157
	v_mov_b64_e32 v[174:175], v[6:7]
	v_cndmask_b32_e32 v157, v157, v167, vcc
	v_sqrt_f32_e32 v167, v157
	s_nop 0
	v_add_u32_e32 v169, -1, v167
	v_fma_f32 v170, -v169, v167, v157
	v_cmp_ge_f32_e64 s[0:1], 0, v170
	v_add_u32_e32 v170, 1, v167
	s_nop 0
	v_cndmask_b32_e64 v169, v167, v169, s[0:1]
	v_fma_f32 v167, -v170, v167, v157
	v_cmp_lt_f32_e64 s[0:1], 0, v167
	s_nop 1
	v_cndmask_b32_e64 v167, v169, v170, s[0:1]
	v_mul_f32_e32 v169, 0x37800000, v167
	v_cndmask_b32_e32 v167, v167, v169, vcc
	v_cmp_class_f32_e32 vcc, v157, v236
	s_nop 1
	v_cndmask_b32_e32 v157, v167, v157, vcc
	v_div_scale_f32 v167, s[0:1], v157, v157, 1.0
	v_rcp_f32_e32 v169, v167
	s_nop 0
	v_fma_f32 v170, -v167, v169, 1.0
	v_fmac_f32_e32 v169, v170, v169
	v_div_scale_f32 v170, vcc, 1.0, v157, 1.0
	v_mul_f32_e32 v171, v170, v169
	v_fma_f32 v172, -v167, v171, v170
	v_fmac_f32_e32 v171, v172, v169
	v_fma_f32 v167, -v167, v171, v170
	v_div_fmas_f32 v167, v167, v169, v171
	v_mov_b64_e32 v[172:173], v[4:5]
	v_mov_b64_e32 v[170:171], v[2:3]
	v_div_fixup_f32 v157, v167, v157, 1.0
	v_cvt_f32_i32_e32 v177, v177
	v_cvt_f32_i32_e32 v176, v176
	v_cvt_f32_i32_e32 v175, v175
	v_cvt_f32_i32_e32 v174, v174
	v_cvt_f32_i32_e32 v171, v171
	v_cvt_f32_i32_e32 v170, v170
	v_cvt_f32_i32_e32 v173, v173
	v_cvt_f32_i32_e32 v172, v172
	v_mul_f32_e32 v166, v166, v157
	v_pk_mul_f32 v[174:175], v[166:167], v[174:175] op_sel_hi:[0,1]
	v_pk_mul_f32 v[176:177], v[166:167], v[176:177] op_sel_hi:[0,1]
	v_pk_mul_f32 v[172:173], v[166:167], v[172:173] op_sel_hi:[0,1]
	v_pk_mul_f32 v[166:167], v[166:167], v[170:171] op_sel_hi:[0,1]
	v_pk_mul_f32 v[122:123], v[122:123], v[166:167]
	v_pk_mul_f32 v[124:125], v[124:125], v[172:173]
	v_pk_mul_f32 v[128:129], v[128:129], v[176:177]
	v_pk_mul_f32 v[126:127], v[126:127], v[174:175]
	v_pk_mul_f32 v[166:167], v[152:153], v[124:125]
	v_pk_mul_f32 v[170:171], v[150:151], v[122:123]
	v_pk_fma_f32 v[166:167], v[148:149], v[128:129], v[166:167] neg_lo:[0,0,1] neg_hi:[0,0,1]
	v_pk_fma_f32 v[170:171], v[146:147], v[126:127], v[170:171] neg_lo:[0,0,1] neg_hi:[0,0,1]
	v_pk_mul_f32 v[128:129], v[152:153], v[128:129]
	v_pk_mul_f32 v[126:127], v[150:151], v[126:127]
	v_pk_fma_f32 v[148:149], v[148:149], v[124:125], v[128:129]
	v_pk_fma_f32 v[146:147], v[146:147], v[122:123], v[126:127]
	v_pk_add_f32 v[128:129], v[140:141], v[166:167]
	v_pk_add_f32 v[126:127], v[138:139], v[170:171]
	v_pk_add_f32 v[124:125], v[144:145], v[148:149]
	v_pk_add_f32 v[122:123], v[142:143], v[146:147]
	s_nop 0
	v_cvt_pk_bf16_f32 v138, v170, v171
	v_cvt_pk_bf16_f32 v139, v166, v167
	v_cvt_pk_bf16_f32 v140, v146, v147
	v_cvt_pk_bf16_f32 v141, v148, v149
	global_store_dwordx2 v[178:179], v[138:139], off offset:256
	global_store_dwordx2 v[178:179], v[140:141], off offset:384
	s_cbranch_scc1 .LBB0_2160
	v_xor_b32_e32 v138, 1, v238
	v_cmp_lt_i32_e32 vcc, v138, v155
	v_xor_b32_e32 v139, 2, v238
	s_nop 0
	v_cndmask_b32_e32 v138, v238, v138, vcc
	v_lshlrev_b32_e32 v138, 2, v138
	s_nop 1
	v_mov_b32_dpp v143, v134 quad_perm:[1,0,3,2] row_mask:0xf bank_mask:0xf
	v_cmp_lt_i32_e32 vcc, v139, v155
	s_waitcnt lgkmcnt(0)
	v_add_f32_e32 v134, v134, v143
	v_cndmask_b32_e32 v139, v238, v139, vcc
	v_lshlrev_b32_e32 v140, 2, v139
	s_nop 1
	v_mov_b32_dpp v143, v134 quad_perm:[2,3,0,1] row_mask:0xf bank_mask:0xf
	v_xor_b32_e32 v139, 4, v238
	v_cmp_lt_i32_e32 vcc, v139, v155
	v_add_f32_e32 v134, v134, v143
	v_cndmask_b32_e32 v139, v238, v139, vcc
	v_lshlrev_b32_e32 v141, 2, v139
	s_nop 1
	v_mov_b32_dpp v143, v134 row_half_mirror row_mask:0xf bank_mask:0xf
	v_xor_b32_e32 v139, 8, v238
	v_cmp_lt_i32_e32 vcc, v139, v155
	v_add_f32_e32 v134, v134, v143
	v_cndmask_b32_e32 v139, v238, v139, vcc
	v_lshlrev_b32_e32 v142, 2, v139
	s_nop 1
	v_mov_b32_dpp v143, v134 row_mirror row_mask:0xf bank_mask:0xf
	v_cmp_eq_u32_e32 vcc, 0, v189
	v_lshl_add_u32 v139, v168, 2, s60
	s_and_saveexec_b64 s[0:1], vcc
	s_cbranch_execz .LBB0_2127
	v_add_f32_e32 v134, v134, v143
	ds_write_b32 v139, v134
.LBB0_2127:
	s_or_b64 exec, exec, s[0:1]
	s_nop 1
	v_mov_b32_dpp v134, v135 quad_perm:[1,0,3,2] row_mask:0xf bank_mask:0xf
	v_add_f32_e32 v134, v135, v134
	s_nop 1
	v_mov_b32_dpp v135, v134 quad_perm:[2,3,0,1] row_mask:0xf bank_mask:0xf
	v_add_f32_e32 v134, v134, v135
	s_nop 1
	v_mov_b32_dpp v135, v134 row_half_mirror row_mask:0xf bank_mask:0xf
	v_add_f32_e32 v134, v134, v135
	s_nop 1
	v_mov_b32_dpp v135, v134 row_mirror row_mask:0xf bank_mask:0xf
	s_and_saveexec_b64 s[0:1], vcc
	s_cbranch_execz .LBB0_2129
	v_add_f32_e32 v134, v134, v135
	ds_write_b32 v139, v134 offset:4
.LBB0_2129:
	s_or_b64 exec, exec, s[0:1]
	s_nop 1
	v_mov_b32_dpp v134, v136 quad_perm:[1,0,3,2] row_mask:0xf bank_mask:0xf
	v_add_f32_e32 v134, v136, v134
	s_nop 1
	v_mov_b32_dpp v135, v134 quad_perm:[2,3,0,1] row_mask:0xf bank_mask:0xf
	v_add_f32_e32 v134, v134, v135
	s_nop 1
	v_mov_b32_dpp v135, v134 row_half_mirror row_mask:0xf bank_mask:0xf
	v_add_f32_e32 v134, v134, v135
	s_nop 1
	v_mov_b32_dpp v135, v134 row_mirror row_mask:0xf bank_mask:0xf
	s_and_saveexec_b64 s[0:1], vcc
	s_cbranch_execz .LBB0_2131
	v_add_f32_e32 v134, v134, v135
	ds_write_b32 v139, v134 offset:8
.LBB0_2131:
	s_or_b64 exec, exec, s[0:1]
	s_nop 1
	v_mov_b32_dpp v134, v137 quad_perm:[1,0,3,2] row_mask:0xf bank_mask:0xf
	v_add_f32_e32 v134, v137, v134
	s_nop 1
	v_mov_b32_dpp v135, v134 quad_perm:[2,3,0,1] row_mask:0xf bank_mask:0xf
	v_add_f32_e32 v134, v134, v135
	s_nop 1
	v_mov_b32_dpp v135, v134 row_half_mirror row_mask:0xf bank_mask:0xf
	v_add_f32_e32 v134, v134, v135
	s_nop 1
	v_mov_b32_dpp v135, v134 row_mirror row_mask:0xf bank_mask:0xf
	s_and_saveexec_b64 s[0:1], vcc
	s_cbranch_execz .LBB0_2133
	v_add_f32_e32 v134, v134, v135
	ds_write_b32 v139, v134 offset:12
.LBB0_2133:
	s_or_b64 exec, exec, s[0:1]
	s_nop 1
	v_mov_b32_dpp v134, v130 quad_perm:[1,0,3,2] row_mask:0xf bank_mask:0xf
	v_add_f32_e32 v130, v130, v134
	s_nop 1
	v_mov_b32_dpp v134, v130 quad_perm:[2,3,0,1] row_mask:0xf bank_mask:0xf
	v_add_f32_e32 v130, v130, v134
	s_nop 1
	v_mov_b32_dpp v134, v130 row_half_mirror row_mask:0xf bank_mask:0xf
	v_add_f32_e32 v130, v130, v134
	s_nop 1
	v_mov_b32_dpp v134, v130 row_mirror row_mask:0xf bank_mask:0xf
	s_and_saveexec_b64 s[0:1], vcc
	s_cbranch_execz .LBB0_2135
	v_add_f32_e32 v130, v130, v134
	ds_write_b32 v139, v130 offset:256
.LBB0_2135:
	s_or_b64 exec, exec, s[0:1]
	s_nop 1
	v_mov_b32_dpp v130, v131 quad_perm:[1,0,3,2] row_mask:0xf bank_mask:0xf
	v_add_f32_e32 v130, v131, v130
	s_nop 1
	v_mov_b32_dpp v131, v130 quad_perm:[2,3,0,1] row_mask:0xf bank_mask:0xf
	v_add_f32_e32 v130, v130, v131
	s_nop 1
	v_mov_b32_dpp v131, v130 row_half_mirror row_mask:0xf bank_mask:0xf
	v_add_f32_e32 v130, v130, v131
	s_nop 1
	v_mov_b32_dpp v131, v130 row_mirror row_mask:0xf bank_mask:0xf
	s_and_saveexec_b64 s[0:1], vcc
	s_cbranch_execz .LBB0_2137
	v_add_f32_e32 v130, v130, v131
	ds_write_b32 v139, v130 offset:260
.LBB0_2137:
	s_or_b64 exec, exec, s[0:1]
	s_nop 1
	v_mov_b32_dpp v130, v132 quad_perm:[1,0,3,2] row_mask:0xf bank_mask:0xf
	v_add_f32_e32 v130, v132, v130
	s_nop 1
	v_mov_b32_dpp v131, v130 quad_perm:[2,3,0,1] row_mask:0xf bank_mask:0xf
	v_add_f32_e32 v130, v130, v131
	s_nop 1
	v_mov_b32_dpp v131, v130 row_half_mirror row_mask:0xf bank_mask:0xf
	v_add_f32_e32 v130, v130, v131
	s_nop 1
	v_mov_b32_dpp v131, v130 row_mirror row_mask:0xf bank_mask:0xf
	s_and_saveexec_b64 s[0:1], vcc
	s_cbranch_execz .LBB0_2139
	v_add_f32_e32 v130, v130, v131
	ds_write_b32 v139, v130 offset:264
.LBB0_2139:
	s_or_b64 exec, exec, s[0:1]
	s_nop 1
	v_mov_b32_dpp v130, v133 quad_perm:[1,0,3,2] row_mask:0xf bank_mask:0xf
	v_add_f32_e32 v130, v133, v130
	s_nop 1
	v_mov_b32_dpp v131, v130 quad_perm:[2,3,0,1] row_mask:0xf bank_mask:0xf
	v_add_f32_e32 v130, v130, v131
	s_nop 1
	v_mov_b32_dpp v131, v130 row_half_mirror row_mask:0xf bank_mask:0xf
	v_add_f32_e32 v130, v130, v131
	s_nop 1
	v_mov_b32_dpp v131, v130 row_mirror row_mask:0xf bank_mask:0xf
	s_and_saveexec_b64 s[0:1], vcc
	s_cbranch_execz .LBB0_2141
	v_add_f32_e32 v130, v130, v131
	ds_write_b32 v139, v130 offset:268
.LBB0_2141:
	s_or_b64 exec, exec, s[0:1]
	s_nop 1
	v_mov_b32_dpp v130, v126 quad_perm:[1,0,3,2] row_mask:0xf bank_mask:0xf
	v_add_f32_e32 v126, v126, v130
	s_nop 1
	v_mov_b32_dpp v130, v126 quad_perm:[2,3,0,1] row_mask:0xf bank_mask:0xf
	v_add_f32_e32 v126, v126, v130
	s_nop 1
	v_mov_b32_dpp v130, v126 row_half_mirror row_mask:0xf bank_mask:0xf
	v_add_f32_e32 v126, v126, v130
	s_nop 1
	v_mov_b32_dpp v130, v126 row_mirror row_mask:0xf bank_mask:0xf
	s_and_saveexec_b64 s[0:1], vcc
	s_cbranch_execz .LBB0_2143
	v_add_f32_e32 v126, v126, v130
	ds_write_b32 v139, v126 offset:512
.LBB0_2143:
	s_or_b64 exec, exec, s[0:1]
	s_nop 1
	v_mov_b32_dpp v126, v127 quad_perm:[1,0,3,2] row_mask:0xf bank_mask:0xf
	v_add_f32_e32 v126, v127, v126
	s_nop 1
	v_mov_b32_dpp v127, v126 quad_perm:[2,3,0,1] row_mask:0xf bank_mask:0xf
	v_add_f32_e32 v126, v126, v127
	s_nop 1
	v_mov_b32_dpp v127, v126 row_half_mirror row_mask:0xf bank_mask:0xf
	v_add_f32_e32 v126, v126, v127
	s_nop 1
	v_mov_b32_dpp v127, v126 row_mirror row_mask:0xf bank_mask:0xf
	s_and_saveexec_b64 s[0:1], vcc
	s_cbranch_execz .LBB0_2145
	v_add_f32_e32 v126, v126, v127
	ds_write_b32 v139, v126 offset:516
.LBB0_2145:
	s_or_b64 exec, exec, s[0:1]
	s_nop 1
	v_mov_b32_dpp v126, v128 quad_perm:[1,0,3,2] row_mask:0xf bank_mask:0xf
	v_add_f32_e32 v126, v128, v126
	s_nop 1
	v_mov_b32_dpp v127, v126 quad_perm:[2,3,0,1] row_mask:0xf bank_mask:0xf
	v_add_f32_e32 v126, v126, v127
	s_nop 1
	v_mov_b32_dpp v127, v126 row_half_mirror row_mask:0xf bank_mask:0xf
	v_add_f32_e32 v126, v126, v127
	s_nop 1
	v_mov_b32_dpp v127, v126 row_mirror row_mask:0xf bank_mask:0xf
	s_and_saveexec_b64 s[0:1], vcc
	s_cbranch_execz .LBB0_2147
	v_add_f32_e32 v126, v126, v127
	ds_write_b32 v139, v126 offset:520
.LBB0_2147:
	s_or_b64 exec, exec, s[0:1]
	s_nop 1
	v_mov_b32_dpp v126, v129 quad_perm:[1,0,3,2] row_mask:0xf bank_mask:0xf
	v_add_f32_e32 v126, v129, v126
	s_nop 1
	v_mov_b32_dpp v127, v126 quad_perm:[2,3,0,1] row_mask:0xf bank_mask:0xf
	v_add_f32_e32 v126, v126, v127
	s_nop 1
	v_mov_b32_dpp v127, v126 row_half_mirror row_mask:0xf bank_mask:0xf
	v_add_f32_e32 v126, v126, v127
	s_nop 1
	v_mov_b32_dpp v127, v126 row_mirror row_mask:0xf bank_mask:0xf
	s_and_saveexec_b64 s[0:1], vcc
	s_cbranch_execz .LBB0_2149
	v_add_f32_e32 v126, v126, v127
	ds_write_b32 v139, v126 offset:524
.LBB0_2149:
	s_or_b64 exec, exec, s[0:1]
	s_nop 1
	v_mov_b32_dpp v126, v122 quad_perm:[1,0,3,2] row_mask:0xf bank_mask:0xf
	v_add_f32_e32 v122, v122, v126
	s_nop 1
	v_mov_b32_dpp v126, v122 quad_perm:[2,3,0,1] row_mask:0xf bank_mask:0xf
	v_add_f32_e32 v122, v122, v126
	s_nop 1
	v_mov_b32_dpp v126, v122 row_half_mirror row_mask:0xf bank_mask:0xf
	v_add_f32_e32 v122, v122, v126
	s_nop 1
	v_mov_b32_dpp v126, v122 row_mirror row_mask:0xf bank_mask:0xf
	s_and_saveexec_b64 s[0:1], vcc
	s_cbranch_execz .LBB0_2151
	v_add_f32_e32 v122, v122, v126
	ds_write_b32 v139, v122 offset:768
.LBB0_2151:
	s_or_b64 exec, exec, s[0:1]
	s_nop 1
	v_mov_b32_dpp v122, v123 quad_perm:[1,0,3,2] row_mask:0xf bank_mask:0xf
	v_add_f32_e32 v122, v123, v122
	s_nop 1
	v_mov_b32_dpp v123, v122 quad_perm:[2,3,0,1] row_mask:0xf bank_mask:0xf
	v_add_f32_e32 v122, v122, v123
	s_nop 1
	v_mov_b32_dpp v123, v122 row_half_mirror row_mask:0xf bank_mask:0xf
	v_add_f32_e32 v122, v122, v123
	s_nop 1
	v_mov_b32_dpp v123, v122 row_mirror row_mask:0xf bank_mask:0xf
	s_and_saveexec_b64 s[0:1], vcc
	s_cbranch_execz .LBB0_2153
	v_add_f32_e32 v122, v122, v123
	ds_write_b32 v139, v122 offset:772
.LBB0_2153:
	s_or_b64 exec, exec, s[0:1]
	s_nop 1
	v_mov_b32_dpp v122, v124 quad_perm:[1,0,3,2] row_mask:0xf bank_mask:0xf
	v_add_f32_e32 v122, v124, v122
	s_nop 1
	v_mov_b32_dpp v123, v122 quad_perm:[2,3,0,1] row_mask:0xf bank_mask:0xf
	v_add_f32_e32 v122, v122, v123
	s_nop 1
	v_mov_b32_dpp v123, v122 row_half_mirror row_mask:0xf bank_mask:0xf
	v_add_f32_e32 v122, v122, v123
	s_nop 1
	v_mov_b32_dpp v123, v122 row_mirror row_mask:0xf bank_mask:0xf
	s_and_saveexec_b64 s[0:1], vcc
	s_cbranch_execz .LBB0_2155
	v_add_f32_e32 v122, v122, v123
	ds_write_b32 v139, v122 offset:776
.LBB0_2155:
	s_or_b64 exec, exec, s[0:1]
	s_nop 1
	v_mov_b32_dpp v122, v125 quad_perm:[1,0,3,2] row_mask:0xf bank_mask:0xf
	v_add_f32_e32 v122, v125, v122
	s_nop 1
	v_mov_b32_dpp v123, v122 quad_perm:[2,3,0,1] row_mask:0xf bank_mask:0xf
	v_add_f32_e32 v122, v122, v123
	s_nop 1
	v_mov_b32_dpp v123, v122 row_half_mirror row_mask:0xf bank_mask:0xf
	v_add_f32_e32 v122, v122, v123
	s_nop 1
	v_mov_b32_dpp v123, v122 row_mirror row_mask:0xf bank_mask:0xf
	s_and_saveexec_b64 s[0:1], vcc
	s_cbranch_execz .LBB0_2157
	v_add_f32_e32 v122, v122, v123
	ds_write_b32 v139, v122 offset:780

.LBB0_2514:
	v_cvt_f32_i32_e32 v161, v135
	v_cvt_f32_i32_e32 v160, v134
	v_cvt_f32_i32_e32 v165, v137
	v_cvt_f32_i32_e32 v164, v136
	v_cvt_f32_i32_e32 v159, v131
	v_cvt_f32_i32_e32 v158, v130
	v_cvt_f32_i32_e32 v163, v133
	v_cvt_f32_i32_e32 v162, v132
	s_mov_b64 s[0:1], -1
	s_cmp_lt_i32 s28, 16
	v_mul_f32_e32 v156, v218, v229
	s_cbranch_scc0 .LBB0_2585
	v_and_b32_e32 v123, 64, v234
	v_pk_mul_f32 v[124:125], v[156:157], v[164:165] op_sel_hi:[0,1]
	v_pk_mul_f32 v[126:127], v[156:157], v[160:161] op_sel_hi:[0,1]
	v_add_u32_e32 v155, 64, v123
	v_pk_mul_f32 v[138:139], v[156:157], v[158:159] op_sel_hi:[0,1]
	v_mul_f32_e32 v123, v127, v127
	v_mul_f32_e32 v125, v125, v125
	v_fmac_f32_e32 v123, v126, v126
	v_fmac_f32_e32 v125, v124, v124
	v_mul_f32_e32 v124, v139, v139
	v_xor_b32_e32 v122, 16, v234
	v_pk_mul_f32 v[128:129], v[156:157], v[162:163] op_sel_hi:[0,1]
	v_add_f32_e32 v123, v123, v125
	v_fmac_f32_e32 v124, v138, v138
	v_cmp_lt_i32_e32 vcc, v122, v155
	v_add_f32_e32 v123, v124, v123
	v_mul_f32_e32 v124, v129, v129
	v_cndmask_b32_e32 v122, v234, v122, vcc
	v_fmac_f32_e32 v124, v128, v128
	v_lshlrev_b32_e32 v122, 2, v122
	v_add_f32_e32 v123, v124, v123
	v_mov_b32_e32 v125, v123
	s_nop 1
	v_permlane16_swap_b32_e32 v125, v123
	v_xor_b32_e32 v124, 32, v234
	v_cmp_lt_i32_e32 vcc, v124, v155
	v_lshlrev_b32_e32 v146, 5, v190
	s_waitcnt lgkmcnt(0)
	v_add_f32_e32 v125, v123, v125
	v_cndmask_b32_e32 v124, v234, v124, vcc
	v_lshlrev_b32_e32 v124, 2, v124
	v_mov_b32_e32 v126, v125
	s_nop 1
	v_permlane32_swap_b32_e32 v126, v125
	v_cmp_eq_u32_e32 vcc, 0, v188
	v_add_u32_e32 v123, s59, v146
	s_and_saveexec_b64 s[0:1], vcc
	s_cbranch_execz .LBB0_2517
	v_add_f32_e32 v125, v125, v126
	ds_write_b32 v123, v125

.LBB0_2547:
	s_or_b64 exec, exec, s[0:1]
	v_readlane_b32 s68, v254, 24
	v_lshl_add_u32 v168, v188, 2, s58
	s_cmp_gt_i32 s28, 7
	v_readlane_b32 s78, v254, 34
	v_readlane_b32 s79, v254, 35
	v_readlane_b32 s80, v254, 36
	v_readlane_b32 s81, v254, 37
	v_ashrrev_i32_e32 v169, 31, v168
	v_lshlrev_b32_e32 v138, 8, v154
	s_cselect_b32 s0, s80, s78
	s_cselect_b32 s1, s81, s79
	v_lshlrev_b64 v[172:173], 2, v[168:169]
	v_and_b32_e32 v202, 0x7ff00, v138
	s_waitcnt lgkmcnt(0)
	s_barrier
	s_mov_b64 s[98:99], 0x1000
	s_mov_b64 s[100:101], 0x5000
	v_lshl_add_u64 v[122:123], s[0:1], 0, v[172:173]
	v_lshl_add_u64 v[138:139], s[8:9], 0, v[202:203]
	v_lshl_add_u64 v[142:143], s[16:17], 0, v[202:203]
	global_load_dwordx4 v[126:129], v[122:123], off
	s_waitcnt lgkmcnt(0)
	global_load_dwordx4 v[122:125], v[122:123], off offset:256
	v_lshl_add_u64 v[138:139], v[138:139], 0, v[172:173]
	v_lshl_add_u64 v[142:143], v[142:143], 0, v[172:173]
	v_lshl_add_u64 v[244:245], v[138:139], 0, s[98:99]
	v_lshl_add_u64 v[250:251], v[142:143], 0, s[98:99]
	global_load_dwordx4 v[138:141], v[138:139], off
	s_cselect_b32 s2, 0x800, 0
	global_load_dwordx4 v[142:145], v[142:143], off
	global_load_dwordx4 v[244:247], v[244:245], off
	global_load_dwordx4 v[250:253], v[250:251], off
	s_lshl_b32 s21, s28, 8
	s_and_b32 s21, s21, 0x700
	s_or_b32 s2, s2, s21
	s_add_i32 s21, 0, 0x20000
	v_add_u32_e32 v157, s21, v146
	ds_read_b128 v[146:149], v157
	v_mov_b64_e32 v[176:177], s[6:7]
	v_cvt_f32_i32_e32 v131, v131
	v_cvt_f32_i32_e32 v130, v130
	s_waitcnt lgkmcnt(0)
	v_mov_b32_e32 v150, v147
	v_mov_b32_e32 v151, v148
	v_mov_b32_e32 v147, v149
	v_pk_add_f32 v[146:147], v[150:151], v[146:147]
	v_cvt_f32_i32_e32 v133, v133
	v_add_f32_e32 v146, v146, v147
	v_fmamk_f32 v146, v146, 0x3c000000, v230
	v_cmp_gt_f32_e32 vcc, s63, v146
	v_mul_f32_e32 v147, 0x4f800000, v146
	v_cvt_f32_i32_e32 v132, v132
	v_cndmask_b32_e32 v146, v146, v147, vcc
	v_sqrt_f32_e32 v147, v146
	v_cvt_f32_i32_e32 v137, v137
	v_cvt_f32_i32_e32 v136, v136
	v_cvt_f32_i32_e32 v135, v135
	v_add_u32_e32 v148, -1, v147
	v_fma_f32 v149, -v148, v147, v146
	v_cmp_ge_f32_e64 s[0:1], 0, v149
	v_add_u32_e32 v149, 1, v147
	v_cvt_f32_i32_e32 v134, v134
	v_cndmask_b32_e64 v148, v147, v148, s[0:1]
	v_fma_f32 v147, -v149, v147, v146
	v_cmp_lt_f32_e64 s[0:1], 0, v147
	s_lshl_b32 s2, s2, 1
	v_mov_b64_e32 v[216:217], v[112:113]
	v_cndmask_b32_e64 v147, v148, v149, s[0:1]
	v_mul_f32_e32 v148, 0x37800000, v147
	v_cndmask_b32_e32 v147, v147, v148, vcc
	v_cmp_class_f32_e32 vcc, v146, v231
	v_mad_i64_i32 v[178:179], s[0:1], v154, s64, v[176:177]
	s_nop 0
	v_cndmask_b32_e32 v146, v147, v146, vcc
	v_div_scale_f32 v147, s[0:1], v146, v146, 1.0
	v_rcp_f32_e32 v148, v147
	v_lshl_add_u64 v[192:193], v[178:179], 0, s[2:3]
	v_lshlrev_b64 v[178:179], 1, v[168:169]
	v_lshl_add_u64 v[192:193], v[192:193], 0, v[178:179]
	v_fma_f32 v149, -v147, v148, 1.0
	v_fmac_f32_e32 v148, v149, v148
	v_div_scale_f32 v149, vcc, 1.0, v146, 1.0
	v_mul_f32_e32 v150, v149, v148
	v_fma_f32 v151, -v147, v150, v149
	v_fmac_f32_e32 v150, v151, v148
	v_fma_f32 v147, -v147, v150, v149
	v_div_fmas_f32 v147, v147, v148, v150
	v_div_fixup_f32 v146, v147, v146, 1.0
	v_mul_f32_e32 v146, v156, v146
	v_pk_mul_f32 v[132:133], v[146:147], v[132:133] op_sel_hi:[0,1]
	v_pk_mul_f32 v[130:131], v[146:147], v[130:131] op_sel_hi:[0,1]
	v_pk_mul_f32 v[134:135], v[146:147], v[134:135] op_sel_hi:[0,1]
	v_pk_mul_f32 v[136:137], v[146:147], v[136:137] op_sel_hi:[0,1]
	v_mov_b64_e32 v[214:215], v[110:111]
	s_cmp_lt_i32 s28, 8
	v_readlane_b32 s69, v254, 25
	v_readlane_b32 s70, v254, 26
	v_readlane_b32 s71, v254, 27
	v_readlane_b32 s72, v254, 28
	v_readlane_b32 s73, v254, 29
	v_readlane_b32 s74, v254, 30
	v_readlane_b32 s75, v254, 31
	v_readlane_b32 s76, v254, 32
	s_waitcnt vmcnt(2)
	v_pk_mul_f32 v[136:137], v[128:129], v[136:137]
	v_pk_mul_f32 v[130:131], v[122:123], v[130:131]
	v_pk_mul_f32 v[132:133], v[124:125], v[132:133]
	v_pk_mul_f32 v[134:135], v[126:127], v[134:135]
	v_readlane_b32 s77, v254, 33
	v_readlane_b32 s82, v254, 38
	v_pk_mul_f32 v[146:147], v[144:145], v[132:133]
	v_pk_mul_f32 v[148:149], v[142:143], v[130:131]
	v_pk_fma_f32 v[146:147], v[140:141], v[136:137], v[146:147] neg_lo:[0,0,1] neg_hi:[0,0,1]
	v_pk_fma_f32 v[148:149], v[138:139], v[134:135], v[148:149] neg_lo:[0,0,1] neg_hi:[0,0,1]
	v_pk_mul_f32 v[136:137], v[144:145], v[136:137]
	v_pk_mul_f32 v[134:135], v[142:143], v[134:135]
	v_pk_fma_f32 v[152:153], v[140:141], v[132:133], v[136:137]
	v_pk_fma_f32 v[150:151], v[138:139], v[130:131], v[134:135]
	v_pk_add_f32 v[136:137], v[146:147], 0 op_sel_hi:[1,0]
	v_pk_add_f32 v[134:135], v[148:149], 0 op_sel_hi:[1,0]
	v_pk_add_f32 v[132:133], v[152:153], 0 op_sel_hi:[1,0]
	v_pk_add_f32 v[130:131], v[150:151], 0 op_sel_hi:[1,0]
	v_readlane_b32 s83, v254, 39
	v_cvt_pk_bf16_f32 v148, v148, v149
	v_cvt_pk_bf16_f32 v149, v146, v147
	v_cvt_pk_bf16_f32 v146, v150, v151
	v_cvt_pk_bf16_f32 v147, v152, v153
	global_store_dwordx2 v[192:193], v[148:149], off
	global_store_dwordx2 v[192:193], v[146:147], off offset:128
	ds_read_b128 v[146:149], v157 offset:16
	s_waitcnt lgkmcnt(0)
	v_mov_b32_e32 v150, v147
	v_mov_b32_e32 v151, v148
	v_mov_b32_e32 v147, v149
	v_pk_add_f32 v[146:147], v[150:151], v[146:147]
	s_nop 0
	v_add_f32_e32 v146, v146, v147
	v_fmamk_f32 v146, v146, 0x3c000000, v230
	v_cmp_gt_f32_e32 vcc, s63, v146
	v_mul_f32_e32 v147, 0x4f800000, v146
	s_nop 0
	v_cndmask_b32_e32 v146, v146, v147, vcc
	v_sqrt_f32_e32 v147, v146
	s_nop 0
	v_add_u32_e32 v148, -1, v147
	v_fma_f32 v149, -v148, v147, v146
	v_cmp_ge_f32_e64 s[0:1], 0, v149
	v_add_u32_e32 v149, 1, v147
	s_nop 0
	v_cndmask_b32_e64 v148, v147, v148, s[0:1]
	v_fma_f32 v147, -v149, v147, v146
	v_cmp_lt_f32_e64 s[0:1], 0, v147
	s_nop 1
	v_cndmask_b32_e64 v147, v148, v149, s[0:1]
	v_mul_f32_e32 v148, 0x37800000, v147
	v_cndmask_b32_e32 v147, v147, v148, vcc
	v_cmp_class_f32_e32 vcc, v146, v231
	s_nop 1
	v_cndmask_b32_e32 v146, v147, v146, vcc
	v_div_scale_f32 v147, s[0:1], v146, v146, 1.0
	v_rcp_f32_e32 v148, v147
	s_nop 0
	v_fma_f32 v149, -v147, v148, 1.0
	v_fmac_f32_e32 v148, v149, v148
	v_div_scale_f32 v149, vcc, 1.0, v146, 1.0
	v_mul_f32_e32 v150, v149, v148
	v_fma_f32 v151, -v147, v150, v149
	v_fmac_f32_e32 v150, v151, v148
	v_fma_f32 v147, -v147, v150, v149
	v_div_fmas_f32 v147, v147, v148, v150
	v_div_fixup_f32 v157, v147, v146, 1.0
	v_mov_b64_e32 v[148:149], v[120:121]
	v_mov_b64_e32 v[152:153], v[116:117]
	v_mov_b64_e32 v[146:147], v[118:119]
	v_mov_b64_e32 v[150:151], v[114:115]
	v_mul_f32_e32 v202, v156, v157
	v_cvt_f32_i32_e32 v149, v149
	v_cvt_f32_i32_e32 v148, v148
	v_cvt_f32_i32_e32 v147, v147
	v_cvt_f32_i32_e32 v146, v146
	v_cvt_f32_i32_e32 v151, v151
	v_cvt_f32_i32_e32 v150, v150
	v_cvt_f32_i32_e32 v153, v153
	v_cvt_f32_i32_e32 v152, v152
	v_pk_mul_f32 v[146:147], v[202:203], v[146:147] op_sel_hi:[0,1]
	v_pk_mul_f32 v[148:149], v[202:203], v[148:149] op_sel_hi:[0,1]
	v_pk_mul_f32 v[150:151], v[202:203], v[150:151] op_sel_hi:[0,1]
	v_pk_mul_f32 v[152:153], v[202:203], v[152:153] op_sel_hi:[0,1]
	v_pk_mul_f32 v[148:149], v[128:129], v[148:149]
	v_pk_mul_f32 v[146:147], v[126:127], v[146:147]
	v_pk_mul_f32 v[150:151], v[122:123], v[150:151]
	v_pk_mul_f32 v[152:153], v[124:125], v[152:153]
	v_pk_mul_f32 v[212:213], v[142:143], v[150:151]
	v_pk_mul_f32 v[210:211], v[144:145], v[152:153]
	v_pk_mul_f32 v[144:145], v[144:145], v[148:149]
	v_pk_mul_f32 v[142:143], v[142:143], v[146:147]
	v_pk_fma_f32 v[212:213], v[138:139], v[146:147], v[212:213] neg_lo:[0,0,1] neg_hi:[0,0,1]
	v_pk_fma_f32 v[210:211], v[140:141], v[148:149], v[210:211] neg_lo:[0,0,1] neg_hi:[0,0,1]
	v_pk_fma_f32 v[146:147], v[138:139], v[150:151], v[142:143]
	v_pk_fma_f32 v[148:149], v[140:141], v[152:153], v[144:145]
	v_pk_add_f32 v[144:145], v[210:211], 0 op_sel_hi:[1,0]
	v_pk_add_f32 v[142:143], v[212:213], 0 op_sel_hi:[1,0]
	v_pk_add_f32 v[140:141], v[148:149], 0 op_sel_hi:[1,0]
	v_pk_add_f32 v[138:139], v[146:147], 0 op_sel_hi:[1,0]
	v_add_u32_e32 v157, 16, v190
	v_cvt_pk_bf16_f32 v150, v212, v213
	v_cvt_pk_bf16_f32 v151, v210, v211
	v_cvt_pk_bf16_f32 v146, v146, v147
	v_add_u32_e32 v167, s19, v157
	v_cvt_pk_bf16_f32 v147, v148, v149
	global_store_dwordx2 v[192:193], v[150:151], off offset:256
	global_store_dwordx2 v[192:193], v[146:147], off offset:384
	v_lshlrev_b32_e32 v146, 8, v167
	v_and_b32_e32 v202, 0x7ff00, v146
	v_lshl_add_u64 v[146:147], s[8:9], 0, v[202:203]
	v_lshl_add_u64 v[150:151], s[16:17], 0, v[202:203]
	v_lshl_add_u64 v[146:147], v[146:147], 0, v[172:173]
	v_lshl_add_u64 v[150:151], v[150:151], 0, v[172:173]
	s_waitcnt vmcnt(4)
	v_mov_b32_e32 v148, v246
	v_mov_b32_e32 v149, v247
	v_lshl_add_u64 v[246:247], v[146:147], 0, s[98:99]
	v_mov_b32_e32 v146, v244
	v_mov_b32_e32 v147, v245
	global_load_dwordx4 v[244:247], v[246:247], off
	v_lshl_add_u32 v157, v157, 5, s21
	v_mov_b32_e32 v152, v252
	v_mov_b32_e32 v153, v253
	v_lshl_add_u64 v[252:253], v[150:151], 0, s[98:99]
	v_mov_b32_e32 v150, v250
	v_mov_b32_e32 v151, v251
	global_load_dwordx4 v[250:253], v[252:253], off
	ds_read_b128 v[210:213], v157
	s_waitcnt lgkmcnt(0)
	v_mov_b32_e32 v192, v211
	v_mov_b32_e32 v193, v212
	v_mov_b32_e32 v211, v213
	v_pk_add_f32 v[192:193], v[192:193], v[210:211]
	v_mov_b64_e32 v[212:213], v[108:109]
	v_add_f32_e32 v169, v192, v193
	v_fmamk_f32 v169, v169, 0x3c000000, v230
	v_cmp_gt_f32_e32 vcc, s63, v169
	v_mul_f32_e32 v171, 0x4f800000, v169
	v_mov_b64_e32 v[210:211], v[106:107]
	v_cndmask_b32_e32 v169, v169, v171, vcc
	v_sqrt_f32_e32 v171, v169
	s_nop 0
	v_cvt_f32_i32_e32 v211, v211
	v_add_u32_e32 v175, -1, v171
	v_fma_f32 v181, -v175, v171, v169
	v_cmp_ge_f32_e64 s[0:1], 0, v181
	v_add_u32_e32 v181, 1, v171
	v_cvt_f32_i32_e32 v210, v210
	v_cndmask_b32_e64 v175, v171, v175, s[0:1]
	v_fma_f32 v171, -v181, v171, v169
	v_cmp_lt_f32_e64 s[0:1], 0, v171
	v_cvt_f32_i32_e32 v213, v213
	v_cvt_f32_i32_e32 v212, v212
	v_cndmask_b32_e64 v171, v175, v181, s[0:1]
	v_mul_f32_e32 v175, 0x37800000, v171
	v_cndmask_b32_e32 v171, v171, v175, vcc
	v_cmp_class_f32_e32 vcc, v169, v231
	v_cvt_f32_i32_e32 v193, v217
	v_cvt_f32_i32_e32 v192, v216
	v_cndmask_b32_e32 v169, v171, v169, vcc
	v_div_scale_f32 v171, s[0:1], v169, v169, 1.0
	v_rcp_f32_e32 v175, v171
	v_cvt_f32_i32_e32 v215, v215
	v_cvt_f32_i32_e32 v214, v214
	v_fma_f32 v181, -v171, v175, 1.0
	v_fmac_f32_e32 v175, v181, v175
	v_div_scale_f32 v181, vcc, 1.0, v169, 1.0
	v_mul_f32_e32 v183, v181, v175
	v_fma_f32 v185, -v171, v183, v181
	v_fmac_f32_e32 v183, v185, v175
	v_fma_f32 v171, -v171, v183, v181
	v_div_fmas_f32 v171, v171, v175, v183
	v_div_fixup_f32 v169, v171, v169, 1.0
	v_mul_f32_e32 v202, v186, v169
	v_pk_mul_f32 v[212:213], v[202:203], v[212:213] op_sel_hi:[0,1]
	v_pk_mul_f32 v[210:211], v[202:203], v[210:211] op_sel_hi:[0,1]
	v_pk_mul_f32 v[214:215], v[202:203], v[214:215] op_sel_hi:[0,1]
	v_pk_mul_f32 v[192:193], v[202:203], v[192:193] op_sel_hi:[0,1]
	v_pk_mul_f32 v[210:211], v[122:123], v[210:211]
	v_pk_mul_f32 v[212:213], v[124:125], v[212:213]
	v_pk_mul_f32 v[192:193], v[128:129], v[192:193]
	v_pk_mul_f32 v[214:215], v[126:127], v[214:215]
	v_pk_mul_f32 v[216:217], v[152:153], v[212:213]
	v_pk_mul_f32 v[236:237], v[150:151], v[210:211]
	v_pk_fma_f32 v[216:217], v[148:149], v[192:193], v[216:217] neg_lo:[0,0,1] neg_hi:[0,0,1]
	v_pk_fma_f32 v[236:237], v[146:147], v[214:215], v[236:237] neg_lo:[0,0,1] neg_hi:[0,0,1]
	v_pk_mul_f32 v[192:193], v[152:153], v[192:193]
	v_pk_mul_f32 v[214:215], v[150:151], v[214:215]
	v_pk_fma_f32 v[192:193], v[148:149], v[212:213], v[192:193]
	v_pk_fma_f32 v[210:211], v[146:147], v[210:211], v[214:215]
	v_mad_i64_i32 v[212:213], s[0:1], v167, s64, v[176:177]
	v_pk_add_f32 v[136:137], v[136:137], v[216:217]
	v_pk_add_f32 v[134:135], v[134:135], v[236:237]
	v_pk_add_f32 v[132:133], v[132:133], v[192:193]
	v_pk_add_f32 v[130:131], v[130:131], v[210:211]
	v_lshl_add_u64 v[212:213], v[212:213], 0, s[2:3]
	v_lshl_add_u64 v[238:239], v[212:213], 0, v[178:179]
	v_cvt_pk_bf16_f32 v212, v236, v237
	v_cvt_pk_bf16_f32 v213, v216, v217
	v_cvt_pk_bf16_f32 v210, v210, v211
	v_cvt_pk_bf16_f32 v211, v192, v193
	global_store_dwordx2 v[238:239], v[212:213], off
	global_store_dwordx2 v[238:239], v[210:211], off offset:128
	ds_read_b128 v[210:213], v157 offset:16
	v_mov_b64_e32 v[216:217], v[104:105]
	v_mov_b64_e32 v[214:215], v[102:103]
	s_waitcnt lgkmcnt(0)
	v_mov_b32_e32 v192, v211
	v_mov_b32_e32 v193, v212
	v_mov_b32_e32 v211, v213
	v_pk_add_f32 v[192:193], v[192:193], v[210:211]
	v_mov_b64_e32 v[212:213], v[100:101]
	v_add_f32_e32 v157, v192, v193
	v_fmamk_f32 v157, v157, 0x3c000000, v230
	v_cmp_gt_f32_e32 vcc, s63, v157
	v_mul_f32_e32 v167, 0x4f800000, v157
	v_mov_b64_e32 v[210:211], v[98:99]
	v_cndmask_b32_e32 v157, v157, v167, vcc
	v_sqrt_f32_e32 v167, v157
	s_nop 0
	v_cvt_f32_i32_e32 v193, v217
	v_add_u32_e32 v169, -1, v167
	v_fma_f32 v171, -v169, v167, v157
	v_cmp_ge_f32_e64 s[0:1], 0, v171
	v_add_u32_e32 v171, 1, v167
	v_cvt_f32_i32_e32 v192, v216
	v_cndmask_b32_e64 v169, v167, v169, s[0:1]
	v_fma_f32 v167, -v171, v167, v157
	v_cmp_lt_f32_e64 s[0:1], 0, v167
	v_cvt_f32_i32_e32 v215, v215
	v_cvt_f32_i32_e32 v214, v214
	v_cndmask_b32_e64 v167, v169, v171, s[0:1]
	v_mul_f32_e32 v169, 0x37800000, v167
	v_cndmask_b32_e32 v167, v167, v169, vcc
	v_cmp_class_f32_e32 vcc, v157, v231
	v_cvt_f32_i32_e32 v211, v211
	v_cvt_f32_i32_e32 v210, v210
	v_cndmask_b32_e32 v157, v167, v157, vcc
	v_div_scale_f32 v167, s[0:1], v157, v157, 1.0
	v_rcp_f32_e32 v169, v167
	v_cvt_f32_i32_e32 v213, v213
	v_cvt_f32_i32_e32 v212, v212
	v_fma_f32 v171, -v167, v169, 1.0
	v_fmac_f32_e32 v169, v171, v169
	v_div_scale_f32 v171, vcc, 1.0, v157, 1.0
	v_mul_f32_e32 v175, v171, v169
	v_fma_f32 v181, -v167, v175, v171
	v_fmac_f32_e32 v175, v181, v169
	v_fma_f32 v167, -v167, v175, v171
	v_div_fmas_f32 v167, v167, v169, v175
	v_div_fixup_f32 v157, v167, v157, 1.0
	v_mul_f32_e32 v186, v186, v157
	v_pk_mul_f32 v[214:215], v[186:187], v[214:215] op_sel_hi:[0,1]
	v_pk_mul_f32 v[192:193], v[186:187], v[192:193] op_sel_hi:[0,1]
	v_pk_mul_f32 v[212:213], v[186:187], v[212:213] op_sel_hi:[0,1]
	v_pk_mul_f32 v[186:187], v[186:187], v[210:211] op_sel_hi:[0,1]
	v_pk_mul_f32 v[192:193], v[128:129], v[192:193]
	v_pk_mul_f32 v[214:215], v[126:127], v[214:215]
	v_pk_mul_f32 v[186:187], v[122:123], v[186:187]
	v_pk_mul_f32 v[210:211], v[124:125], v[212:213]
	v_pk_mul_f32 v[216:217], v[150:151], v[186:187]
	v_pk_mul_f32 v[212:213], v[152:153], v[210:211]
	v_pk_mul_f32 v[152:153], v[152:153], v[192:193]
	v_pk_mul_f32 v[150:151], v[150:151], v[214:215]
	v_pk_fma_f32 v[216:217], v[146:147], v[214:215], v[216:217] neg_lo:[0,0,1] neg_hi:[0,0,1]
	v_pk_fma_f32 v[212:213], v[148:149], v[192:193], v[212:213] neg_lo:[0,0,1] neg_hi:[0,0,1]
	v_pk_fma_f32 v[146:147], v[146:147], v[186:187], v[150:151]
	v_pk_fma_f32 v[148:149], v[148:149], v[210:211], v[152:153]
	v_pk_add_f32 v[144:145], v[144:145], v[212:213]
	v_pk_add_f32 v[142:143], v[142:143], v[216:217]
	v_pk_add_f32 v[140:141], v[140:141], v[148:149]
	v_pk_add_f32 v[138:139], v[138:139], v[146:147]
	v_add_u32_e32 v157, 32, v190
	v_cvt_pk_bf16_f32 v150, v216, v217
	v_cvt_pk_bf16_f32 v151, v212, v213
	v_cvt_pk_bf16_f32 v146, v146, v147
	v_add_u32_e32 v167, s19, v157
	v_cvt_pk_bf16_f32 v147, v148, v149
	global_store_dwordx2 v[238:239], v[150:151], off offset:256
	global_store_dwordx2 v[238:239], v[146:147], off offset:384
	v_lshlrev_b32_e32 v146, 8, v167
	v_and_b32_e32 v202, 0x7ff00, v146
	v_lshl_add_u64 v[146:147], s[8:9], 0, v[202:203]
	v_lshl_add_u64 v[150:151], s[16:17], 0, v[202:203]
	v_lshl_add_u64 v[146:147], v[146:147], 0, v[172:173]
	v_lshl_add_u64 v[150:151], v[150:151], 0, v[172:173]
	s_waitcnt vmcnt(4)
	v_mov_b32_e32 v148, v246
	v_mov_b32_e32 v149, v247
	v_lshl_add_u64 v[246:247], v[146:147], 0, s[98:99]
	v_mov_b32_e32 v146, v244
	v_mov_b32_e32 v147, v245
	global_load_dwordx4 v[244:247], v[246:247], off
	v_lshl_add_u32 v157, v157, 5, s21
	v_mov_b32_e32 v152, v252
	v_mov_b32_e32 v153, v253
	v_lshl_add_u64 v[252:253], v[150:151], 0, s[98:99]
	v_mov_b32_e32 v150, v250
	v_mov_b32_e32 v151, v251
	global_load_dwordx4 v[250:253], v[252:253], off
	ds_read_b128 v[210:213], v157
	v_mov_b64_e32 v[216:217], v[92:93]
	v_mov_b64_e32 v[214:215], v[90:91]
	s_waitcnt lgkmcnt(0)
	v_mov_b32_e32 v186, v211
	v_mov_b32_e32 v187, v212
	v_mov_b32_e32 v211, v213
	v_pk_add_f32 v[186:187], v[186:187], v[210:211]
	v_mov_b64_e32 v[212:213], v[96:97]
	v_add_f32_e32 v169, v186, v187
	v_fmamk_f32 v169, v169, 0x3c000000, v230
	v_cmp_gt_f32_e32 vcc, s63, v169
	v_mul_f32_e32 v171, 0x4f800000, v169
	v_mov_b64_e32 v[210:211], v[94:95]
	v_cndmask_b32_e32 v169, v169, v171, vcc
	v_sqrt_f32_e32 v171, v169
	s_nop 0
	v_cvt_f32_i32_e32 v187, v213
	v_add_u32_e32 v175, -1, v171
	v_fma_f32 v181, -v175, v171, v169
	v_cmp_ge_f32_e64 s[0:1], 0, v181
	v_add_u32_e32 v181, 1, v171
	v_cvt_f32_i32_e32 v186, v212
	v_cndmask_b32_e64 v175, v171, v175, s[0:1]
	v_fma_f32 v171, -v181, v171, v169
	v_cmp_lt_f32_e64 s[0:1], 0, v171
	v_cvt_f32_i32_e32 v193, v211
	v_cvt_f32_i32_e32 v192, v210
	v_cndmask_b32_e64 v171, v175, v181, s[0:1]
	v_mul_f32_e32 v175, 0x37800000, v171
	v_cndmask_b32_e32 v171, v171, v175, vcc
	v_cmp_class_f32_e32 vcc, v169, v231
	v_cvt_f32_i32_e32 v211, v215
	v_cvt_f32_i32_e32 v210, v214
	v_cndmask_b32_e32 v169, v171, v169, vcc
	v_div_scale_f32 v171, s[0:1], v169, v169, 1.0
	v_rcp_f32_e32 v175, v171
	v_cvt_f32_i32_e32 v213, v217
	v_cvt_f32_i32_e32 v212, v216
	v_fma_f32 v181, -v171, v175, 1.0
	v_fmac_f32_e32 v175, v181, v175
	v_div_scale_f32 v181, vcc, 1.0, v169, 1.0
	v_mul_f32_e32 v183, v181, v175
	v_fma_f32 v185, -v171, v183, v181
	v_fmac_f32_e32 v183, v185, v175
	v_fma_f32 v171, -v171, v183, v181
	v_div_fmas_f32 v171, v171, v175, v183
	v_div_fixup_f32 v169, v171, v169, 1.0
	v_mul_f32_e32 v202, v184, v169
	v_pk_mul_f32 v[212:213], v[202:203], v[212:213] op_sel_hi:[0,1]
	v_pk_mul_f32 v[210:211], v[202:203], v[210:211] op_sel_hi:[0,1]
	v_pk_mul_f32 v[192:193], v[202:203], v[192:193] op_sel_hi:[0,1]
	v_pk_mul_f32 v[186:187], v[202:203], v[186:187] op_sel_hi:[0,1]
	v_pk_mul_f32 v[210:211], v[122:123], v[210:211]
	v_pk_mul_f32 v[212:213], v[124:125], v[212:213]
	v_pk_mul_f32 v[186:187], v[128:129], v[186:187]
	v_pk_mul_f32 v[192:193], v[126:127], v[192:193]
	v_pk_mul_f32 v[214:215], v[152:153], v[212:213]
	v_pk_mul_f32 v[216:217], v[150:151], v[210:211]
	v_pk_fma_f32 v[214:215], v[148:149], v[186:187], v[214:215] neg_lo:[0,0,1] neg_hi:[0,0,1]
	v_pk_fma_f32 v[216:217], v[146:147], v[192:193], v[216:217] neg_lo:[0,0,1] neg_hi:[0,0,1]
	v_pk_mul_f32 v[186:187], v[152:153], v[186:187]
	v_pk_mul_f32 v[192:193], v[150:151], v[192:193]
	v_pk_fma_f32 v[186:187], v[148:149], v[212:213], v[186:187]
	v_pk_fma_f32 v[192:193], v[146:147], v[210:211], v[192:193]
	v_mad_i64_i32 v[210:211], s[0:1], v167, s64, v[176:177]
	v_pk_add_f32 v[136:137], v[136:137], v[214:215]
	v_pk_add_f32 v[134:135], v[134:135], v[216:217]
	v_pk_add_f32 v[132:133], v[132:133], v[186:187]
	v_pk_add_f32 v[130:131], v[130:131], v[192:193]
	v_lshl_add_u64 v[210:211], v[210:211], 0, s[2:3]
	v_lshl_add_u64 v[236:237], v[210:211], 0, v[178:179]
	v_cvt_pk_bf16_f32 v210, v216, v217
	v_cvt_pk_bf16_f32 v211, v214, v215
	v_cvt_pk_bf16_f32 v192, v192, v193
	v_cvt_pk_bf16_f32 v193, v186, v187
	global_store_dwordx2 v[236:237], v[210:211], off
	global_store_dwordx2 v[236:237], v[192:193], off offset:128
	ds_read_b128 v[210:213], v157 offset:16
	v_mov_b64_e32 v[216:217], v[88:89]
	v_mov_b64_e32 v[214:215], v[86:87]
	s_waitcnt lgkmcnt(0)
	v_mov_b32_e32 v186, v211
	v_mov_b32_e32 v187, v212
	v_mov_b32_e32 v211, v213
	v_pk_add_f32 v[186:187], v[186:187], v[210:211]
	v_mov_b64_e32 v[212:213], v[84:85]
	v_add_f32_e32 v157, v186, v187
	v_fmamk_f32 v157, v157, 0x3c000000, v230
	v_cmp_gt_f32_e32 vcc, s63, v157
	v_mul_f32_e32 v167, 0x4f800000, v157
	v_mov_b64_e32 v[210:211], v[82:83]
	v_cndmask_b32_e32 v157, v157, v167, vcc
	v_sqrt_f32_e32 v167, v157
	s_nop 0
	v_cvt_f32_i32_e32 v187, v217
	v_add_u32_e32 v169, -1, v167
	v_fma_f32 v171, -v169, v167, v157
	v_cmp_ge_f32_e64 s[0:1], 0, v171
	v_add_u32_e32 v171, 1, v167
	v_cvt_f32_i32_e32 v186, v216
	v_cndmask_b32_e64 v169, v167, v169, s[0:1]
	v_fma_f32 v167, -v171, v167, v157
	v_cmp_lt_f32_e64 s[0:1], 0, v167
	v_cvt_f32_i32_e32 v193, v215
	v_cvt_f32_i32_e32 v192, v214
	v_cndmask_b32_e64 v167, v169, v171, s[0:1]
	v_mul_f32_e32 v169, 0x37800000, v167
	v_cndmask_b32_e32 v167, v167, v169, vcc
	v_cmp_class_f32_e32 vcc, v157, v231
	v_cvt_f32_i32_e32 v211, v211
	v_cvt_f32_i32_e32 v210, v210
	v_cndmask_b32_e32 v157, v167, v157, vcc
	v_div_scale_f32 v167, s[0:1], v157, v157, 1.0
	v_rcp_f32_e32 v169, v167
	v_cvt_f32_i32_e32 v213, v213
	v_cvt_f32_i32_e32 v212, v212
	v_fma_f32 v171, -v167, v169, 1.0
	v_fmac_f32_e32 v169, v171, v169
	v_div_scale_f32 v171, vcc, 1.0, v157, 1.0
	v_mul_f32_e32 v175, v171, v169
	v_fma_f32 v181, -v167, v175, v171
	v_fmac_f32_e32 v175, v181, v169
	v_fma_f32 v167, -v167, v175, v171
	v_div_fmas_f32 v167, v167, v169, v175
	v_div_fixup_f32 v157, v167, v157, 1.0
	v_mul_f32_e32 v184, v184, v157
	v_pk_mul_f32 v[192:193], v[184:185], v[192:193] op_sel_hi:[0,1]
	v_pk_mul_f32 v[186:187], v[184:185], v[186:187] op_sel_hi:[0,1]
	v_pk_mul_f32 v[212:213], v[184:185], v[212:213] op_sel_hi:[0,1]
	v_pk_mul_f32 v[184:185], v[184:185], v[210:211] op_sel_hi:[0,1]
	v_pk_mul_f32 v[186:187], v[128:129], v[186:187]
	v_pk_mul_f32 v[192:193], v[126:127], v[192:193]
	v_pk_mul_f32 v[184:185], v[122:123], v[184:185]
	v_pk_mul_f32 v[210:211], v[124:125], v[212:213]
	v_pk_mul_f32 v[214:215], v[150:151], v[184:185]
	v_pk_mul_f32 v[212:213], v[152:153], v[210:211]
	v_pk_mul_f32 v[152:153], v[152:153], v[186:187]
	v_pk_mul_f32 v[150:151], v[150:151], v[192:193]
	v_pk_fma_f32 v[214:215], v[146:147], v[192:193], v[214:215] neg_lo:[0,0,1] neg_hi:[0,0,1]
	v_pk_fma_f32 v[212:213], v[148:149], v[186:187], v[212:213] neg_lo:[0,0,1] neg_hi:[0,0,1]
	v_pk_fma_f32 v[146:147], v[146:147], v[184:185], v[150:151]
	v_pk_fma_f32 v[148:149], v[148:149], v[210:211], v[152:153]
	v_pk_add_f32 v[144:145], v[144:145], v[212:213]
	v_pk_add_f32 v[142:143], v[142:143], v[214:215]
	v_pk_add_f32 v[140:141], v[140:141], v[148:149]
	v_pk_add_f32 v[138:139], v[138:139], v[146:147]
	v_add_u32_e32 v157, 48, v190
	v_cvt_pk_bf16_f32 v150, v214, v215
	v_cvt_pk_bf16_f32 v151, v212, v213
	v_cvt_pk_bf16_f32 v146, v146, v147
	v_add_u32_e32 v167, s19, v157
	v_cvt_pk_bf16_f32 v147, v148, v149
	global_store_dwordx2 v[236:237], v[150:151], off offset:256
	global_store_dwordx2 v[236:237], v[146:147], off offset:384
	v_lshlrev_b32_e32 v146, 8, v167
	v_and_b32_e32 v202, 0x7ff00, v146
	v_lshl_add_u64 v[146:147], s[8:9], 0, v[202:203]
	v_lshl_add_u64 v[150:151], s[16:17], 0, v[202:203]
	v_lshl_add_u64 v[146:147], v[146:147], 0, v[172:173]
	v_lshl_add_u64 v[150:151], v[150:151], 0, v[172:173]
	s_waitcnt vmcnt(4)
	v_mov_b32_e32 v148, v246
	v_mov_b32_e32 v149, v247
	v_lshl_add_u64 v[246:247], v[146:147], 0, s[100:101]
	v_mov_b32_e32 v146, v244
	v_mov_b32_e32 v147, v245
	global_load_dwordx4 v[244:247], v[246:247], off
	v_lshl_add_u32 v157, v157, 5, s21
	v_mov_b32_e32 v152, v252
	v_mov_b32_e32 v153, v253
	v_lshl_add_u64 v[252:253], v[150:151], 0, s[100:101]
	v_mov_b32_e32 v150, v250
	v_mov_b32_e32 v151, v251
	global_load_dwordx4 v[250:253], v[252:253], off
	ds_read_b128 v[184:187], v157
	v_mov_b64_e32 v[212:213], v[76:77]
	v_mov_b64_e32 v[210:211], v[74:75]
	s_waitcnt lgkmcnt(0)
	v_mov_b32_e32 v192, v185
	v_mov_b32_e32 v193, v186
	v_mov_b32_e32 v185, v187
	v_pk_add_f32 v[184:185], v[192:193], v[184:185]
	s_nop 0
	v_add_f32_e32 v169, v184, v185
	v_fmamk_f32 v169, v169, 0x3c000000, v230
	v_cmp_gt_f32_e32 vcc, s63, v169
	v_mul_f32_e32 v171, 0x4f800000, v169
	s_nop 0
	v_cndmask_b32_e32 v169, v169, v171, vcc
	v_sqrt_f32_e32 v171, v169
	s_nop 0
	v_add_u32_e32 v175, -1, v171
	v_fma_f32 v181, -v175, v171, v169
	v_cmp_ge_f32_e64 s[0:1], 0, v181
	v_add_u32_e32 v181, 1, v171
	s_nop 0
	v_cndmask_b32_e64 v175, v171, v175, s[0:1]
	v_fma_f32 v171, -v181, v171, v169
	v_cmp_lt_f32_e64 s[0:1], 0, v171
	s_nop 1
	v_cndmask_b32_e64 v171, v175, v181, s[0:1]
	v_mul_f32_e32 v175, 0x37800000, v171
	v_cndmask_b32_e32 v171, v171, v175, vcc
	v_cmp_class_f32_e32 vcc, v169, v231
	s_nop 1
	v_cndmask_b32_e32 v169, v171, v169, vcc
	v_div_scale_f32 v171, s[0:1], v169, v169, 1.0
	v_rcp_f32_e32 v175, v171
	s_nop 0
	v_fma_f32 v181, -v171, v175, 1.0
	v_fmac_f32_e32 v175, v181, v175
	v_div_scale_f32 v181, vcc, 1.0, v169, 1.0
	v_mul_f32_e32 v183, v181, v175
	v_fma_f32 v184, -v171, v183, v181
	v_fmac_f32_e32 v183, v184, v175
	v_mov_b64_e32 v[186:187], v[80:81]
	v_mov_b64_e32 v[184:185], v[78:79]
	v_fma_f32 v171, -v171, v183, v181
	v_cvt_f32_i32_e32 v187, v187
	v_cvt_f32_i32_e32 v186, v186
	v_cvt_f32_i32_e32 v185, v185
	v_cvt_f32_i32_e32 v184, v184
	v_cvt_f32_i32_e32 v211, v211
	v_cvt_f32_i32_e32 v210, v210
	v_cvt_f32_i32_e32 v213, v213
	v_cvt_f32_i32_e32 v212, v212
	v_div_fmas_f32 v171, v171, v175, v183
	v_div_fixup_f32 v169, v171, v169, 1.0
	v_mul_f32_e32 v192, v182, v169
	v_pk_mul_f32 v[184:185], v[192:193], v[184:185] op_sel_hi:[0,1]
	v_pk_mul_f32 v[186:187], v[192:193], v[186:187] op_sel_hi:[0,1]
	v_pk_mul_f32 v[212:213], v[192:193], v[212:213] op_sel_hi:[0,1]
	v_pk_mul_f32 v[192:193], v[192:193], v[210:211] op_sel_hi:[0,1]
	v_pk_mul_f32 v[192:193], v[122:123], v[192:193]
	v_pk_mul_f32 v[210:211], v[124:125], v[212:213]
	v_pk_mul_f32 v[186:187], v[128:129], v[186:187]
	v_pk_mul_f32 v[184:185], v[126:127], v[184:185]
	v_pk_mul_f32 v[212:213], v[152:153], v[210:211]
	v_pk_mul_f32 v[214:215], v[150:151], v[192:193]
	v_pk_fma_f32 v[212:213], v[148:149], v[186:187], v[212:213] neg_lo:[0,0,1] neg_hi:[0,0,1]
	v_pk_fma_f32 v[214:215], v[146:147], v[184:185], v[214:215] neg_lo:[0,0,1] neg_hi:[0,0,1]
	v_pk_mul_f32 v[186:187], v[152:153], v[186:187]
	v_pk_mul_f32 v[184:185], v[150:151], v[184:185]
	v_pk_fma_f32 v[186:187], v[148:149], v[210:211], v[186:187]
	v_pk_fma_f32 v[184:185], v[146:147], v[192:193], v[184:185]
	v_mad_i64_i32 v[192:193], s[0:1], v167, s64, v[176:177]
	v_pk_add_f32 v[136:137], v[136:137], v[212:213]
	v_pk_add_f32 v[134:135], v[134:135], v[214:215]
	v_pk_add_f32 v[132:133], v[132:133], v[186:187]
	v_pk_add_f32 v[130:131], v[130:131], v[184:185]
	v_lshl_add_u64 v[192:193], v[192:193], 0, s[2:3]
	v_lshl_add_u64 v[192:193], v[192:193], 0, v[178:179]
	v_cvt_pk_bf16_f32 v210, v214, v215
	v_cvt_pk_bf16_f32 v211, v212, v213
	v_cvt_pk_bf16_f32 v184, v184, v185
	v_cvt_pk_bf16_f32 v185, v186, v187
	global_store_dwordx2 v[192:193], v[210:211], off
	global_store_dwordx2 v[192:193], v[184:185], off offset:128
	ds_read_b128 v[184:187], v157 offset:16
	s_waitcnt lgkmcnt(0)
	v_mov_b32_e32 v210, v185
	v_mov_b32_e32 v211, v186
	v_mov_b32_e32 v185, v187
	v_pk_add_f32 v[184:185], v[210:211], v[184:185]
	v_mov_b64_e32 v[212:213], v[72:73]
	v_add_f32_e32 v157, v184, v185
	v_fmamk_f32 v157, v157, 0x3c000000, v230
	v_cmp_gt_f32_e32 vcc, s63, v157
	v_mul_f32_e32 v167, 0x4f800000, v157
	v_mov_b64_e32 v[186:187], v[68:69]
	v_cndmask_b32_e32 v157, v157, v167, vcc
	v_sqrt_f32_e32 v167, v157
	v_mov_b64_e32 v[184:185], v[66:67]
	v_mov_b64_e32 v[210:211], v[70:71]
	v_add_u32_e32 v169, -1, v167
	v_fma_f32 v171, -v169, v167, v157
	v_cmp_ge_f32_e64 s[0:1], 0, v171
	v_add_u32_e32 v171, 1, v167
	v_cvt_f32_i32_e32 v213, v213
	v_cndmask_b32_e64 v169, v167, v169, s[0:1]
	v_fma_f32 v167, -v171, v167, v157
	v_cmp_lt_f32_e64 s[0:1], 0, v167
	v_cvt_f32_i32_e32 v212, v212
	v_cvt_f32_i32_e32 v211, v211
	v_cndmask_b32_e64 v167, v169, v171, s[0:1]
	v_mul_f32_e32 v169, 0x37800000, v167
	v_cndmask_b32_e32 v167, v167, v169, vcc
	v_cmp_class_f32_e32 vcc, v157, v231
	v_cvt_f32_i32_e32 v210, v210
	v_cvt_f32_i32_e32 v185, v185
	v_cndmask_b32_e32 v157, v167, v157, vcc
	v_div_scale_f32 v167, s[0:1], v157, v157, 1.0
	v_rcp_f32_e32 v169, v167
	v_cvt_f32_i32_e32 v184, v184
	v_cvt_f32_i32_e32 v187, v187
	v_cvt_f32_i32_e32 v186, v186
	v_fma_f32 v171, -v167, v169, 1.0
	v_fmac_f32_e32 v169, v171, v169
	v_div_scale_f32 v171, vcc, 1.0, v157, 1.0
	v_mul_f32_e32 v175, v171, v169
	v_fma_f32 v181, -v167, v175, v171
	v_fmac_f32_e32 v175, v181, v169
	v_fma_f32 v167, -v167, v175, v171
	v_div_fmas_f32 v167, v167, v169, v175
	v_div_fixup_f32 v157, v167, v157, 1.0
	v_mul_f32_e32 v182, v182, v157
	v_pk_mul_f32 v[210:211], v[182:183], v[210:211] op_sel_hi:[0,1]
	v_pk_mul_f32 v[212:213], v[182:183], v[212:213] op_sel_hi:[0,1]
	v_pk_mul_f32 v[186:187], v[182:183], v[186:187] op_sel_hi:[0,1]
	v_pk_mul_f32 v[182:183], v[182:183], v[184:185] op_sel_hi:[0,1]
	v_pk_mul_f32 v[212:213], v[128:129], v[212:213]
	v_pk_mul_f32 v[210:211], v[126:127], v[210:211]
	v_pk_mul_f32 v[182:183], v[122:123], v[182:183]
	v_pk_mul_f32 v[184:185], v[124:125], v[186:187]
	v_pk_mul_f32 v[214:215], v[150:151], v[182:183]
	v_pk_mul_f32 v[186:187], v[152:153], v[184:185]
	v_pk_mul_f32 v[152:153], v[152:153], v[212:213]
	v_pk_mul_f32 v[150:151], v[150:151], v[210:211]
	v_pk_fma_f32 v[214:215], v[146:147], v[210:211], v[214:215] neg_lo:[0,0,1] neg_hi:[0,0,1]
	v_pk_fma_f32 v[186:187], v[148:149], v[212:213], v[186:187] neg_lo:[0,0,1] neg_hi:[0,0,1]
	v_pk_fma_f32 v[146:147], v[146:147], v[182:183], v[150:151]
	v_pk_fma_f32 v[148:149], v[148:149], v[184:185], v[152:153]
	v_pk_add_f32 v[144:145], v[144:145], v[186:187]
	v_pk_add_f32 v[142:143], v[142:143], v[214:215]
	v_pk_add_f32 v[140:141], v[140:141], v[148:149]
	v_pk_add_f32 v[138:139], v[138:139], v[146:147]
	v_add_u32_e32 v157, 0x80, v190
	v_cvt_pk_bf16_f32 v150, v214, v215
	v_cvt_pk_bf16_f32 v151, v186, v187
	v_cvt_pk_bf16_f32 v146, v146, v147
	v_add_u32_e32 v167, s19, v157
	v_cvt_pk_bf16_f32 v147, v148, v149
	global_store_dwordx2 v[192:193], v[150:151], off offset:256
	global_store_dwordx2 v[192:193], v[146:147], off offset:384
	v_lshlrev_b32_e32 v146, 8, v167
	v_and_b32_e32 v202, 0x7ff00, v146
	v_lshl_add_u64 v[146:147], s[8:9], 0, v[202:203]
	v_lshl_add_u64 v[150:151], s[16:17], 0, v[202:203]
	v_lshl_add_u64 v[146:147], v[146:147], 0, v[172:173]
	v_lshl_add_u64 v[150:151], v[150:151], 0, v[172:173]
	s_waitcnt vmcnt(4)
	v_mov_b32_e32 v148, v246
	v_mov_b32_e32 v149, v247
	v_lshl_add_u64 v[246:247], v[146:147], 0, s[98:99]
	v_mov_b32_e32 v146, v244
	v_mov_b32_e32 v147, v245
	global_load_dwordx4 v[244:247], v[246:247], off
	v_lshl_add_u32 v157, v157, 5, s21
	v_mov_b32_e32 v152, v252
	v_mov_b32_e32 v153, v253
	v_lshl_add_u64 v[252:253], v[150:151], 0, s[98:99]
	v_mov_b32_e32 v150, v250
	v_mov_b32_e32 v151, v251
	global_load_dwordx4 v[250:253], v[252:253], off
	ds_read_b128 v[182:185], v157
	v_mov_b64_e32 v[212:213], v[60:61]
	v_mov_b64_e32 v[210:211], v[58:59]
	s_waitcnt lgkmcnt(0)
	v_mov_b32_e32 v186, v183
	v_mov_b32_e32 v187, v184
	v_mov_b32_e32 v183, v185
	v_pk_add_f32 v[182:183], v[186:187], v[182:183]
	s_nop 0
	v_add_f32_e32 v169, v182, v183
	v_fmamk_f32 v169, v169, 0x3c000000, v230
	v_cmp_gt_f32_e32 vcc, s63, v169
	v_mul_f32_e32 v171, 0x4f800000, v169
	s_nop 0
	v_cndmask_b32_e32 v169, v169, v171, vcc
	v_sqrt_f32_e32 v171, v169
	s_nop 0
	v_add_u32_e32 v175, -1, v171
	v_fma_f32 v181, -v175, v171, v169
	v_cmp_ge_f32_e64 s[0:1], 0, v181
	v_add_u32_e32 v181, 1, v171
	s_nop 0
	v_cndmask_b32_e64 v175, v171, v175, s[0:1]
	v_fma_f32 v171, -v181, v171, v169
	v_cmp_lt_f32_e64 s[0:1], 0, v171
	s_nop 1
	v_cndmask_b32_e64 v171, v175, v181, s[0:1]
	v_mul_f32_e32 v175, 0x37800000, v171
	v_cndmask_b32_e32 v171, v171, v175, vcc
	v_cmp_class_f32_e32 vcc, v169, v231
	s_nop 1
	v_cndmask_b32_e32 v169, v171, v169, vcc
	v_div_scale_f32 v171, s[0:1], v169, v169, 1.0
	v_rcp_f32_e32 v175, v171
	s_nop 0
	v_fma_f32 v181, -v171, v175, 1.0
	v_fmac_f32_e32 v175, v181, v175
	v_div_scale_f32 v181, vcc, 1.0, v169, 1.0
	v_mul_f32_e32 v182, v181, v175
	v_fma_f32 v183, -v171, v182, v181
	v_fmac_f32_e32 v182, v183, v175
	v_fma_f32 v171, -v171, v182, v181
	v_div_fmas_f32 v171, v171, v175, v182
	v_mov_b64_e32 v[184:185], v[64:65]
	v_mov_b64_e32 v[182:183], v[62:63]
	v_div_fixup_f32 v169, v171, v169, 1.0
	v_cvt_f32_i32_e32 v185, v185
	v_cvt_f32_i32_e32 v184, v184
	v_cvt_f32_i32_e32 v183, v183
	v_cvt_f32_i32_e32 v182, v182
	v_cvt_f32_i32_e32 v193, v211
	v_cvt_f32_i32_e32 v192, v210
	v_cvt_f32_i32_e32 v211, v213
	v_cvt_f32_i32_e32 v210, v212
	v_mul_f32_e32 v186, v180, v169
	v_pk_mul_f32 v[182:183], v[186:187], v[182:183] op_sel_hi:[0,1]
	v_pk_mul_f32 v[184:185], v[186:187], v[184:185] op_sel_hi:[0,1]
	v_pk_mul_f32 v[210:211], v[186:187], v[210:211] op_sel_hi:[0,1]
	v_pk_mul_f32 v[186:187], v[186:187], v[192:193] op_sel_hi:[0,1]
	v_pk_mul_f32 v[186:187], v[122:123], v[186:187]
	v_pk_mul_f32 v[192:193], v[124:125], v[210:211]
	v_pk_mul_f32 v[184:185], v[128:129], v[184:185]
	v_pk_mul_f32 v[182:183], v[126:127], v[182:183]
	v_pk_mul_f32 v[210:211], v[152:153], v[192:193]
	v_pk_mul_f32 v[212:213], v[150:151], v[186:187]
	v_pk_fma_f32 v[210:211], v[148:149], v[184:185], v[210:211] neg_lo:[0,0,1] neg_hi:[0,0,1]
	v_pk_fma_f32 v[212:213], v[146:147], v[182:183], v[212:213] neg_lo:[0,0,1] neg_hi:[0,0,1]
	v_pk_mul_f32 v[184:185], v[152:153], v[184:185]
	v_pk_mul_f32 v[182:183], v[150:151], v[182:183]
	v_pk_fma_f32 v[184:185], v[148:149], v[192:193], v[184:185]
	v_pk_fma_f32 v[182:183], v[146:147], v[186:187], v[182:183]
	v_mad_i64_i32 v[186:187], s[0:1], v167, s64, v[176:177]
	v_pk_add_f32 v[136:137], v[136:137], v[210:211]
	v_pk_add_f32 v[134:135], v[134:135], v[212:213]
	v_pk_add_f32 v[132:133], v[132:133], v[184:185]
	v_pk_add_f32 v[130:131], v[130:131], v[182:183]
	v_lshl_add_u64 v[186:187], v[186:187], 0, s[2:3]
	v_lshl_add_u64 v[186:187], v[186:187], 0, v[178:179]
	v_cvt_pk_bf16_f32 v192, v212, v213
	v_cvt_pk_bf16_f32 v193, v210, v211
	v_cvt_pk_bf16_f32 v182, v182, v183
	v_cvt_pk_bf16_f32 v183, v184, v185
	global_store_dwordx2 v[186:187], v[192:193], off
	global_store_dwordx2 v[186:187], v[182:183], off offset:128
	ds_read_b128 v[182:185], v157 offset:16
	v_mov_b64_e32 v[212:213], v[56:57]
	v_mov_b64_e32 v[210:211], v[54:55]
	s_waitcnt lgkmcnt(0)
	v_mov_b32_e32 v192, v183
	v_mov_b32_e32 v193, v184
	v_mov_b32_e32 v183, v185
	v_pk_add_f32 v[182:183], v[192:193], v[182:183]
	s_nop 0
	v_add_f32_e32 v157, v182, v183
	v_fmamk_f32 v157, v157, 0x3c000000, v230
	v_cmp_gt_f32_e32 vcc, s63, v157
	v_mul_f32_e32 v167, 0x4f800000, v157
	v_mov_b64_e32 v[184:185], v[52:53]
	v_cndmask_b32_e32 v157, v157, v167, vcc
	v_sqrt_f32_e32 v167, v157
	v_mov_b64_e32 v[182:183], v[50:51]
	v_add_u32_e32 v169, -1, v167
	v_fma_f32 v171, -v169, v167, v157
	v_cmp_ge_f32_e64 s[0:1], 0, v171
	v_add_u32_e32 v171, 1, v167
	v_cvt_f32_i32_e32 v193, v213
	v_cndmask_b32_e64 v169, v167, v169, s[0:1]
	v_fma_f32 v167, -v171, v167, v157
	v_cmp_lt_f32_e64 s[0:1], 0, v167
	v_cvt_f32_i32_e32 v192, v212
	v_cvt_f32_i32_e32 v211, v211
	v_cndmask_b32_e64 v167, v169, v171, s[0:1]
	v_mul_f32_e32 v169, 0x37800000, v167
	v_cndmask_b32_e32 v167, v167, v169, vcc
	v_cmp_class_f32_e32 vcc, v157, v231
	v_cvt_f32_i32_e32 v210, v210
	v_cvt_f32_i32_e32 v183, v183
	v_cndmask_b32_e32 v157, v167, v157, vcc
	v_div_scale_f32 v167, s[0:1], v157, v157, 1.0
	v_rcp_f32_e32 v169, v167
	v_cvt_f32_i32_e32 v182, v182
	v_cvt_f32_i32_e32 v185, v185
	v_cvt_f32_i32_e32 v184, v184
	v_fma_f32 v171, -v167, v169, 1.0
	v_fmac_f32_e32 v169, v171, v169
	v_div_scale_f32 v171, vcc, 1.0, v157, 1.0
	v_mul_f32_e32 v175, v171, v169
	v_fma_f32 v181, -v167, v175, v171
	v_fmac_f32_e32 v175, v181, v169
	v_fma_f32 v167, -v167, v175, v171
	v_div_fmas_f32 v167, v167, v169, v175
	v_div_fixup_f32 v157, v167, v157, 1.0
	v_mul_f32_e32 v180, v180, v157
	v_pk_mul_f32 v[210:211], v[180:181], v[210:211] op_sel_hi:[0,1]
	v_pk_mul_f32 v[192:193], v[180:181], v[192:193] op_sel_hi:[0,1]
	v_pk_mul_f32 v[184:185], v[180:181], v[184:185] op_sel_hi:[0,1]
	v_pk_mul_f32 v[180:181], v[180:181], v[182:183] op_sel_hi:[0,1]
	v_pk_mul_f32 v[192:193], v[128:129], v[192:193]
	v_pk_mul_f32 v[210:211], v[126:127], v[210:211]
	v_pk_mul_f32 v[180:181], v[122:123], v[180:181]
	v_pk_mul_f32 v[182:183], v[124:125], v[184:185]
	v_pk_mul_f32 v[212:213], v[150:151], v[180:181]
	v_pk_mul_f32 v[184:185], v[152:153], v[182:183]
	v_pk_mul_f32 v[152:153], v[152:153], v[192:193]
	v_pk_mul_f32 v[150:151], v[150:151], v[210:211]
	v_pk_fma_f32 v[212:213], v[146:147], v[210:211], v[212:213] neg_lo:[0,0,1] neg_hi:[0,0,1]
	v_pk_fma_f32 v[184:185], v[148:149], v[192:193], v[184:185] neg_lo:[0,0,1] neg_hi:[0,0,1]
	v_pk_fma_f32 v[146:147], v[146:147], v[180:181], v[150:151]
	v_pk_fma_f32 v[148:149], v[148:149], v[182:183], v[152:153]
	v_pk_add_f32 v[144:145], v[144:145], v[184:185]
	v_pk_add_f32 v[142:143], v[142:143], v[212:213]
	v_pk_add_f32 v[140:141], v[140:141], v[148:149]
	v_pk_add_f32 v[138:139], v[138:139], v[146:147]
	v_add_u32_e32 v157, 0x90, v190
	v_cvt_pk_bf16_f32 v150, v212, v213
	v_cvt_pk_bf16_f32 v151, v184, v185
	v_cvt_pk_bf16_f32 v146, v146, v147
	v_add_u32_e32 v167, s19, v157
	v_cvt_pk_bf16_f32 v147, v148, v149
	global_store_dwordx2 v[186:187], v[150:151], off offset:256
	global_store_dwordx2 v[186:187], v[146:147], off offset:384
	v_lshlrev_b32_e32 v146, 8, v167
	v_and_b32_e32 v202, 0x7ff00, v146
	v_lshl_add_u64 v[146:147], s[8:9], 0, v[202:203]
	v_lshl_add_u64 v[150:151], s[16:17], 0, v[202:203]
	v_lshl_add_u64 v[146:147], v[146:147], 0, v[172:173]
	v_lshl_add_u64 v[150:151], v[150:151], 0, v[172:173]
	s_waitcnt vmcnt(4)
	v_mov_b32_e32 v148, v246
	v_mov_b32_e32 v149, v247
	v_lshl_add_u64 v[246:247], v[146:147], 0, s[98:99]
	v_mov_b32_e32 v146, v244
	v_mov_b32_e32 v147, v245
	global_load_dwordx4 v[244:247], v[246:247], off
	v_lshl_add_u32 v157, v157, 5, s21
	v_mov_b32_e32 v152, v252
	v_mov_b32_e32 v153, v253
	v_lshl_add_u64 v[252:253], v[150:151], 0, s[98:99]
	v_mov_b32_e32 v150, v250
	v_mov_b32_e32 v151, v251
	global_load_dwordx4 v[250:253], v[252:253], off
	ds_read_b128 v[180:183], v157
	s_waitcnt lgkmcnt(0)
	v_mov_b32_e32 v184, v181
	v_mov_b32_e32 v185, v182
	v_mov_b32_e32 v181, v183
	v_pk_add_f32 v[180:181], v[184:185], v[180:181]
	v_mov_b64_e32 v[186:187], v[48:49]
	v_add_f32_e32 v169, v180, v181
	v_fmamk_f32 v169, v169, 0x3c000000, v230
	v_cmp_gt_f32_e32 vcc, s63, v169
	v_mul_f32_e32 v171, 0x4f800000, v169
	v_mov_b64_e32 v[184:185], v[46:47]
	v_cndmask_b32_e32 v169, v169, v171, vcc
	v_sqrt_f32_e32 v171, v169
	s_nop 0
	v_add_u32_e32 v175, -1, v171
	v_fma_f32 v180, -v175, v171, v169
	v_cmp_ge_f32_e64 s[0:1], 0, v180
	v_add_u32_e32 v180, 1, v171
	s_nop 0
	v_cndmask_b32_e64 v175, v171, v175, s[0:1]
	v_fma_f32 v171, -v180, v171, v169
	v_cmp_lt_f32_e64 s[0:1], 0, v171
	s_nop 1
	v_cndmask_b32_e64 v171, v175, v180, s[0:1]
	v_mul_f32_e32 v175, 0x37800000, v171
	v_cndmask_b32_e32 v171, v171, v175, vcc
	v_cmp_class_f32_e32 vcc, v169, v231
	s_nop 1
	v_cndmask_b32_e32 v169, v171, v169, vcc
	v_div_scale_f32 v171, s[0:1], v169, v169, 1.0
	v_rcp_f32_e32 v175, v171
	s_nop 0
	v_fma_f32 v180, -v171, v175, 1.0
	v_fmac_f32_e32 v175, v180, v175
	v_div_scale_f32 v180, vcc, 1.0, v169, 1.0
	v_mul_f32_e32 v181, v180, v175
	v_fma_f32 v182, -v171, v181, v180
	v_fmac_f32_e32 v181, v182, v175
	v_fma_f32 v171, -v171, v181, v180
	v_div_fmas_f32 v171, v171, v175, v181
	v_mov_b64_e32 v[182:183], v[44:45]
	v_mov_b64_e32 v[180:181], v[42:43]
	v_div_fixup_f32 v169, v171, v169, 1.0
	v_cvt_f32_i32_e32 v181, v181
	v_cvt_f32_i32_e32 v180, v180
	v_cvt_f32_i32_e32 v183, v183
	v_cvt_f32_i32_e32 v182, v182
	v_cvt_f32_i32_e32 v187, v187
	v_cvt_f32_i32_e32 v186, v186
	v_cvt_f32_i32_e32 v185, v185
	v_cvt_f32_i32_e32 v184, v184
	v_mul_f32_e32 v192, v174, v169
	v_pk_mul_f32 v[182:183], v[192:193], v[182:183] op_sel_hi:[0,1]
	v_pk_mul_f32 v[180:181], v[192:193], v[180:181] op_sel_hi:[0,1]
	v_pk_mul_f32 v[184:185], v[192:193], v[184:185] op_sel_hi:[0,1]
	v_pk_mul_f32 v[186:187], v[192:193], v[186:187] op_sel_hi:[0,1]
	v_pk_mul_f32 v[180:181], v[122:123], v[180:181]
	v_pk_mul_f32 v[182:183], v[124:125], v[182:183]
	v_pk_mul_f32 v[186:187], v[128:129], v[186:187]
	v_pk_mul_f32 v[184:185], v[126:127], v[184:185]
	v_pk_mul_f32 v[192:193], v[152:153], v[182:183]
	v_pk_mul_f32 v[210:211], v[150:151], v[180:181]
	v_pk_fma_f32 v[192:193], v[148:149], v[186:187], v[192:193] neg_lo:[0,0,1] neg_hi:[0,0,1]
	v_pk_fma_f32 v[210:211], v[146:147], v[184:185], v[210:211] neg_lo:[0,0,1] neg_hi:[0,0,1]
	v_pk_mul_f32 v[186:187], v[152:153], v[186:187]
	v_pk_mul_f32 v[184:185], v[150:151], v[184:185]
	v_pk_fma_f32 v[182:183], v[148:149], v[182:183], v[186:187]
	v_pk_fma_f32 v[180:181], v[146:147], v[180:181], v[184:185]
	v_mad_i64_i32 v[184:185], s[0:1], v167, s64, v[176:177]
	v_pk_add_f32 v[136:137], v[136:137], v[192:193]
	v_pk_add_f32 v[134:135], v[134:135], v[210:211]
	v_pk_add_f32 v[132:133], v[132:133], v[182:183]
	v_pk_add_f32 v[130:131], v[130:131], v[180:181]
	v_lshl_add_u64 v[184:185], v[184:185], 0, s[2:3]
	v_lshl_add_u64 v[212:213], v[184:185], 0, v[178:179]
	v_cvt_pk_bf16_f32 v184, v210, v211
	v_cvt_pk_bf16_f32 v185, v192, v193
	v_cvt_pk_bf16_f32 v180, v180, v181
	v_cvt_pk_bf16_f32 v181, v182, v183
	global_store_dwordx2 v[212:213], v[184:185], off
	global_store_dwordx2 v[212:213], v[180:181], off offset:128
	ds_read_b128 v[180:183], v157 offset:16
	s_waitcnt lgkmcnt(0)
	v_mov_b32_e32 v184, v181
	v_mov_b32_e32 v185, v182
	v_mov_b32_e32 v181, v183
	v_pk_add_f32 v[180:181], v[184:185], v[180:181]
	v_mov_b64_e32 v[186:187], v[36:37]
	v_add_f32_e32 v157, v180, v181
	v_fmamk_f32 v157, v157, 0x3c000000, v230
	v_cmp_gt_f32_e32 vcc, s63, v157
	v_mul_f32_e32 v167, 0x4f800000, v157
	v_mov_b64_e32 v[184:185], v[34:35]
	v_cndmask_b32_e32 v157, v157, v167, vcc
	v_sqrt_f32_e32 v167, v157
	s_nop 0
	v_add_u32_e32 v169, -1, v167
	v_fma_f32 v171, -v169, v167, v157
	v_cmp_ge_f32_e64 s[0:1], 0, v171
	v_add_u32_e32 v171, 1, v167
	s_nop 0
	v_cndmask_b32_e64 v169, v167, v169, s[0:1]
	v_fma_f32 v167, -v171, v167, v157
	v_cmp_lt_f32_e64 s[0:1], 0, v167
	s_nop 1
	v_cndmask_b32_e64 v167, v169, v171, s[0:1]
	v_mul_f32_e32 v169, 0x37800000, v167
	v_cndmask_b32_e32 v167, v167, v169, vcc
	v_cmp_class_f32_e32 vcc, v157, v231
	s_nop 1
	v_cndmask_b32_e32 v157, v167, v157, vcc
	v_div_scale_f32 v167, s[0:1], v157, v157, 1.0
	v_rcp_f32_e32 v169, v167
	s_nop 0
	v_fma_f32 v171, -v167, v169, 1.0
	v_fmac_f32_e32 v169, v171, v169
	v_div_scale_f32 v171, vcc, 1.0, v157, 1.0
	v_mul_f32_e32 v175, v171, v169
	v_fma_f32 v180, -v167, v175, v171
	v_fmac_f32_e32 v175, v180, v169
	v_mov_b64_e32 v[182:183], v[40:41]
	v_mov_b64_e32 v[180:181], v[38:39]
	v_fma_f32 v167, -v167, v175, v171
	v_cvt_f32_i32_e32 v183, v183
	v_cvt_f32_i32_e32 v182, v182
	v_cvt_f32_i32_e32 v181, v181
	v_cvt_f32_i32_e32 v180, v180
	v_cvt_f32_i32_e32 v185, v185
	v_cvt_f32_i32_e32 v184, v184
	v_cvt_f32_i32_e32 v187, v187
	v_cvt_f32_i32_e32 v186, v186
	v_div_fmas_f32 v167, v167, v169, v175
	v_div_fixup_f32 v157, v167, v157, 1.0
	v_mul_f32_e32 v174, v174, v157
	v_pk_mul_f32 v[180:181], v[174:175], v[180:181] op_sel_hi:[0,1]
	v_pk_mul_f32 v[182:183], v[174:175], v[182:183] op_sel_hi:[0,1]
	v_pk_mul_f32 v[186:187], v[174:175], v[186:187] op_sel_hi:[0,1]
	v_pk_mul_f32 v[174:175], v[174:175], v[184:185] op_sel_hi:[0,1]
	v_pk_mul_f32 v[182:183], v[128:129], v[182:183]
	v_pk_mul_f32 v[180:181], v[126:127], v[180:181]
	v_pk_mul_f32 v[174:175], v[122:123], v[174:175]
	v_pk_mul_f32 v[184:185], v[124:125], v[186:187]
	v_pk_mul_f32 v[192:193], v[150:151], v[174:175]
	v_pk_mul_f32 v[186:187], v[152:153], v[184:185]
	v_pk_mul_f32 v[152:153], v[152:153], v[182:183]
	v_pk_mul_f32 v[150:151], v[150:151], v[180:181]
	v_pk_fma_f32 v[192:193], v[146:147], v[180:181], v[192:193] neg_lo:[0,0,1] neg_hi:[0,0,1]
	v_pk_fma_f32 v[186:187], v[148:149], v[182:183], v[186:187] neg_lo:[0,0,1] neg_hi:[0,0,1]
	v_pk_fma_f32 v[150:151], v[146:147], v[174:175], v[150:151]
	v_pk_fma_f32 v[152:153], v[148:149], v[184:185], v[152:153]
	v_pk_add_f32 v[144:145], v[144:145], v[186:187]
	v_pk_add_f32 v[142:143], v[142:143], v[192:193]
	v_pk_add_f32 v[148:149], v[140:141], v[152:153]
	v_pk_add_f32 v[146:147], v[138:139], v[150:151]
	v_add_u32_e32 v157, 0xa0, v190
	v_cvt_pk_bf16_f32 v138, v192, v193
	v_cvt_pk_bf16_f32 v139, v186, v187
	v_add_u32_e32 v167, s19, v157
	v_cvt_pk_bf16_f32 v140, v150, v151
	v_cvt_pk_bf16_f32 v141, v152, v153
	global_store_dwordx2 v[212:213], v[138:139], off offset:256
	global_store_dwordx2 v[212:213], v[140:141], off offset:384
	v_lshlrev_b32_e32 v138, 8, v167
	v_and_b32_e32 v202, 0x7ff00, v138
	v_lshl_add_u64 v[138:139], s[8:9], 0, v[202:203]
	v_lshl_add_u64 v[150:151], s[16:17], 0, v[202:203]
	v_lshl_add_u64 v[138:139], v[138:139], 0, v[172:173]
	v_lshl_add_u64 v[150:151], v[150:151], 0, v[172:173]
	s_waitcnt vmcnt(4)
	v_mov_b32_e32 v140, v246
	v_mov_b32_e32 v141, v247
	v_lshl_add_u64 v[246:247], v[138:139], 0, s[98:99]
	v_mov_b32_e32 v138, v244
	v_mov_b32_e32 v139, v245
	global_load_dwordx4 v[244:247], v[246:247], off
	v_lshl_add_u32 v157, v157, 5, s21
	v_mov_b32_e32 v152, v252
	v_mov_b32_e32 v153, v253
	v_lshl_add_u64 v[252:253], v[150:151], 0, s[98:99]
	v_mov_b32_e32 v150, v250
	v_mov_b32_e32 v151, v251
	global_load_dwordx4 v[250:253], v[252:253], off
	ds_read_b128 v[180:183], v157
	v_mov_b64_e32 v[186:187], v[32:33]
	v_mov_b64_e32 v[184:185], v[30:31]
	s_waitcnt lgkmcnt(0)
	v_mov_b32_e32 v174, v181
	v_mov_b32_e32 v175, v182
	v_mov_b32_e32 v181, v183
	v_pk_add_f32 v[174:175], v[174:175], v[180:181]
	s_nop 0
	v_add_f32_e32 v169, v174, v175
	v_fmamk_f32 v169, v169, 0x3c000000, v230
	v_cmp_gt_f32_e32 vcc, s63, v169
	v_mul_f32_e32 v171, 0x4f800000, v169
	s_nop 0
	v_cndmask_b32_e32 v169, v169, v171, vcc
	v_sqrt_f32_e32 v171, v169
	s_nop 0
	v_add_u32_e32 v174, -1, v171
	v_fma_f32 v175, -v174, v171, v169
	v_cmp_ge_f32_e64 s[0:1], 0, v175
	v_add_u32_e32 v175, 1, v171
	s_nop 0
	v_cndmask_b32_e64 v174, v171, v174, s[0:1]
	v_fma_f32 v171, -v175, v171, v169
	v_cmp_lt_f32_e64 s[0:1], 0, v171
	s_nop 1
	v_cndmask_b32_e64 v171, v174, v175, s[0:1]
	v_mul_f32_e32 v174, 0x37800000, v171
	v_cndmask_b32_e32 v171, v171, v174, vcc
	v_cmp_class_f32_e32 vcc, v169, v231
	s_nop 1
	v_cndmask_b32_e32 v169, v171, v169, vcc
	v_div_scale_f32 v171, s[0:1], v169, v169, 1.0
	v_rcp_f32_e32 v174, v171
	s_nop 0
	v_fma_f32 v175, -v171, v174, 1.0
	v_fmac_f32_e32 v174, v175, v174
	v_div_scale_f32 v175, vcc, 1.0, v169, 1.0
	v_mul_f32_e32 v180, v175, v174
	v_fma_f32 v181, -v171, v180, v175
	v_fmac_f32_e32 v180, v181, v174
	v_fma_f32 v171, -v171, v180, v175
	v_div_fmas_f32 v171, v171, v174, v180
	v_mov_b64_e32 v[182:183], v[28:29]
	v_mov_b64_e32 v[180:181], v[26:27]
	v_div_fixup_f32 v169, v171, v169, 1.0
	v_cvt_f32_i32_e32 v181, v181
	v_cvt_f32_i32_e32 v180, v180
	v_cvt_f32_i32_e32 v183, v183
	v_cvt_f32_i32_e32 v182, v182
	v_cvt_f32_i32_e32 v175, v187
	v_cvt_f32_i32_e32 v174, v186
	v_cvt_f32_i32_e32 v185, v185
	v_cvt_f32_i32_e32 v184, v184
	v_mul_f32_e32 v186, v170, v169
	v_pk_mul_f32 v[182:183], v[186:187], v[182:183] op_sel_hi:[0,1]
	v_pk_mul_f32 v[180:181], v[186:187], v[180:181] op_sel_hi:[0,1]
	v_pk_mul_f32 v[184:185], v[186:187], v[184:185] op_sel_hi:[0,1]
	v_pk_mul_f32 v[174:175], v[186:187], v[174:175] op_sel_hi:[0,1]
	v_pk_mul_f32 v[180:181], v[122:123], v[180:181]
	v_pk_mul_f32 v[182:183], v[124:125], v[182:183]
	v_pk_mul_f32 v[174:175], v[128:129], v[174:175]
	v_pk_mul_f32 v[184:185], v[126:127], v[184:185]
	v_pk_mul_f32 v[186:187], v[152:153], v[182:183]
	v_pk_mul_f32 v[192:193], v[150:151], v[180:181]
	v_pk_fma_f32 v[186:187], v[140:141], v[174:175], v[186:187] neg_lo:[0,0,1] neg_hi:[0,0,1]
	v_pk_fma_f32 v[192:193], v[138:139], v[184:185], v[192:193] neg_lo:[0,0,1] neg_hi:[0,0,1]
	v_pk_mul_f32 v[174:175], v[152:153], v[174:175]
	v_pk_mul_f32 v[184:185], v[150:151], v[184:185]
	v_pk_fma_f32 v[174:175], v[140:141], v[182:183], v[174:175]
	v_pk_fma_f32 v[180:181], v[138:139], v[180:181], v[184:185]
	v_mad_i64_i32 v[182:183], s[0:1], v167, s64, v[176:177]
	v_pk_add_f32 v[136:137], v[136:137], v[186:187]
	v_pk_add_f32 v[134:135], v[134:135], v[192:193]
	v_pk_add_f32 v[132:133], v[132:133], v[174:175]
	v_pk_add_f32 v[130:131], v[130:131], v[180:181]
	v_lshl_add_u64 v[182:183], v[182:183], 0, s[2:3]
	v_lshl_add_u64 v[210:211], v[182:183], 0, v[178:179]
	v_cvt_pk_bf16_f32 v182, v192, v193
	v_cvt_pk_bf16_f32 v183, v186, v187
	v_cvt_pk_bf16_f32 v180, v180, v181
	v_cvt_pk_bf16_f32 v181, v174, v175
	global_store_dwordx2 v[210:211], v[182:183], off
	global_store_dwordx2 v[210:211], v[180:181], off offset:128
	ds_read_b128 v[180:183], v157 offset:16
	v_mov_b64_e32 v[186:187], v[20:21]
	v_mov_b64_e32 v[184:185], v[18:19]
	s_waitcnt lgkmcnt(0)
	v_mov_b32_e32 v174, v181
	v_mov_b32_e32 v175, v182
	v_mov_b32_e32 v181, v183
	v_pk_add_f32 v[174:175], v[174:175], v[180:181]
	v_mov_b64_e32 v[182:183], v[24:25]
	v_add_f32_e32 v157, v174, v175
	v_fmamk_f32 v157, v157, 0x3c000000, v230
	v_cmp_gt_f32_e32 vcc, s63, v157
	v_mul_f32_e32 v167, 0x4f800000, v157
	v_mov_b64_e32 v[180:181], v[22:23]
	v_cndmask_b32_e32 v157, v157, v167, vcc
	v_sqrt_f32_e32 v167, v157
	s_nop 0
	v_cvt_f32_i32_e32 v181, v181
	v_add_u32_e32 v169, -1, v167
	v_fma_f32 v171, -v169, v167, v157
	v_cmp_ge_f32_e64 s[0:1], 0, v171
	v_add_u32_e32 v171, 1, v167
	v_cvt_f32_i32_e32 v180, v180
	v_cndmask_b32_e64 v169, v167, v169, s[0:1]
	v_fma_f32 v167, -v171, v167, v157
	v_cmp_lt_f32_e64 s[0:1], 0, v167
	s_nop 1
	v_cndmask_b32_e64 v167, v169, v171, s[0:1]
	v_mul_f32_e32 v169, 0x37800000, v167
	v_cndmask_b32_e32 v167, v167, v169, vcc
	v_cmp_class_f32_e32 vcc, v157, v231
	s_nop 1
	v_cndmask_b32_e32 v157, v167, v157, vcc
	v_div_scale_f32 v167, s[0:1], v157, v157, 1.0
	v_rcp_f32_e32 v169, v167
	s_nop 0
	v_fma_f32 v171, -v167, v169, 1.0
	v_fmac_f32_e32 v169, v171, v169
	v_div_scale_f32 v171, vcc, 1.0, v157, 1.0
	v_mul_f32_e32 v174, v171, v169
	v_fma_f32 v175, -v167, v174, v171
	v_fmac_f32_e32 v174, v175, v169
	v_fma_f32 v167, -v167, v174, v171
	v_div_fmas_f32 v167, v167, v169, v174
	v_cvt_f32_i32_e32 v175, v183
	v_cvt_f32_i32_e32 v174, v182
	v_cvt_f32_i32_e32 v183, v185
	v_cvt_f32_i32_e32 v182, v184
	v_cvt_f32_i32_e32 v185, v187
	v_cvt_f32_i32_e32 v184, v186
	v_div_fixup_f32 v157, v167, v157, 1.0
	v_mul_f32_e32 v170, v170, v157
	v_pk_mul_f32 v[180:181], v[170:171], v[180:181] op_sel_hi:[0,1]
	v_pk_mul_f32 v[174:175], v[170:171], v[174:175] op_sel_hi:[0,1]
	v_pk_mul_f32 v[184:185], v[170:171], v[184:185] op_sel_hi:[0,1]
	v_pk_mul_f32 v[170:171], v[170:171], v[182:183] op_sel_hi:[0,1]
	v_pk_mul_f32 v[174:175], v[128:129], v[174:175]
	v_pk_mul_f32 v[180:181], v[126:127], v[180:181]
	v_pk_mul_f32 v[170:171], v[122:123], v[170:171]
	v_pk_mul_f32 v[182:183], v[124:125], v[184:185]
	v_pk_mul_f32 v[186:187], v[150:151], v[170:171]
	v_pk_mul_f32 v[184:185], v[152:153], v[182:183]
	v_pk_mul_f32 v[152:153], v[152:153], v[174:175]
	v_pk_mul_f32 v[150:151], v[150:151], v[180:181]
	v_pk_fma_f32 v[186:187], v[138:139], v[180:181], v[186:187] neg_lo:[0,0,1] neg_hi:[0,0,1]
	v_pk_fma_f32 v[184:185], v[140:141], v[174:175], v[184:185] neg_lo:[0,0,1] neg_hi:[0,0,1]
	v_pk_fma_f32 v[150:151], v[138:139], v[170:171], v[150:151]
	v_pk_fma_f32 v[152:153], v[140:141], v[182:183], v[152:153]
	v_pk_add_f32 v[140:141], v[144:145], v[184:185]
	v_pk_add_f32 v[138:139], v[142:143], v[186:187]
	v_pk_add_f32 v[144:145], v[148:149], v[152:153]
	v_pk_add_f32 v[142:143], v[146:147], v[150:151]
	v_add_u32_e32 v157, 0xb0, v190
	v_cvt_pk_bf16_f32 v146, v186, v187
	v_cvt_pk_bf16_f32 v147, v184, v185
	v_add_u32_e32 v167, s19, v157
	v_cvt_pk_bf16_f32 v148, v150, v151
	v_cvt_pk_bf16_f32 v149, v152, v153
	global_store_dwordx2 v[210:211], v[146:147], off offset:256
	global_store_dwordx2 v[210:211], v[148:149], off offset:384
	v_lshlrev_b32_e32 v146, 8, v167
	v_and_b32_e32 v202, 0x7ff00, v146
	v_lshl_add_u64 v[146:147], s[8:9], 0, v[202:203]
	v_lshl_add_u64 v[150:151], s[16:17], 0, v[202:203]
	v_lshl_add_u64 v[146:147], v[146:147], 0, v[172:173]
	v_lshl_add_u64 v[150:151], v[150:151], 0, v[172:173]
	s_waitcnt vmcnt(4)
	v_mov_b32_e32 v146, v244
	v_mov_b32_e32 v147, v245
	v_mov_b32_e32 v148, v246
	v_mov_b32_e32 v149, v247
	v_lshl_add_u32 v157, v157, 5, s21
	v_mov_b32_e32 v150, v250
	v_mov_b32_e32 v151, v251
	v_mov_b32_e32 v152, v252
	v_mov_b32_e32 v153, v253
	ds_read_b128 v[170:173], v157
	v_mov_b64_e32 v[182:183], v[16:17]
	v_mov_b64_e32 v[180:181], v[14:15]
	s_waitcnt lgkmcnt(0)
	v_mov_b32_e32 v174, v171
	v_mov_b32_e32 v175, v172
	v_mov_b32_e32 v171, v173
	v_pk_add_f32 v[170:171], v[174:175], v[170:171]
	s_nop 0
	v_add_f32_e32 v169, v170, v171
	v_fmamk_f32 v169, v169, 0x3c000000, v230
	v_cmp_gt_f32_e32 vcc, s63, v169
	v_mul_f32_e32 v170, 0x4f800000, v169
	s_nop 0
	v_cndmask_b32_e32 v169, v169, v170, vcc
	v_sqrt_f32_e32 v170, v169
	s_nop 0
	v_add_u32_e32 v171, -1, v170
	v_fma_f32 v172, -v171, v170, v169
	v_cmp_ge_f32_e64 s[0:1], 0, v172
	v_add_u32_e32 v172, 1, v170
	s_nop 0
	v_cndmask_b32_e64 v171, v170, v171, s[0:1]
	v_fma_f32 v170, -v172, v170, v169
	v_cmp_lt_f32_e64 s[0:1], 0, v170
	s_nop 1
	v_cndmask_b32_e64 v170, v171, v172, s[0:1]
	v_mul_f32_e32 v171, 0x37800000, v170
	v_cndmask_b32_e32 v170, v170, v171, vcc
	v_cmp_class_f32_e32 vcc, v169, v231
	s_nop 1
	v_cndmask_b32_e32 v169, v170, v169, vcc
	v_div_scale_f32 v170, s[0:1], v169, v169, 1.0
	v_rcp_f32_e32 v171, v170
	s_nop 0
	v_fma_f32 v172, -v170, v171, 1.0
	v_fmac_f32_e32 v171, v172, v171
	v_div_scale_f32 v172, vcc, 1.0, v169, 1.0
	v_mul_f32_e32 v173, v172, v171
	v_fma_f32 v174, -v170, v173, v172
	v_fmac_f32_e32 v173, v174, v171
	v_fma_f32 v170, -v170, v173, v172
	v_div_fmas_f32 v170, v170, v171, v173
	v_div_fixup_f32 v169, v170, v169, 1.0
	v_mov_b64_e32 v[172:173], v[12:13]
	v_mov_b64_e32 v[170:171], v[10:11]
	s_nop 0
	v_cvt_f32_i32_e32 v171, v171
	v_cvt_f32_i32_e32 v170, v170
	v_cvt_f32_i32_e32 v173, v173
	v_cvt_f32_i32_e32 v172, v172
	v_cvt_f32_i32_e32 v175, v183
	v_cvt_f32_i32_e32 v174, v182
	v_cvt_f32_i32_e32 v181, v181
	v_cvt_f32_i32_e32 v180, v180
	v_mul_f32_e32 v182, v166, v169
	v_pk_mul_f32 v[172:173], v[182:183], v[172:173] op_sel_hi:[0,1]
	v_pk_mul_f32 v[170:171], v[182:183], v[170:171] op_sel_hi:[0,1]
	v_pk_mul_f32 v[180:181], v[182:183], v[180:181] op_sel_hi:[0,1]
	v_pk_mul_f32 v[174:175], v[182:183], v[174:175] op_sel_hi:[0,1]
	v_pk_mul_f32 v[170:171], v[122:123], v[170:171]
	v_pk_mul_f32 v[172:173], v[124:125], v[172:173]
	v_pk_mul_f32 v[174:175], v[128:129], v[174:175]
	v_pk_mul_f32 v[180:181], v[126:127], v[180:181]
	v_pk_mul_f32 v[182:183], v[152:153], v[172:173]
	v_pk_mul_f32 v[184:185], v[150:151], v[170:171]
	v_pk_fma_f32 v[182:183], v[148:149], v[174:175], v[182:183] neg_lo:[0,0,1] neg_hi:[0,0,1]
	v_pk_fma_f32 v[184:185], v[146:147], v[180:181], v[184:185] neg_lo:[0,0,1] neg_hi:[0,0,1]
	v_pk_mul_f32 v[174:175], v[152:153], v[174:175]
	v_pk_mul_f32 v[180:181], v[150:151], v[180:181]
	v_pk_fma_f32 v[172:173], v[148:149], v[172:173], v[174:175]
	v_pk_fma_f32 v[170:171], v[146:147], v[170:171], v[180:181]
	v_mad_i64_i32 v[174:175], s[0:1], v167, s64, v[176:177]
	v_pk_add_f32 v[136:137], v[136:137], v[182:183]
	v_pk_add_f32 v[134:135], v[134:135], v[184:185]
	v_pk_add_f32 v[132:133], v[132:133], v[172:173]
	v_pk_add_f32 v[130:131], v[130:131], v[170:171]
	v_lshl_add_u64 v[174:175], v[174:175], 0, s[2:3]
	v_lshl_add_u64 v[178:179], v[174:175], 0, v[178:179]
	v_cvt_pk_bf16_f32 v174, v184, v185
	v_cvt_pk_bf16_f32 v175, v182, v183
	v_cvt_pk_bf16_f32 v170, v170, v171
	v_cvt_pk_bf16_f32 v171, v172, v173
	global_store_dwordx2 v[178:179], v[174:175], off
	global_store_dwordx2 v[178:179], v[170:171], off offset:128
	ds_read_b128 v[170:173], v157 offset:16
	s_waitcnt lgkmcnt(0)
	v_mov_b32_e32 v174, v171
	v_mov_b32_e32 v175, v172
	v_mov_b32_e32 v171, v173
	v_pk_add_f32 v[170:171], v[174:175], v[170:171]
	v_mov_b64_e32 v[176:177], v[4:5]
	v_add_f32_e32 v157, v170, v171
	v_fmamk_f32 v157, v157, 0x3c000000, v230
	v_cmp_gt_f32_e32 vcc, s63, v157
	v_mul_f32_e32 v167, 0x4f800000, v157
	v_mov_b64_e32 v[174:175], v[2:3]
	v_cndmask_b32_e32 v157, v157, v167, vcc
	v_sqrt_f32_e32 v167, v157
	s_nop 0
	v_add_u32_e32 v169, -1, v167
	v_fma_f32 v170, -v169, v167, v157
	v_cmp_ge_f32_e64 s[0:1], 0, v170
	v_add_u32_e32 v170, 1, v167
	s_nop 0
	v_cndmask_b32_e64 v169, v167, v169, s[0:1]
	v_fma_f32 v167, -v170, v167, v157
	v_cmp_lt_f32_e64 s[0:1], 0, v167
	s_nop 1
	v_cndmask_b32_e64 v167, v169, v170, s[0:1]
	v_mul_f32_e32 v169, 0x37800000, v167
	v_cndmask_b32_e32 v167, v167, v169, vcc
	v_cmp_class_f32_e32 vcc, v157, v231
	s_nop 1
	v_cndmask_b32_e32 v157, v167, v157, vcc
	v_div_scale_f32 v167, s[0:1], v157, v157, 1.0
	v_rcp_f32_e32 v169, v167
	s_nop 0
	v_fma_f32 v170, -v167, v169, 1.0
	v_fmac_f32_e32 v169, v170, v169
	v_div_scale_f32 v170, vcc, 1.0, v157, 1.0
	v_mul_f32_e32 v171, v170, v169
	v_fma_f32 v172, -v167, v171, v170
	v_fmac_f32_e32 v171, v172, v169
	v_fma_f32 v167, -v167, v171, v170
	v_div_fmas_f32 v167, v167, v169, v171
	v_mov_b64_e32 v[172:173], v[8:9]
	v_mov_b64_e32 v[170:171], v[6:7]
	v_div_fixup_f32 v157, v167, v157, 1.0
	v_cvt_f32_i32_e32 v173, v173
	v_cvt_f32_i32_e32 v172, v172
	v_cvt_f32_i32_e32 v171, v171
	v_cvt_f32_i32_e32 v170, v170
	v_mul_f32_e32 v166, v166, v157
	v_pk_mul_f32 v[172:173], v[166:167], v[172:173] op_sel_hi:[0,1]
	v_pk_mul_f32 v[128:129], v[128:129], v[172:173]
	v_pk_mul_f32 v[170:171], v[166:167], v[170:171] op_sel_hi:[0,1]
	v_pk_mul_f32 v[126:127], v[126:127], v[170:171]
	v_cvt_f32_i32_e32 v171, v175
	v_cvt_f32_i32_e32 v170, v174
	v_cvt_f32_i32_e32 v173, v177
	v_cvt_f32_i32_e32 v172, v176
	v_pk_mul_f32 v[172:173], v[166:167], v[172:173] op_sel_hi:[0,1]
	v_pk_mul_f32 v[166:167], v[166:167], v[170:171] op_sel_hi:[0,1]
	v_pk_mul_f32 v[122:123], v[122:123], v[166:167]
	v_pk_mul_f32 v[124:125], v[124:125], v[172:173]
	v_pk_mul_f32 v[170:171], v[150:151], v[122:123]
	v_pk_mul_f32 v[166:167], v[152:153], v[124:125]
	v_pk_fma_f32 v[170:171], v[146:147], v[126:127], v[170:171] neg_lo:[0,0,1] neg_hi:[0,0,1]
	v_pk_fma_f32 v[166:167], v[148:149], v[128:129], v[166:167] neg_lo:[0,0,1] neg_hi:[0,0,1]
	v_pk_mul_f32 v[128:129], v[152:153], v[128:129]
	v_pk_mul_f32 v[126:127], v[150:151], v[126:127]
	v_pk_fma_f32 v[148:149], v[148:149], v[124:125], v[128:129]
	v_pk_fma_f32 v[146:147], v[146:147], v[122:123], v[126:127]
	v_pk_add_f32 v[128:129], v[140:141], v[166:167]
	v_pk_add_f32 v[126:127], v[138:139], v[170:171]
	v_pk_add_f32 v[124:125], v[144:145], v[148:149]
	v_pk_add_f32 v[122:123], v[142:143], v[146:147]
	s_nop 0
	v_cvt_pk_bf16_f32 v138, v170, v171
	v_cvt_pk_bf16_f32 v139, v166, v167
	v_cvt_pk_bf16_f32 v140, v146, v147
	v_cvt_pk_bf16_f32 v141, v148, v149
	global_store_dwordx2 v[178:179], v[138:139], off offset:256
	global_store_dwordx2 v[178:179], v[140:141], off offset:384
	s_cbranch_scc1 .LBB0_2583
	v_xor_b32_e32 v138, 1, v234
	v_cmp_lt_i32_e32 vcc, v138, v155
	v_xor_b32_e32 v139, 2, v234
	s_nop 0
	v_cndmask_b32_e32 v138, v234, v138, vcc
	v_lshlrev_b32_e32 v138, 2, v138
	s_nop 1
	v_mov_b32_dpp v143, v134 quad_perm:[1,0,3,2] row_mask:0xf bank_mask:0xf
	v_cmp_lt_i32_e32 vcc, v139, v155
	s_waitcnt lgkmcnt(0)
	v_add_f32_e32 v134, v134, v143
	v_cndmask_b32_e32 v139, v234, v139, vcc
	v_lshlrev_b32_e32 v140, 2, v139
	s_nop 1
	v_mov_b32_dpp v143, v134 quad_perm:[2,3,0,1] row_mask:0xf bank_mask:0xf
	v_xor_b32_e32 v139, 4, v234
	v_cmp_lt_i32_e32 vcc, v139, v155
	v_add_f32_e32 v134, v134, v143
	v_cndmask_b32_e32 v139, v234, v139, vcc
	v_lshlrev_b32_e32 v141, 2, v139
	s_nop 1
	v_mov_b32_dpp v143, v134 row_half_mirror row_mask:0xf bank_mask:0xf
	v_xor_b32_e32 v139, 8, v234
	v_cmp_lt_i32_e32 vcc, v139, v155
	v_add_f32_e32 v134, v134, v143
	v_cndmask_b32_e32 v139, v234, v139, vcc
	v_lshlrev_b32_e32 v142, 2, v139
	s_nop 1
	v_mov_b32_dpp v143, v134 row_mirror row_mask:0xf bank_mask:0xf
	v_cmp_eq_u32_e32 vcc, 0, v189
	v_lshl_add_u32 v139, v168, 2, s60
	s_and_saveexec_b64 s[0:1], vcc
	s_cbranch_execz .LBB0_2550
	v_add_f32_e32 v134, v134, v143
	ds_write_b32 v139, v134
